# plus: all P2 stores (projection epilogue outputs + converted weights) non-temporal
# baseline (speedup 1.0000x reference)
; __global__ void __launch_bounds__(NWAVES * 64, 2) mk_fwd(Args args) {
;     ...
; #pragma unroll 1
;               for (;;) { int g0 = 0; if (lane == 0) g0 = I_IN + (int)__hip_atomic_fetch_add(ctl + CW_Q4, 8u, __ATOMIC_RELAXED, __HIP_MEMORY_SCOPE_AGENT);
;                   g0 = __builtin_amdgcn_readfirstlane(g0); if (g0 >= NIT) break;
; #pragma unroll 1
;                   for (int k = 0; k < 8; k += 2) wtile_copy_pair(mixer_tile_addr(Xm, g0 + k), mixer_tile_addr(Xm, g0 + k + 1), lane); } }
.LBB0_220:
	v_lshl_add_u64 v[66:67], v[140:141], 0, v[134:135]
	v_lshlrev_b32_e32 v134, 12, v133
	v_lshl_add_u64 v[74:75], v[66:67], 0, v[134:135]
	s_waitcnt vmcnt(22)
	v_cvt_pk_bf16_f32 v66, v2, v6
	s_waitcnt vmcnt(20)
	v_cvt_pk_bf16_f32 v67, v10, v14
	s_waitcnt vmcnt(18)
	v_cvt_pk_bf16_f32 v68, v18, v22
	s_waitcnt vmcnt(16)
	v_cvt_pk_bf16_f32 v69, v34, v42
	v_add_co_u32_e32 v2, vcc, s41, v74
	s_waitcnt vmcnt(14)
	v_cvt_pk_bf16_f32 v70, v26, v30
	s_waitcnt vmcnt(12)
	v_cvt_pk_bf16_f32 v71, v38, v46
	s_waitcnt vmcnt(10)
	v_cvt_pk_bf16_f32 v72, v50, v54
	s_waitcnt vmcnt(8)
	v_cvt_pk_bf16_f32 v73, v58, v62
	global_store_dwordx4 v[74:75], v[66:69], off nt
	global_store_dwordx4 v[74:75], v[70:73], off offset:16 nt
	s_add_i32 s46, s46, 2
	v_cvt_pk_bf16_f32 v66, v3, v7
	v_addc_co_u32_e32 v3, vcc, 0, v75, vcc
	v_add_co_u32_e32 v6, vcc, s42, v74
	v_cvt_pk_bf16_f32 v67, v11, v15
	v_cvt_pk_bf16_f32 v68, v19, v23
	v_cvt_pk_bf16_f32 v69, v35, v43
	v_addc_co_u32_e32 v7, vcc, 0, v75, vcc
	v_cvt_pk_bf16_f32 v70, v27, v31
	v_cvt_pk_bf16_f32 v71, v39, v47
	v_cvt_pk_bf16_f32 v72, v51, v55
	v_cvt_pk_bf16_f32 v73, v59, v63
	global_store_dwordx4 v[6:7], v[66:69], off offset:-4096 nt
	global_store_dwordx4 v[2:3], v[70:73], off offset:16 nt
	v_add_co_u32_e32 v10, vcc, 0x3000, v74
	v_cvt_pk_bf16_f32 v66, v4, v8
	v_cvt_pk_bf16_f32 v67, v12, v16
	v_cvt_pk_bf16_f32 v68, v20, v24
	v_cvt_pk_bf16_f32 v69, v36, v44
	s_add_i32 s44, s44, 4
	s_addk_i32 s45, 0x80
	v_cvt_pk_bf16_f32 v70, v28, v32
	v_cvt_pk_bf16_f32 v71, v40, v48
	v_cvt_pk_bf16_f32 v72, v52, v56
	v_cvt_pk_bf16_f32 v73, v60, v64
	global_store_dwordx4 v[6:7], v[66:69], off nt
	global_store_dwordx4 v[6:7], v[70:73], off offset:16 nt
	v_cvt_pk_bf16_f32 v2, v5, v9
	v_cvt_pk_bf16_f32 v3, v13, v17
	v_cvt_pk_bf16_f32 v4, v21, v25
	v_cvt_pk_bf16_f32 v5, v37, v45
	v_cvt_pk_bf16_f32 v6, v29, v33
	v_cvt_pk_bf16_f32 v7, v41, v49
	v_cvt_pk_bf16_f32 v8, v53, v57
	v_cvt_pk_bf16_f32 v9, v61, v65
	v_addc_co_u32_e32 v11, vcc, 0, v75, vcc
	s_cmp_gt_u32 s46, 5
	global_store_dwordx4 v[10:11], v[2:5], off nt
	global_store_dwordx4 v[10:11], v[6:9], off offset:16 nt
	s_cbranch_scc1 .LBB0_212

.LBB0_287:
	v_lshlrev_b32_e32 v134, 1, v130
	v_lshl_add_u64 v[138:139], v[138:139], 0, v[134:135]
	v_lshlrev_b32_e32 v144, 12, v131
	v_mov_b32_e32 v145, v135
	v_lshl_add_u64 v[138:139], v[138:139], 0, v[144:145]
	s_waitcnt vmcnt(30)
	v_cvt_pk_bf16_f32 v144, v66, v70
	s_waitcnt vmcnt(28)
	v_cvt_pk_bf16_f32 v145, v74, v78
	s_waitcnt vmcnt(26)
	v_cvt_pk_bf16_f32 v146, v82, v86
	s_waitcnt vmcnt(24)
	v_cvt_pk_bf16_f32 v147, v90, v94
	v_add_co_u32_e32 v66, vcc, s41, v138
	s_waitcnt vmcnt(22)
	v_cvt_pk_bf16_f32 v148, v98, v102
	s_waitcnt vmcnt(20)
	v_cvt_pk_bf16_f32 v149, v106, v110
	s_waitcnt vmcnt(18)
	v_cvt_pk_bf16_f32 v150, v114, v118
	s_waitcnt vmcnt(16)
	v_cvt_pk_bf16_f32 v151, v122, v126
	global_store_dwordx4 v[138:139], v[144:147], off nt
	global_store_dwordx4 v[138:139], v[148:151], off offset:16 nt
	s_cmp_eq_u64 s[24:25], 0
	v_cvt_pk_bf16_f32 v144, v67, v71
	v_addc_co_u32_e32 v67, vcc, 0, v139, vcc
	v_add_co_u32_e32 v70, vcc, s42, v138
	v_cvt_pk_bf16_f32 v145, v75, v79
	v_cvt_pk_bf16_f32 v146, v83, v87
	v_cvt_pk_bf16_f32 v147, v91, v95
	v_addc_co_u32_e32 v71, vcc, 0, v139, vcc
	v_cvt_pk_bf16_f32 v148, v99, v103
	v_cvt_pk_bf16_f32 v149, v107, v111
	v_cvt_pk_bf16_f32 v150, v115, v119
	v_cvt_pk_bf16_f32 v151, v123, v127
	global_store_dwordx4 v[70:71], v[144:147], off offset:-4096 nt
	global_store_dwordx4 v[66:67], v[148:151], off offset:16 nt
	v_add_co_u32_e32 v74, vcc, 0x3000, v138
	v_cvt_pk_bf16_f32 v144, v68, v72
	v_cvt_pk_bf16_f32 v145, v76, v80
	v_cvt_pk_bf16_f32 v146, v84, v88
	v_cvt_pk_bf16_f32 v147, v92, v96
	v_cvt_pk_bf16_f32 v148, v100, v104
	v_cvt_pk_bf16_f32 v149, v108, v112
	v_cvt_pk_bf16_f32 v150, v116, v120
	v_cvt_pk_bf16_f32 v151, v124, v128
	global_store_dwordx4 v[70:71], v[144:147], off nt
	global_store_dwordx4 v[70:71], v[148:151], off offset:16 nt
	v_cvt_pk_bf16_f32 v66, v69, v73
	v_cvt_pk_bf16_f32 v67, v77, v81
	v_cvt_pk_bf16_f32 v68, v85, v89
	v_cvt_pk_bf16_f32 v69, v93, v97
	v_cvt_pk_bf16_f32 v70, v101, v105
	v_cvt_pk_bf16_f32 v71, v109, v113
	v_cvt_pk_bf16_f32 v72, v117, v121
	v_cvt_pk_bf16_f32 v73, v125, v129
	v_addc_co_u32_e32 v75, vcc, 0, v139, vcc
	global_store_dwordx4 v[74:75], v[66:69], off nt
	global_store_dwordx4 v[74:75], v[70:73], off offset:16 nt
	s_cbranch_scc1 .LBB0_220
	global_load_dwordx4 v[66:69], v142, s[24:25]
	global_load_dwordx4 v[70:73], v142, s[24:25] offset:16
	global_load_dwordx4 v[74:77], v142, s[24:25] offset:32
	global_load_dwordx3 v[78:80], v142, s[24:25] offset:48
	global_load_dword v82, v137, s[24:25]
	s_waitcnt vmcnt(4)
	v_pk_mul_f32 v[4:5], v[4:5], v[66:67] op_sel_hi:[1,0]
	v_pk_mul_f32 v[2:3], v[2:3], v[66:67] op_sel_hi:[1,0]
	v_pk_mul_f32 v[8:9], v[8:9], v[66:67] op_sel:[0,1]
	v_pk_mul_f32 v[6:7], v[6:7], v[66:67] op_sel:[0,1]
	v_pk_mul_f32 v[12:13], v[12:13], v[68:69] op_sel_hi:[1,0]
	v_pk_mul_f32 v[10:11], v[10:11], v[68:69] op_sel_hi:[1,0]
	v_mov_b32_e32 v66, v69
	s_waitcnt vmcnt(3)
	v_pk_mul_f32 v[20:21], v[20:21], v[70:71] op_sel_hi:[1,0]
	v_pk_mul_f32 v[18:19], v[18:19], v[70:71] op_sel_hi:[1,0]
	v_pk_mul_f32 v[24:25], v[24:25], v[70:71] op_sel:[0,1]
	v_pk_mul_f32 v[22:23], v[22:23], v[70:71] op_sel:[0,1]
	v_pk_mul_f32 v[36:37], v[36:37], v[72:73] op_sel_hi:[1,0]
	v_pk_mul_f32 v[34:35], v[34:35], v[72:73] op_sel_hi:[1,0]
	v_mov_b32_e32 v68, v73
	s_waitcnt vmcnt(2)
	v_mov_b32_e32 v70, v77
	s_waitcnt vmcnt(1)
	v_mov_b32_e32 v72, v80
	v_pk_mul_f32 v[28:29], v[28:29], v[74:75] op_sel_hi:[1,0]
	v_pk_mul_f32 v[26:27], v[26:27], v[74:75] op_sel_hi:[1,0]
	v_pk_mul_f32 v[32:33], v[32:33], v[74:75] op_sel:[0,1]
	v_pk_mul_f32 v[30:31], v[30:31], v[74:75] op_sel:[0,1]
	v_pk_mul_f32 v[40:41], v[40:41], v[76:77] op_sel_hi:[1,0]
	v_pk_mul_f32 v[38:39], v[38:39], v[76:77] op_sel_hi:[1,0]
	v_pk_mul_f32 v[52:53], v[52:53], v[78:79] op_sel_hi:[1,0]
	v_pk_mul_f32 v[50:51], v[50:51], v[78:79] op_sel_hi:[1,0]
	v_pk_mul_f32 v[56:57], v[56:57], v[78:79] op_sel:[0,1]
	v_pk_mul_f32 v[54:55], v[54:55], v[78:79] op_sel:[0,1]
	s_waitcnt vmcnt(0)
	v_pk_mul_f32 v[64:65], v[64:65], v[82:83] op_sel_hi:[1,0]
	v_pk_mul_f32 v[16:17], v[16:17], v[66:67] op_sel_hi:[1,0]
	v_pk_mul_f32 v[14:15], v[14:15], v[66:67] op_sel_hi:[1,0]
	v_pk_mul_f32 v[44:45], v[44:45], v[68:69] op_sel_hi:[1,0]
	v_pk_mul_f32 v[42:43], v[42:43], v[68:69] op_sel_hi:[1,0]
	v_pk_mul_f32 v[48:49], v[48:49], v[70:71] op_sel_hi:[1,0]
	v_pk_mul_f32 v[46:47], v[46:47], v[70:71] op_sel_hi:[1,0]
	v_pk_mul_f32 v[60:61], v[60:61], v[72:73] op_sel_hi:[1,0]
	v_pk_mul_f32 v[58:59], v[58:59], v[72:73] op_sel_hi:[1,0]
	v_pk_mul_f32 v[62:63], v[62:63], v[82:83] op_sel_hi:[1,0]
	s_branch .LBB0_220

; #define WTILE_LOAD(T, v) do { const float* s_ = (T).src + (size_t)(16 * kq) * (T).ldw + 4 * n4; \
;     _Pragma("unroll") for (int j = 0; j < 16; ++j) v[j] = __builtin_nontemporal_load((const f32x4*)(s_ + (size_t)j * (T).ldw)); } while (0)
; __device__ __forceinline__ WTile expert_tile_addr(const ExpertCopy& X, int it) {
;     ...
;     const int e = it / (3 * I_SQ); int r = it % (3 * I_SQ); const int which = r / I_SQ; r %= I_SQ; const int kb = r / 32, nb = r % 32, n0 = nb * 64, k0 = kb * 64;
;     WTile t; t.ksc = nullptr; t.perm = 0;
;     if (which == 0) { t.src = X.w_e1 + (size_t)e * D * FF + (size_t)k0 * FF + n0; t.ldw = FF; t.dst = X.W13 + (size_t)(e * 4096 + 256 * (n0 / 128) + (n0 % 128)) * D + k0; t.ldk = D; }
;     else if (which == 1) { t.src = X.w_e3 + (size_t)e * D * FF + (size_t)k0 * FF + n0; t.ldw = FF; t.dst = X.W13 + (size_t)(e * 4096 + 256 * (n0 / 128) + 128 + (n0 % 128)) * D + k0; t.ldk = D; }
;     else { t.src = X.w_e2 + (size_t)e * FF * D + (size_t)k0 * D + n0; t.ldw = D; t.dst = X.W2 + (size_t)(e * 2048 + n0) * FF + k0; t.ldk = FF; }
; __device__ __forceinline__ void expert_copy_share(const ExpertCopy& X, unsigned* qhead, int lane) {
;     ...
;     for (;;) { int g0 = 0; if (lane == 0) g0 = (int)__hip_atomic_fetch_add(qhead, (unsigned)GRP, __ATOMIC_RELAXED, __HIP_MEMORY_SCOPE_AGENT);
;         g0 = __builtin_amdgcn_readfirstlane(g0); if (g0 >= NIT) break;
;         const WTile t0 = expert_tile_addr(X, g0); const bool w13 = (g0 / (32 * 32)) % 3 != 2;
;         f32x4 va[16], vb[16];
;         WTile ta = t0, tb = t0; tb.src = t0.src + 64; tb.dst = t0.dst + (size_t)64 * D;
;         WTILE_LOAD(ta, va); WTILE_LOAD(tb, vb);
.LBB0_290:
	v_lshl_add_u64 v[16:17], s[28:29], 0, v[2:3]
	v_mov_b32_e32 v15, v3
	v_lshl_add_u64 v[16:17], v[16:17], 0, v[14:15]
	v_add_co_u32_e32 v18, vcc, s6, v16
	s_add_u32 s10, s0, s22
	s_nop 0
	v_addc_co_u32_e32 v19, vcc, 0, v17, vcc
	v_add_co_u32_e32 v20, vcc, s7, v16
	s_addc_u32 s22, s1, s23
	s_nop 0
	v_addc_co_u32_e32 v21, vcc, 0, v17, vcc
	v_add_co_u32_e32 v22, vcc, s33, v16
	s_ashr_i32 s21, s20, 31
	s_nop 0
	v_addc_co_u32_e32 v23, vcc, 0, v17, vcc
	v_add_co_u32_e32 v24, vcc, s34, v16
	s_lshl_b64 s[20:21], s[20:21], 12
	s_nop 0
	v_addc_co_u32_e32 v25, vcc, 0, v17, vcc
	v_add_co_u32_e32 v26, vcc, s35, v16
	s_add_u32 s10, s10, s20
	s_nop 0
	v_addc_co_u32_e32 v27, vcc, 0, v17, vcc
	v_add_co_u32_e32 v28, vcc, s36, v16
	s_addc_u32 s20, s22, s21
	s_nop 0
	v_addc_co_u32_e32 v29, vcc, 0, v17, vcc
	v_add_co_u32_e32 v30, vcc, s37, v16
	s_ashr_i32 s21, s60, 31
	s_nop 0
	v_addc_co_u32_e32 v31, vcc, 0, v17, vcc
	v_add_co_u32_e32 v32, vcc, s38, v16
	s_lshr_b32 s21, s21, 22
	s_nop 0
	v_addc_co_u32_e32 v33, vcc, 0, v17, vcc
	v_add_co_u32_e32 v34, vcc, s39, v16
	s_add_i32 s60, s60, s21
	s_nop 0
	v_addc_co_u32_e32 v35, vcc, 0, v17, vcc
	v_add_co_u32_e32 v36, vcc, s40, v16
	s_ashr_i32 s21, s60, 10
	s_nop 0
	v_addc_co_u32_e32 v37, vcc, 0, v17, vcc
	v_add_co_u32_e32 v38, vcc, s41, v16
	s_mul_hi_i32 s22, s21, 0x55555556
	s_nop 0
	v_addc_co_u32_e32 v39, vcc, 0, v17, vcc
	v_add_co_u32_e32 v40, vcc, s42, v16
	s_lshr_b32 s23, s22, 31
	s_nop 0
	v_addc_co_u32_e32 v41, vcc, 0, v17, vcc
	v_add_co_u32_e32 v42, vcc, s43, v16
	s_add_i32 s22, s22, s23
	s_nop 0
	v_addc_co_u32_e32 v43, vcc, 0, v17, vcc
	v_add_co_u32_e32 v44, vcc, s44, v16
	s_mul_i32 s22, s22, 3
	s_nop 0
	v_addc_co_u32_e32 v45, vcc, 0, v17, vcc
	v_add_co_u32_e32 v46, vcc, s45, v16
	s_sub_i32 s21, s21, s22
	s_nop 0
	v_addc_co_u32_e32 v47, vcc, 0, v17, vcc
	global_load_dwordx4 v[48:51], v[16:17], off nt
	global_load_dwordx4 v[52:55], v[16:17], off offset:256 nt
	global_load_dwordx4 v[56:59], v[18:19], off nt
	global_load_dwordx4 v[60:63], v[18:19], off offset:256 nt
	global_load_dwordx4 v[64:67], v[20:21], off nt
	global_load_dwordx4 v[68:71], v[20:21], off offset:256 nt
	global_load_dwordx4 v[72:75], v[22:23], off nt
	global_load_dwordx4 v[76:79], v[22:23], off offset:256 nt
	global_load_dwordx4 v[80:83], v[24:25], off nt
	global_load_dwordx4 v[84:87], v[24:25], off offset:256 nt
	global_load_dwordx4 v[88:91], v[26:27], off nt
	global_load_dwordx4 v[92:95], v[26:27], off offset:256 nt
	global_load_dwordx4 v[96:99], v[28:29], off nt
	global_load_dwordx4 v[100:103], v[28:29], off offset:256 nt
	global_load_dwordx4 v[104:107], v[30:31], off nt
	global_load_dwordx4 v[108:111], v[30:31], off offset:256 nt
	global_load_dwordx4 v[112:115], v[32:33], off nt
	global_load_dwordx4 v[116:119], v[32:33], off offset:256 nt
	global_load_dwordx4 v[120:123], v[34:35], off nt
	global_load_dwordx4 v[124:127], v[34:35], off offset:256 nt
	global_load_dwordx4 v[132:135], v[36:37], off nt
	global_load_dwordx4 v[136:139], v[36:37], off offset:256 nt
	global_load_dwordx4 v[140:143], v[38:39], off nt
	global_load_dwordx4 v[144:147], v[38:39], off offset:256 nt
	global_load_dwordx4 v[148:151], v[40:41], off nt
	global_load_dwordx4 v[152:155], v[40:41], off offset:256 nt
	global_load_dwordx4 v[156:159], v[42:43], off nt
	global_load_dwordx4 v[160:163], v[42:43], off offset:256 nt
	global_load_dwordx4 v[164:167], v[44:45], off nt
	global_load_dwordx4 v[168:171], v[44:45], off offset:256 nt
	global_load_dwordx4 v[172:175], v[46:47], off nt
	global_load_dwordx4 v[176:179], v[46:47], off offset:256 nt
	s_lshl_b64 s[18:19], s[18:19], 1
	s_add_u32 s18, s10, s18
	s_addc_u32 s19, s20, s19
	s_cmp_eq_u32 s21, 2
	v_mov_b32_e32 v5, v3
	v_lshl_add_u64 v[128:129], s[18:19], 0, v[4:5]
	v_mov_b32_e32 v7, v3
	v_lshl_add_u64 v[184:185], v[128:129], 0, v[6:7]
	s_waitcnt vmcnt(29)
	v_cvt_pk_bf16_f32 v180, v48, v56
	s_waitcnt vmcnt(25)
	v_cvt_pk_bf16_f32 v181, v64, v72
	s_waitcnt vmcnt(21)
	v_cvt_pk_bf16_f32 v182, v80, v88
	s_waitcnt vmcnt(17)
	v_cvt_pk_bf16_f32 v183, v96, v104
	v_mov_b32_e32 v9, v3
	s_waitcnt vmcnt(13)
	v_cvt_pk_bf16_f32 v188, v112, v120
	s_waitcnt vmcnt(9)
	v_cvt_pk_bf16_f32 v189, v132, v140
	s_waitcnt vmcnt(5)
	v_cvt_pk_bf16_f32 v190, v148, v156
	s_waitcnt vmcnt(1)
; #define WTILE_LOAD(T, v) do { const float* s_ = (T).src + (size_t)(16 * kq) * (T).ldw + 4 * n4; \
;     _Pragma("unroll") for (int j = 0; j < 16; ++j) v[j] = __builtin_nontemporal_load((const f32x4*)(s_ + (size_t)j * (T).ldw)); } while (0)
; __device__ __forceinline__ void expert_copy_share(const ExpertCopy& X, unsigned* qhead, int lane) {
;     ...
;         for (int k = 0; k < GRP; k += 2) {
;             __builtin_amdgcn_sched_barrier(0);
;             WTILE_STORE(ta, va);
;             if (k + 2 < GRP) { ta.src = t0.src + 64 * (k + 2); ta.dst = t0.dst + (size_t)(w13 ? 256 * ((k + 2) >> 1) : 64 * (k + 2)) * D; WTILE_LOAD(ta, va); }
;             __builtin_amdgcn_sched_barrier(0);
;             WTILE_STORE(tb, vb);
;             if (k + 3 < GRP) { tb.src = t0.src + 64 * (k + 3); tb.dst = t0.dst + (size_t)(w13 ? 256 * ((k + 3) >> 1) + 64 : 64 * (k + 3)) * D; WTILE_LOAD(tb, vb); }
	v_cvt_pk_bf16_f32 v191, v164, v172
	global_store_dwordx4 v[184:185], v[180:183], off nt
	global_store_dwordx4 v[184:185], v[188:191], off offset:16 nt
	v_lshl_add_u64 v[184:185], v[128:129], 0, v[8:9]
	v_cvt_pk_bf16_f32 v180, v49, v57
	v_cvt_pk_bf16_f32 v181, v65, v73
	v_cvt_pk_bf16_f32 v182, v81, v89
	v_cvt_pk_bf16_f32 v183, v97, v105
	v_mov_b32_e32 v11, v3
	v_cvt_pk_bf16_f32 v188, v113, v121
	v_cvt_pk_bf16_f32 v189, v133, v141
	v_cvt_pk_bf16_f32 v190, v149, v157
	v_cvt_pk_bf16_f32 v191, v165, v173
	global_store_dwordx4 v[184:185], v[180:183], off nt
	global_store_dwordx4 v[184:185], v[188:191], off offset:16 nt
	v_lshl_add_u64 v[48:49], v[128:129], 0, v[10:11]
	v_cvt_pk_bf16_f32 v180, v50, v58
	v_cvt_pk_bf16_f32 v181, v66, v74
	v_cvt_pk_bf16_f32 v182, v82, v90
	v_cvt_pk_bf16_f32 v183, v98, v106
	v_mov_b32_e32 v13, v3
	v_cvt_pk_bf16_f32 v188, v114, v122
	v_cvt_pk_bf16_f32 v189, v134, v142
	v_cvt_pk_bf16_f32 v190, v150, v158
	v_cvt_pk_bf16_f32 v191, v166, v174
	global_store_dwordx4 v[48:49], v[180:183], off nt
	global_store_dwordx4 v[48:49], v[188:191], off offset:16 nt
	v_lshl_add_u64 v[64:65], v[128:129], 0, v[12:13]
	v_cvt_pk_bf16_f32 v48, v51, v59
	v_cvt_pk_bf16_f32 v49, v67, v75
	v_cvt_pk_bf16_f32 v50, v83, v91
	v_cvt_pk_bf16_f32 v51, v99, v107
	v_cvt_pk_bf16_f32 v56, v115, v123
	v_cvt_pk_bf16_f32 v57, v135, v143
	v_cvt_pk_bf16_f32 v58, v151, v159
	v_cvt_pk_bf16_f32 v59, v167, v175
	global_store_dwordx4 v[64:65], v[48:51], off nt
	global_store_dwordx4 v[64:65], v[56:59], off offset:16 nt
	global_load_dwordx4 v[48:51], v[16:17], off offset:512 nt
	s_nop 0
	global_load_dwordx4 v[56:59], v[18:19], off offset:512 nt
	global_load_dwordx4 v[64:67], v[20:21], off offset:512 nt
	global_load_dwordx4 v[72:75], v[22:23], off offset:512 nt
	global_load_dwordx4 v[80:83], v[24:25], off offset:512 nt
	global_load_dwordx4 v[88:91], v[26:27], off offset:512 nt
	global_load_dwordx4 v[96:99], v[28:29], off offset:512 nt
	global_load_dwordx4 v[104:107], v[30:31], off offset:512 nt
	global_load_dwordx4 v[112:115], v[32:33], off offset:512 nt
	global_load_dwordx4 v[120:123], v[34:35], off offset:512 nt
	global_load_dwordx4 v[132:135], v[36:37], off offset:512 nt
	global_load_dwordx4 v[140:143], v[38:39], off offset:512 nt
	global_load_dwordx4 v[148:151], v[40:41], off offset:512 nt
	global_load_dwordx4 v[156:159], v[42:43], off offset:512 nt
	global_load_dwordx4 v[164:167], v[44:45], off offset:512 nt
	global_load_dwordx4 v[172:175], v[46:47], off offset:512 nt
	s_cselect_b32 s31, s46, 0x100000
	v_lshl_add_u64 v[128:129], v[128:129], 0, s[16:17]
	v_lshl_add_u64 v[184:185], v[128:129], 0, v[6:7]
	v_cvt_pk_bf16_f32 v180, v52, v60
	v_cvt_pk_bf16_f32 v181, v68, v76
	v_cvt_pk_bf16_f32 v182, v84, v92
	v_cvt_pk_bf16_f32 v183, v100, v108
	v_cvt_pk_bf16_f32 v188, v116, v124
	v_cvt_pk_bf16_f32 v189, v136, v144
	v_cvt_pk_bf16_f32 v190, v152, v160
	s_waitcnt vmcnt(24)
	v_cvt_pk_bf16_f32 v191, v168, v176
	global_store_dwordx4 v[184:185], v[180:183], off nt
	global_store_dwordx4 v[184:185], v[188:191], off offset:16 nt
	v_lshl_add_u64 v[184:185], v[128:129], 0, v[8:9]
	v_cvt_pk_bf16_f32 v180, v53, v61
	v_cvt_pk_bf16_f32 v181, v69, v77
	v_cvt_pk_bf16_f32 v182, v85, v93
	v_cvt_pk_bf16_f32 v183, v101, v109
	v_cvt_pk_bf16_f32 v188, v117, v125
	v_cvt_pk_bf16_f32 v189, v137, v145
	v_cvt_pk_bf16_f32 v190, v153, v161
	v_cvt_pk_bf16_f32 v191, v169, v177
	global_store_dwordx4 v[184:185], v[180:183], off nt
	global_store_dwordx4 v[184:185], v[188:191], off offset:16 nt
	v_lshl_add_u64 v[52:53], v[128:129], 0, v[10:11]
	v_cvt_pk_bf16_f32 v180, v54, v62
	v_cvt_pk_bf16_f32 v181, v70, v78
	v_cvt_pk_bf16_f32 v182, v86, v94
	v_cvt_pk_bf16_f32 v183, v102, v110
	v_cvt_pk_bf16_f32 v188, v118, v126
	v_cvt_pk_bf16_f32 v189, v138, v146
	v_cvt_pk_bf16_f32 v190, v154, v162
	v_cvt_pk_bf16_f32 v191, v170, v178
	global_store_dwordx4 v[52:53], v[180:183], off nt
	global_store_dwordx4 v[52:53], v[188:191], off offset:16 nt
	v_lshl_add_u64 v[68:69], v[128:129], 0, v[12:13]
	v_cvt_pk_bf16_f32 v52, v55, v63
	v_cvt_pk_bf16_f32 v53, v71, v79
	v_cvt_pk_bf16_f32 v54, v87, v95
	v_cvt_pk_bf16_f32 v55, v103, v111
	v_cvt_pk_bf16_f32 v60, v119, v127
	v_cvt_pk_bf16_f32 v61, v139, v147
	v_cvt_pk_bf16_f32 v62, v155, v163
	v_cvt_pk_bf16_f32 v63, v171, v179
	global_store_dwordx4 v[68:69], v[52:55], off nt
	global_store_dwordx4 v[68:69], v[60:63], off offset:16 nt
	global_load_dwordx4 v[52:55], v[16:17], off offset:768 nt
	s_nop 0
	global_load_dwordx4 v[60:63], v[18:19], off offset:768 nt
	global_load_dwordx4 v[68:71], v[20:21], off offset:768 nt
	global_load_dwordx4 v[76:79], v[22:23], off offset:768 nt
	global_load_dwordx4 v[84:87], v[24:25], off offset:768 nt
	global_load_dwordx4 v[92:95], v[26:27], off offset:768 nt
	global_load_dwordx4 v[100:103], v[28:29], off offset:768 nt
	global_load_dwordx4 v[108:111], v[30:31], off offset:768 nt
	global_load_dwordx4 v[116:119], v[32:33], off offset:768 nt
	global_load_dwordx4 v[124:127], v[34:35], off offset:768 nt
	global_load_dwordx4 v[136:139], v[36:37], off offset:768 nt
	global_load_dwordx4 v[144:147], v[38:39], off offset:768 nt
	global_load_dwordx4 v[152:155], v[40:41], off offset:768 nt
	global_load_dwordx4 v[160:163], v[42:43], off offset:768 nt
	global_load_dwordx4 v[168:171], v[44:45], off offset:768 nt
	global_load_dwordx4 v[176:179], v[46:47], off offset:768 nt
	s_cselect_b32 s62, s47, 0x140000
	s_cselect_b32 s30, 0x100000, s48
	s_cselect_b32 s29, 0x140000, s49
	s_cselect_b32 s28, s50, 0x300000
	s_cselect_b32 s27, s51, 0x340000
	s_cselect_b32 s26, 0x200000, s52
	s_cselect_b32 s25, 0x240000, s53
	s_cselect_b32 s24, s54, 0x500000
	s_cselect_b32 s23, s55, 0x540000
	s_cselect_b32 s22, 0x300000, s56
	s_cselect_b32 s21, 0x340000, s57
	s_cselect_b32 s20, s58, 0x700000
	s_cselect_b32 s10, s59, 0x740000
	s_add_u32 s60, s18, s31
	s_addc_u32 s61, s19, 0
	v_lshl_add_u64 v[128:129], s[60:61], 0, v[4:5]
	v_lshl_add_u64 v[184:185], v[128:129], 0, v[6:7]
	s_waitcnt vmcnt(38)
; #define WTILE_LOAD(T, v) do { const float* s_ = (T).src + (size_t)(16 * kq) * (T).ldw + 4 * n4; \
;     _Pragma("unroll") for (int j = 0; j < 16; ++j) v[j] = __builtin_nontemporal_load((const f32x4*)(s_ + (size_t)j * (T).ldw)); } while (0)
; __device__ __forceinline__ void expert_copy_share(const ExpertCopy& X, unsigned* qhead, int lane) {
;     ...
;         for (int k = 0; k < GRP; k += 2) {
;             __builtin_amdgcn_sched_barrier(0);
;             WTILE_STORE(ta, va);
;             if (k + 2 < GRP) { ta.src = t0.src + 64 * (k + 2); ta.dst = t0.dst + (size_t)(w13 ? 256 * ((k + 2) >> 1) : 64 * (k + 2)) * D; WTILE_LOAD(ta, va); }
;             __builtin_amdgcn_sched_barrier(0);
;             WTILE_STORE(tb, vb);
;             if (k + 3 < GRP) { tb.src = t0.src + 64 * (k + 3); tb.dst = t0.dst + (size_t)(w13 ? 256 * ((k + 3) >> 1) + 64 : 64 * (k + 3)) * D; WTILE_LOAD(tb, vb); }
	v_cvt_pk_bf16_f32 v180, v48, v56
	s_waitcnt vmcnt(36)
	v_cvt_pk_bf16_f32 v181, v64, v72
	s_waitcnt vmcnt(34)
	v_cvt_pk_bf16_f32 v182, v80, v88
	s_waitcnt vmcnt(32)
	v_cvt_pk_bf16_f32 v183, v96, v104
	s_waitcnt vmcnt(30)
	v_cvt_pk_bf16_f32 v188, v112, v120
	s_waitcnt vmcnt(28)
	v_cvt_pk_bf16_f32 v189, v132, v140
	s_waitcnt vmcnt(26)
	v_cvt_pk_bf16_f32 v190, v148, v156
	s_waitcnt vmcnt(24)
	v_cvt_pk_bf16_f32 v191, v164, v172
	global_store_dwordx4 v[184:185], v[180:183], off nt
	global_store_dwordx4 v[184:185], v[188:191], off offset:16 nt
	v_lshl_add_u64 v[184:185], v[128:129], 0, v[8:9]
	v_cvt_pk_bf16_f32 v180, v49, v57
	v_cvt_pk_bf16_f32 v181, v65, v73
	v_cvt_pk_bf16_f32 v182, v81, v89
	v_cvt_pk_bf16_f32 v183, v97, v105
	v_cvt_pk_bf16_f32 v188, v113, v121
	v_cvt_pk_bf16_f32 v189, v133, v141
	v_cvt_pk_bf16_f32 v190, v149, v157
	v_cvt_pk_bf16_f32 v191, v165, v173
	global_store_dwordx4 v[184:185], v[180:183], off nt
	global_store_dwordx4 v[184:185], v[188:191], off offset:16 nt
	v_lshl_add_u64 v[48:49], v[128:129], 0, v[10:11]
	v_cvt_pk_bf16_f32 v180, v50, v58
	v_cvt_pk_bf16_f32 v181, v66, v74
	v_cvt_pk_bf16_f32 v182, v82, v90
	v_cvt_pk_bf16_f32 v183, v98, v106
	v_cvt_pk_bf16_f32 v188, v114, v122
	v_cvt_pk_bf16_f32 v189, v134, v142
	v_cvt_pk_bf16_f32 v190, v150, v158
	v_cvt_pk_bf16_f32 v191, v166, v174
	global_store_dwordx4 v[48:49], v[180:183], off nt
	global_store_dwordx4 v[48:49], v[188:191], off offset:16 nt
	v_lshl_add_u64 v[64:65], v[128:129], 0, v[12:13]
	v_cvt_pk_bf16_f32 v48, v51, v59
	v_cvt_pk_bf16_f32 v49, v67, v75
	v_cvt_pk_bf16_f32 v50, v83, v91
	v_cvt_pk_bf16_f32 v51, v99, v107
	v_cvt_pk_bf16_f32 v56, v115, v123
	v_cvt_pk_bf16_f32 v57, v135, v143
	v_cvt_pk_bf16_f32 v58, v151, v159
	v_cvt_pk_bf16_f32 v59, v167, v175
	global_store_dwordx4 v[64:65], v[48:51], off nt
	global_store_dwordx4 v[64:65], v[56:59], off offset:16 nt
	global_load_dwordx4 v[48:51], v[16:17], off offset:1024 nt
	s_nop 0
	global_load_dwordx4 v[56:59], v[18:19], off offset:1024 nt
	global_load_dwordx4 v[64:67], v[20:21], off offset:1024 nt
	global_load_dwordx4 v[72:75], v[22:23], off offset:1024 nt
	global_load_dwordx4 v[80:83], v[24:25], off offset:1024 nt
	global_load_dwordx4 v[88:91], v[26:27], off offset:1024 nt
	global_load_dwordx4 v[96:99], v[28:29], off offset:1024 nt
	global_load_dwordx4 v[104:107], v[30:31], off offset:1024 nt
	global_load_dwordx4 v[112:115], v[32:33], off offset:1024 nt
	global_load_dwordx4 v[120:123], v[34:35], off offset:1024 nt
	global_load_dwordx4 v[132:135], v[36:37], off offset:1024 nt
	global_load_dwordx4 v[140:143], v[38:39], off offset:1024 nt
	global_load_dwordx4 v[148:151], v[40:41], off offset:1024 nt
	global_load_dwordx4 v[156:159], v[42:43], off offset:1024 nt
	global_load_dwordx4 v[164:167], v[44:45], off offset:1024 nt
	global_load_dwordx4 v[172:175], v[46:47], off offset:1024 nt
	s_add_u32 s60, s18, s62
	s_addc_u32 s61, s19, 0
	v_lshl_add_u64 v[128:129], s[60:61], 0, v[4:5]
	v_lshl_add_u64 v[184:185], v[128:129], 0, v[6:7]
	s_waitcnt vmcnt(38)
	v_cvt_pk_bf16_f32 v180, v52, v60
	s_waitcnt vmcnt(36)
	v_cvt_pk_bf16_f32 v181, v68, v76
	s_waitcnt vmcnt(34)
	v_cvt_pk_bf16_f32 v182, v84, v92
	s_waitcnt vmcnt(32)
	v_cvt_pk_bf16_f32 v183, v100, v108
	s_waitcnt vmcnt(30)
	v_cvt_pk_bf16_f32 v188, v116, v124
	s_waitcnt vmcnt(28)
	v_cvt_pk_bf16_f32 v189, v136, v144
	s_waitcnt vmcnt(26)
	v_cvt_pk_bf16_f32 v190, v152, v160
	s_waitcnt vmcnt(24)
	v_cvt_pk_bf16_f32 v191, v168, v176
	global_store_dwordx4 v[184:185], v[180:183], off nt
	global_store_dwordx4 v[184:185], v[188:191], off offset:16 nt
	v_lshl_add_u64 v[184:185], v[128:129], 0, v[8:9]
	v_cvt_pk_bf16_f32 v180, v53, v61
	v_cvt_pk_bf16_f32 v181, v69, v77
	v_cvt_pk_bf16_f32 v182, v85, v93
	v_cvt_pk_bf16_f32 v183, v101, v109
	v_cvt_pk_bf16_f32 v188, v117, v125
	v_cvt_pk_bf16_f32 v189, v137, v145
	v_cvt_pk_bf16_f32 v190, v153, v161
	v_cvt_pk_bf16_f32 v191, v169, v177
	global_store_dwordx4 v[184:185], v[180:183], off nt
	global_store_dwordx4 v[184:185], v[188:191], off offset:16 nt
	v_lshl_add_u64 v[52:53], v[128:129], 0, v[10:11]
	v_cvt_pk_bf16_f32 v180, v54, v62
	v_cvt_pk_bf16_f32 v181, v70, v78
	v_cvt_pk_bf16_f32 v182, v86, v94
	v_cvt_pk_bf16_f32 v183, v102, v110
	v_cvt_pk_bf16_f32 v188, v118, v126
	v_cvt_pk_bf16_f32 v189, v138, v146
	v_cvt_pk_bf16_f32 v190, v154, v162
	v_cvt_pk_bf16_f32 v191, v170, v178
	global_store_dwordx4 v[52:53], v[180:183], off nt
	global_store_dwordx4 v[52:53], v[188:191], off offset:16 nt
	v_lshl_add_u64 v[68:69], v[128:129], 0, v[12:13]
	v_cvt_pk_bf16_f32 v52, v55, v63
	v_cvt_pk_bf16_f32 v53, v71, v79
	v_cvt_pk_bf16_f32 v54, v87, v95
	v_cvt_pk_bf16_f32 v55, v103, v111
	v_cvt_pk_bf16_f32 v60, v119, v127
	v_cvt_pk_bf16_f32 v61, v139, v147
	v_cvt_pk_bf16_f32 v62, v155, v163
	v_cvt_pk_bf16_f32 v63, v171, v179
	global_store_dwordx4 v[68:69], v[52:55], off nt
	global_store_dwordx4 v[68:69], v[60:63], off offset:16 nt
	global_load_dwordx4 v[52:55], v[16:17], off offset:1280 nt
	s_nop 0
	global_load_dwordx4 v[60:63], v[18:19], off offset:1280 nt
	global_load_dwordx4 v[68:71], v[20:21], off offset:1280 nt
	global_load_dwordx4 v[76:79], v[22:23], off offset:1280 nt
	global_load_dwordx4 v[84:87], v[24:25], off offset:1280 nt
	global_load_dwordx4 v[92:95], v[26:27], off offset:1280 nt
	global_load_dwordx4 v[100:103], v[28:29], off offset:1280 nt
	global_load_dwordx4 v[108:111], v[30:31], off offset:1280 nt
	global_load_dwordx4 v[116:119], v[32:33], off offset:1280 nt
	global_load_dwordx4 v[124:127], v[34:35], off offset:1280 nt
	global_load_dwordx4 v[136:139], v[36:37], off offset:1280 nt
	global_load_dwordx4 v[144:147], v[38:39], off offset:1280 nt
	global_load_dwordx4 v[152:155], v[40:41], off offset:1280 nt
	global_load_dwordx4 v[160:163], v[42:43], off offset:1280 nt
	global_load_dwordx4 v[168:171], v[44:45], off offset:1280 nt
	global_load_dwordx4 v[176:179], v[46:47], off offset:1280 nt
	s_add_u32 s30, s18, s30
	s_addc_u32 s31, s19, 0
	v_lshl_add_u64 v[128:129], s[30:31], 0, v[4:5]
	v_lshl_add_u64 v[184:185], v[128:129], 0, v[6:7]
	s_waitcnt vmcnt(38)
; #define WTILE_LOAD(T, v) do { const float* s_ = (T).src + (size_t)(16 * kq) * (T).ldw + 4 * n4; \
;     _Pragma("unroll") for (int j = 0; j < 16; ++j) v[j] = __builtin_nontemporal_load((const f32x4*)(s_ + (size_t)j * (T).ldw)); } while (0)
; __device__ __forceinline__ void expert_copy_share(const ExpertCopy& X, unsigned* qhead, int lane) {
;     ...
;         for (int k = 0; k < GRP; k += 2) {
;             __builtin_amdgcn_sched_barrier(0);
;             WTILE_STORE(ta, va);
;             if (k + 2 < GRP) { ta.src = t0.src + 64 * (k + 2); ta.dst = t0.dst + (size_t)(w13 ? 256 * ((k + 2) >> 1) : 64 * (k + 2)) * D; WTILE_LOAD(ta, va); }
;             __builtin_amdgcn_sched_barrier(0);
;             WTILE_STORE(tb, vb);
;             if (k + 3 < GRP) { tb.src = t0.src + 64 * (k + 3); tb.dst = t0.dst + (size_t)(w13 ? 256 * ((k + 3) >> 1) + 64 : 64 * (k + 3)) * D; WTILE_LOAD(tb, vb); }
	v_cvt_pk_bf16_f32 v180, v48, v56
	s_waitcnt vmcnt(36)
	v_cvt_pk_bf16_f32 v181, v64, v72
	s_waitcnt vmcnt(34)
	v_cvt_pk_bf16_f32 v182, v80, v88
	s_waitcnt vmcnt(32)
	v_cvt_pk_bf16_f32 v183, v96, v104
	s_waitcnt vmcnt(30)
	v_cvt_pk_bf16_f32 v188, v112, v120
	s_waitcnt vmcnt(28)
	v_cvt_pk_bf16_f32 v189, v132, v140
	s_waitcnt vmcnt(26)
	v_cvt_pk_bf16_f32 v190, v148, v156
	s_waitcnt vmcnt(24)
	v_cvt_pk_bf16_f32 v191, v164, v172
	global_store_dwordx4 v[184:185], v[180:183], off nt
	global_store_dwordx4 v[184:185], v[188:191], off offset:16 nt
	v_lshl_add_u64 v[184:185], v[128:129], 0, v[8:9]
	v_cvt_pk_bf16_f32 v180, v49, v57
	v_cvt_pk_bf16_f32 v181, v65, v73
	v_cvt_pk_bf16_f32 v182, v81, v89
	v_cvt_pk_bf16_f32 v183, v97, v105
	v_cvt_pk_bf16_f32 v188, v113, v121
	v_cvt_pk_bf16_f32 v189, v133, v141
	v_cvt_pk_bf16_f32 v190, v149, v157
	v_cvt_pk_bf16_f32 v191, v165, v173
	global_store_dwordx4 v[184:185], v[180:183], off nt
	global_store_dwordx4 v[184:185], v[188:191], off offset:16 nt
	v_lshl_add_u64 v[48:49], v[128:129], 0, v[10:11]
	v_cvt_pk_bf16_f32 v180, v50, v58
	v_cvt_pk_bf16_f32 v181, v66, v74
	v_cvt_pk_bf16_f32 v182, v82, v90
	v_cvt_pk_bf16_f32 v183, v98, v106
	v_cvt_pk_bf16_f32 v188, v114, v122
	v_cvt_pk_bf16_f32 v189, v134, v142
	v_cvt_pk_bf16_f32 v190, v150, v158
	v_cvt_pk_bf16_f32 v191, v166, v174
	global_store_dwordx4 v[48:49], v[180:183], off nt
	global_store_dwordx4 v[48:49], v[188:191], off offset:16 nt
	v_lshl_add_u64 v[64:65], v[128:129], 0, v[12:13]
	v_cvt_pk_bf16_f32 v48, v51, v59
	v_cvt_pk_bf16_f32 v49, v67, v75
	v_cvt_pk_bf16_f32 v50, v83, v91
	v_cvt_pk_bf16_f32 v51, v99, v107
	v_cvt_pk_bf16_f32 v56, v115, v123
	v_cvt_pk_bf16_f32 v57, v135, v143
	v_cvt_pk_bf16_f32 v58, v151, v159
	v_cvt_pk_bf16_f32 v59, v167, v175
	global_store_dwordx4 v[64:65], v[48:51], off nt
	global_store_dwordx4 v[64:65], v[56:59], off offset:16 nt
	global_load_dwordx4 v[48:51], v[16:17], off offset:1536 nt
	s_nop 0
	global_load_dwordx4 v[56:59], v[18:19], off offset:1536 nt
	global_load_dwordx4 v[64:67], v[20:21], off offset:1536 nt
	global_load_dwordx4 v[72:75], v[22:23], off offset:1536 nt
	global_load_dwordx4 v[80:83], v[24:25], off offset:1536 nt
	global_load_dwordx4 v[88:91], v[26:27], off offset:1536 nt
	global_load_dwordx4 v[96:99], v[28:29], off offset:1536 nt
	global_load_dwordx4 v[104:107], v[30:31], off offset:1536 nt
	global_load_dwordx4 v[112:115], v[32:33], off offset:1536 nt
	global_load_dwordx4 v[120:123], v[34:35], off offset:1536 nt
	global_load_dwordx4 v[132:135], v[36:37], off offset:1536 nt
	global_load_dwordx4 v[140:143], v[38:39], off offset:1536 nt
	global_load_dwordx4 v[148:151], v[40:41], off offset:1536 nt
	global_load_dwordx4 v[156:159], v[42:43], off offset:1536 nt
	global_load_dwordx4 v[164:167], v[44:45], off offset:1536 nt
	global_load_dwordx4 v[172:175], v[46:47], off offset:1536 nt
	s_add_u32 s30, s18, s29
	s_addc_u32 s31, s19, 0
	v_lshl_add_u64 v[128:129], s[30:31], 0, v[4:5]
	v_lshl_add_u64 v[184:185], v[128:129], 0, v[6:7]
	s_waitcnt vmcnt(38)
	v_cvt_pk_bf16_f32 v180, v52, v60
	s_waitcnt vmcnt(36)
	v_cvt_pk_bf16_f32 v181, v68, v76
	s_waitcnt vmcnt(34)
	v_cvt_pk_bf16_f32 v182, v84, v92
	s_waitcnt vmcnt(32)
	v_cvt_pk_bf16_f32 v183, v100, v108
	s_waitcnt vmcnt(30)
	v_cvt_pk_bf16_f32 v188, v116, v124
	s_waitcnt vmcnt(28)
	v_cvt_pk_bf16_f32 v189, v136, v144
	s_waitcnt vmcnt(26)
	v_cvt_pk_bf16_f32 v190, v152, v160
	s_waitcnt vmcnt(24)
	v_cvt_pk_bf16_f32 v191, v168, v176
	global_store_dwordx4 v[184:185], v[180:183], off nt
	global_store_dwordx4 v[184:185], v[188:191], off offset:16 nt
	v_lshl_add_u64 v[184:185], v[128:129], 0, v[8:9]
	v_cvt_pk_bf16_f32 v180, v53, v61
	v_cvt_pk_bf16_f32 v181, v69, v77
	v_cvt_pk_bf16_f32 v182, v85, v93
	v_cvt_pk_bf16_f32 v183, v101, v109
	v_cvt_pk_bf16_f32 v188, v117, v125
	v_cvt_pk_bf16_f32 v189, v137, v145
	v_cvt_pk_bf16_f32 v190, v153, v161
	v_cvt_pk_bf16_f32 v191, v169, v177
	global_store_dwordx4 v[184:185], v[180:183], off nt
	global_store_dwordx4 v[184:185], v[188:191], off offset:16 nt
	v_lshl_add_u64 v[52:53], v[128:129], 0, v[10:11]
	v_cvt_pk_bf16_f32 v180, v54, v62
	v_cvt_pk_bf16_f32 v181, v70, v78
	v_cvt_pk_bf16_f32 v182, v86, v94
	v_cvt_pk_bf16_f32 v183, v102, v110
	v_cvt_pk_bf16_f32 v188, v118, v126
	v_cvt_pk_bf16_f32 v189, v138, v146
	v_cvt_pk_bf16_f32 v190, v154, v162
	v_cvt_pk_bf16_f32 v191, v170, v178
	global_store_dwordx4 v[52:53], v[180:183], off nt
	global_store_dwordx4 v[52:53], v[188:191], off offset:16 nt
	v_lshl_add_u64 v[68:69], v[128:129], 0, v[12:13]
	v_cvt_pk_bf16_f32 v52, v55, v63
	v_cvt_pk_bf16_f32 v53, v71, v79
	v_cvt_pk_bf16_f32 v54, v87, v95
	v_cvt_pk_bf16_f32 v55, v103, v111
	v_cvt_pk_bf16_f32 v60, v119, v127
	v_cvt_pk_bf16_f32 v61, v139, v147
	v_cvt_pk_bf16_f32 v62, v155, v163
	v_cvt_pk_bf16_f32 v63, v171, v179
	global_store_dwordx4 v[68:69], v[52:55], off nt
	global_store_dwordx4 v[68:69], v[60:63], off offset:16 nt
	global_load_dwordx4 v[52:55], v[16:17], off offset:1792 nt
	s_nop 0
	global_load_dwordx4 v[60:63], v[18:19], off offset:1792 nt
	global_load_dwordx4 v[68:71], v[20:21], off offset:1792 nt
	global_load_dwordx4 v[76:79], v[22:23], off offset:1792 nt
	global_load_dwordx4 v[84:87], v[24:25], off offset:1792 nt
	global_load_dwordx4 v[92:95], v[26:27], off offset:1792 nt
	global_load_dwordx4 v[100:103], v[28:29], off offset:1792 nt
	global_load_dwordx4 v[108:111], v[30:31], off offset:1792 nt
	global_load_dwordx4 v[116:119], v[32:33], off offset:1792 nt
	global_load_dwordx4 v[124:127], v[34:35], off offset:1792 nt
	global_load_dwordx4 v[136:139], v[36:37], off offset:1792 nt
	global_load_dwordx4 v[144:147], v[38:39], off offset:1792 nt
	global_load_dwordx4 v[152:155], v[40:41], off offset:1792 nt
	global_load_dwordx4 v[160:163], v[42:43], off offset:1792 nt
	global_load_dwordx4 v[168:171], v[44:45], off offset:1792 nt
	global_load_dwordx4 v[176:179], v[46:47], off offset:1792 nt
	s_add_u32 s28, s18, s28
	s_addc_u32 s29, s19, 0
	v_lshl_add_u64 v[128:129], s[28:29], 0, v[4:5]
	v_lshl_add_u64 v[184:185], v[128:129], 0, v[6:7]
	s_waitcnt vmcnt(38)
; #define WTILE_LOAD(T, v) do { const float* s_ = (T).src + (size_t)(16 * kq) * (T).ldw + 4 * n4; \
;     _Pragma("unroll") for (int j = 0; j < 16; ++j) v[j] = __builtin_nontemporal_load((const f32x4*)(s_ + (size_t)j * (T).ldw)); } while (0)
; __device__ __forceinline__ void expert_copy_share(const ExpertCopy& X, unsigned* qhead, int lane) {
;     ...
;         for (int k = 0; k < GRP; k += 2) {
;             __builtin_amdgcn_sched_barrier(0);
;             WTILE_STORE(ta, va);
;             if (k + 2 < GRP) { ta.src = t0.src + 64 * (k + 2); ta.dst = t0.dst + (size_t)(w13 ? 256 * ((k + 2) >> 1) : 64 * (k + 2)) * D; WTILE_LOAD(ta, va); }
;             __builtin_amdgcn_sched_barrier(0);
;             WTILE_STORE(tb, vb);
;             if (k + 3 < GRP) { tb.src = t0.src + 64 * (k + 3); tb.dst = t0.dst + (size_t)(w13 ? 256 * ((k + 3) >> 1) + 64 : 64 * (k + 3)) * D; WTILE_LOAD(tb, vb); }
	v_cvt_pk_bf16_f32 v180, v48, v56
	s_waitcnt vmcnt(36)
	v_cvt_pk_bf16_f32 v181, v64, v72
	s_waitcnt vmcnt(34)
	v_cvt_pk_bf16_f32 v182, v80, v88
	s_waitcnt vmcnt(32)
	v_cvt_pk_bf16_f32 v183, v96, v104
	s_waitcnt vmcnt(30)
	v_cvt_pk_bf16_f32 v188, v112, v120
	s_waitcnt vmcnt(28)
	v_cvt_pk_bf16_f32 v189, v132, v140
	s_waitcnt vmcnt(26)
	v_cvt_pk_bf16_f32 v190, v148, v156
	s_waitcnt vmcnt(24)
	v_cvt_pk_bf16_f32 v191, v164, v172
	global_store_dwordx4 v[184:185], v[180:183], off nt
	global_store_dwordx4 v[184:185], v[188:191], off offset:16 nt
	v_lshl_add_u64 v[184:185], v[128:129], 0, v[8:9]
	v_cvt_pk_bf16_f32 v180, v49, v57
	v_cvt_pk_bf16_f32 v181, v65, v73
	v_cvt_pk_bf16_f32 v182, v81, v89
	v_cvt_pk_bf16_f32 v183, v97, v105
	v_cvt_pk_bf16_f32 v188, v113, v121
	v_cvt_pk_bf16_f32 v189, v133, v141
	v_cvt_pk_bf16_f32 v190, v149, v157
	v_cvt_pk_bf16_f32 v191, v165, v173
	global_store_dwordx4 v[184:185], v[180:183], off nt
	global_store_dwordx4 v[184:185], v[188:191], off offset:16 nt
	v_lshl_add_u64 v[48:49], v[128:129], 0, v[10:11]
	v_cvt_pk_bf16_f32 v180, v50, v58
	v_cvt_pk_bf16_f32 v181, v66, v74
	v_cvt_pk_bf16_f32 v182, v82, v90
	v_cvt_pk_bf16_f32 v183, v98, v106
	v_cvt_pk_bf16_f32 v188, v114, v122
	v_cvt_pk_bf16_f32 v189, v134, v142
	v_cvt_pk_bf16_f32 v190, v150, v158
	v_cvt_pk_bf16_f32 v191, v166, v174
	global_store_dwordx4 v[48:49], v[180:183], off nt
	global_store_dwordx4 v[48:49], v[188:191], off offset:16 nt
	v_lshl_add_u64 v[64:65], v[128:129], 0, v[12:13]
	v_cvt_pk_bf16_f32 v48, v51, v59
	v_cvt_pk_bf16_f32 v49, v67, v75
	v_cvt_pk_bf16_f32 v50, v83, v91
	v_cvt_pk_bf16_f32 v51, v99, v107
	v_cvt_pk_bf16_f32 v56, v115, v123
	v_cvt_pk_bf16_f32 v57, v135, v143
	v_cvt_pk_bf16_f32 v58, v151, v159
	v_cvt_pk_bf16_f32 v59, v167, v175
	global_store_dwordx4 v[64:65], v[48:51], off nt
	global_store_dwordx4 v[64:65], v[56:59], off offset:16 nt
	global_load_dwordx4 v[48:51], v[16:17], off offset:2048 nt
	s_nop 0
	global_load_dwordx4 v[56:59], v[18:19], off offset:2048 nt
	global_load_dwordx4 v[64:67], v[20:21], off offset:2048 nt
	global_load_dwordx4 v[72:75], v[22:23], off offset:2048 nt
	global_load_dwordx4 v[80:83], v[24:25], off offset:2048 nt
	global_load_dwordx4 v[88:91], v[26:27], off offset:2048 nt
	global_load_dwordx4 v[96:99], v[28:29], off offset:2048 nt
	global_load_dwordx4 v[104:107], v[30:31], off offset:2048 nt
	global_load_dwordx4 v[112:115], v[32:33], off offset:2048 nt
	global_load_dwordx4 v[120:123], v[34:35], off offset:2048 nt
	global_load_dwordx4 v[132:135], v[36:37], off offset:2048 nt
	global_load_dwordx4 v[140:143], v[38:39], off offset:2048 nt
	global_load_dwordx4 v[148:151], v[40:41], off offset:2048 nt
	global_load_dwordx4 v[156:159], v[42:43], off offset:2048 nt
	global_load_dwordx4 v[164:167], v[44:45], off offset:2048 nt
	global_load_dwordx4 v[172:175], v[46:47], off offset:2048 nt
	s_add_u32 s28, s18, s27
	s_addc_u32 s29, s19, 0
	v_lshl_add_u64 v[128:129], s[28:29], 0, v[4:5]
	v_lshl_add_u64 v[184:185], v[128:129], 0, v[6:7]
	s_waitcnt vmcnt(38)
	v_cvt_pk_bf16_f32 v180, v52, v60
	s_waitcnt vmcnt(36)
	v_cvt_pk_bf16_f32 v181, v68, v76
	s_waitcnt vmcnt(34)
	v_cvt_pk_bf16_f32 v182, v84, v92
	s_waitcnt vmcnt(32)
	v_cvt_pk_bf16_f32 v183, v100, v108
	s_waitcnt vmcnt(30)
	v_cvt_pk_bf16_f32 v188, v116, v124
	s_waitcnt vmcnt(28)
	v_cvt_pk_bf16_f32 v189, v136, v144
	s_waitcnt vmcnt(26)
	v_cvt_pk_bf16_f32 v190, v152, v160
	s_waitcnt vmcnt(24)
	v_cvt_pk_bf16_f32 v191, v168, v176
	global_store_dwordx4 v[184:185], v[180:183], off nt
	global_store_dwordx4 v[184:185], v[188:191], off offset:16 nt
	v_lshl_add_u64 v[184:185], v[128:129], 0, v[8:9]
	v_cvt_pk_bf16_f32 v180, v53, v61
	v_cvt_pk_bf16_f32 v181, v69, v77
	v_cvt_pk_bf16_f32 v182, v85, v93
	v_cvt_pk_bf16_f32 v183, v101, v109
	v_cvt_pk_bf16_f32 v188, v117, v125
	v_cvt_pk_bf16_f32 v189, v137, v145
	v_cvt_pk_bf16_f32 v190, v153, v161
	v_cvt_pk_bf16_f32 v191, v169, v177
	global_store_dwordx4 v[184:185], v[180:183], off nt
	global_store_dwordx4 v[184:185], v[188:191], off offset:16 nt
	v_lshl_add_u64 v[52:53], v[128:129], 0, v[10:11]
	v_cvt_pk_bf16_f32 v180, v54, v62
	v_cvt_pk_bf16_f32 v181, v70, v78
	v_cvt_pk_bf16_f32 v182, v86, v94
	v_cvt_pk_bf16_f32 v183, v102, v110
	v_cvt_pk_bf16_f32 v188, v118, v126
	v_cvt_pk_bf16_f32 v189, v138, v146
	v_cvt_pk_bf16_f32 v190, v154, v162
	v_cvt_pk_bf16_f32 v191, v170, v178
	global_store_dwordx4 v[52:53], v[180:183], off nt
	global_store_dwordx4 v[52:53], v[188:191], off offset:16 nt
	v_lshl_add_u64 v[68:69], v[128:129], 0, v[12:13]
	v_cvt_pk_bf16_f32 v52, v55, v63
	v_cvt_pk_bf16_f32 v53, v71, v79
	v_cvt_pk_bf16_f32 v54, v87, v95
	v_cvt_pk_bf16_f32 v55, v103, v111
	v_cvt_pk_bf16_f32 v60, v119, v127
	v_cvt_pk_bf16_f32 v61, v139, v147
	v_cvt_pk_bf16_f32 v62, v155, v163
	v_cvt_pk_bf16_f32 v63, v171, v179
	global_store_dwordx4 v[68:69], v[52:55], off nt
	global_store_dwordx4 v[68:69], v[60:63], off offset:16 nt
	global_load_dwordx4 v[52:55], v[16:17], off offset:2304 nt
	s_nop 0
	global_load_dwordx4 v[60:63], v[18:19], off offset:2304 nt
	global_load_dwordx4 v[68:71], v[20:21], off offset:2304 nt
	global_load_dwordx4 v[76:79], v[22:23], off offset:2304 nt
	global_load_dwordx4 v[84:87], v[24:25], off offset:2304 nt
	global_load_dwordx4 v[92:95], v[26:27], off offset:2304 nt
	global_load_dwordx4 v[100:103], v[28:29], off offset:2304 nt
	global_load_dwordx4 v[108:111], v[30:31], off offset:2304 nt
	global_load_dwordx4 v[116:119], v[32:33], off offset:2304 nt
	global_load_dwordx4 v[124:127], v[34:35], off offset:2304 nt
	global_load_dwordx4 v[136:139], v[36:37], off offset:2304 nt
	global_load_dwordx4 v[144:147], v[38:39], off offset:2304 nt
	global_load_dwordx4 v[152:155], v[40:41], off offset:2304 nt
	global_load_dwordx4 v[160:163], v[42:43], off offset:2304 nt
	global_load_dwordx4 v[168:171], v[44:45], off offset:2304 nt
	global_load_dwordx4 v[176:179], v[46:47], off offset:2304 nt
	s_add_u32 s26, s18, s26
	s_addc_u32 s27, s19, 0
	v_lshl_add_u64 v[128:129], s[26:27], 0, v[4:5]
	v_lshl_add_u64 v[184:185], v[128:129], 0, v[6:7]
	s_waitcnt vmcnt(38)
; #define WTILE_LOAD(T, v) do { const float* s_ = (T).src + (size_t)(16 * kq) * (T).ldw + 4 * n4; \
;     _Pragma("unroll") for (int j = 0; j < 16; ++j) v[j] = __builtin_nontemporal_load((const f32x4*)(s_ + (size_t)j * (T).ldw)); } while (0)
; __device__ __forceinline__ void expert_copy_share(const ExpertCopy& X, unsigned* qhead, int lane) {
;     ...
;         for (int k = 0; k < GRP; k += 2) {
;             __builtin_amdgcn_sched_barrier(0);
;             WTILE_STORE(ta, va);
;             if (k + 2 < GRP) { ta.src = t0.src + 64 * (k + 2); ta.dst = t0.dst + (size_t)(w13 ? 256 * ((k + 2) >> 1) : 64 * (k + 2)) * D; WTILE_LOAD(ta, va); }
;             __builtin_amdgcn_sched_barrier(0);
;             WTILE_STORE(tb, vb);
;             if (k + 3 < GRP) { tb.src = t0.src + 64 * (k + 3); tb.dst = t0.dst + (size_t)(w13 ? 256 * ((k + 3) >> 1) + 64 : 64 * (k + 3)) * D; WTILE_LOAD(tb, vb); }
	v_cvt_pk_bf16_f32 v180, v48, v56
	s_waitcnt vmcnt(36)
	v_cvt_pk_bf16_f32 v181, v64, v72
	s_waitcnt vmcnt(34)
	v_cvt_pk_bf16_f32 v182, v80, v88
	s_waitcnt vmcnt(32)
	v_cvt_pk_bf16_f32 v183, v96, v104
	s_waitcnt vmcnt(30)
	v_cvt_pk_bf16_f32 v188, v112, v120
	s_waitcnt vmcnt(28)
	v_cvt_pk_bf16_f32 v189, v132, v140
	s_waitcnt vmcnt(26)
	v_cvt_pk_bf16_f32 v190, v148, v156
	s_waitcnt vmcnt(24)
	v_cvt_pk_bf16_f32 v191, v164, v172
	global_store_dwordx4 v[184:185], v[180:183], off nt
	global_store_dwordx4 v[184:185], v[188:191], off offset:16 nt
	v_lshl_add_u64 v[184:185], v[128:129], 0, v[8:9]
	v_cvt_pk_bf16_f32 v180, v49, v57
	v_cvt_pk_bf16_f32 v181, v65, v73
	v_cvt_pk_bf16_f32 v182, v81, v89
	v_cvt_pk_bf16_f32 v183, v97, v105
	v_cvt_pk_bf16_f32 v188, v113, v121
	v_cvt_pk_bf16_f32 v189, v133, v141
	v_cvt_pk_bf16_f32 v190, v149, v157
	v_cvt_pk_bf16_f32 v191, v165, v173
	global_store_dwordx4 v[184:185], v[180:183], off nt
	global_store_dwordx4 v[184:185], v[188:191], off offset:16 nt
	v_lshl_add_u64 v[48:49], v[128:129], 0, v[10:11]
	v_cvt_pk_bf16_f32 v180, v50, v58
	v_cvt_pk_bf16_f32 v181, v66, v74
	v_cvt_pk_bf16_f32 v182, v82, v90
	v_cvt_pk_bf16_f32 v183, v98, v106
	v_cvt_pk_bf16_f32 v188, v114, v122
	v_cvt_pk_bf16_f32 v189, v134, v142
	v_cvt_pk_bf16_f32 v190, v150, v158
	v_cvt_pk_bf16_f32 v191, v166, v174
	global_store_dwordx4 v[48:49], v[180:183], off nt
	global_store_dwordx4 v[48:49], v[188:191], off offset:16 nt
	v_lshl_add_u64 v[64:65], v[128:129], 0, v[12:13]
	v_cvt_pk_bf16_f32 v48, v51, v59
	v_cvt_pk_bf16_f32 v49, v67, v75
	v_cvt_pk_bf16_f32 v50, v83, v91
	v_cvt_pk_bf16_f32 v51, v99, v107
	v_cvt_pk_bf16_f32 v56, v115, v123
	v_cvt_pk_bf16_f32 v57, v135, v143
	v_cvt_pk_bf16_f32 v58, v151, v159
	v_cvt_pk_bf16_f32 v59, v167, v175
	global_store_dwordx4 v[64:65], v[48:51], off nt
	global_store_dwordx4 v[64:65], v[56:59], off offset:16 nt
	global_load_dwordx4 v[48:51], v[16:17], off offset:2560 nt
	s_nop 0
	global_load_dwordx4 v[56:59], v[18:19], off offset:2560 nt
	global_load_dwordx4 v[64:67], v[20:21], off offset:2560 nt
	global_load_dwordx4 v[72:75], v[22:23], off offset:2560 nt
	global_load_dwordx4 v[80:83], v[24:25], off offset:2560 nt
	global_load_dwordx4 v[88:91], v[26:27], off offset:2560 nt
	global_load_dwordx4 v[96:99], v[28:29], off offset:2560 nt
	global_load_dwordx4 v[104:107], v[30:31], off offset:2560 nt
	global_load_dwordx4 v[112:115], v[32:33], off offset:2560 nt
	global_load_dwordx4 v[120:123], v[34:35], off offset:2560 nt
	global_load_dwordx4 v[132:135], v[36:37], off offset:2560 nt
	global_load_dwordx4 v[140:143], v[38:39], off offset:2560 nt
	global_load_dwordx4 v[148:151], v[40:41], off offset:2560 nt
	global_load_dwordx4 v[156:159], v[42:43], off offset:2560 nt
	global_load_dwordx4 v[164:167], v[44:45], off offset:2560 nt
	global_load_dwordx4 v[172:175], v[46:47], off offset:2560 nt
	s_add_u32 s26, s18, s25
	s_addc_u32 s27, s19, 0
	v_lshl_add_u64 v[128:129], s[26:27], 0, v[4:5]
	v_lshl_add_u64 v[184:185], v[128:129], 0, v[6:7]
	s_waitcnt vmcnt(38)
	v_cvt_pk_bf16_f32 v180, v52, v60
	s_waitcnt vmcnt(36)
	v_cvt_pk_bf16_f32 v181, v68, v76
	s_waitcnt vmcnt(34)
	v_cvt_pk_bf16_f32 v182, v84, v92
	s_waitcnt vmcnt(32)
	v_cvt_pk_bf16_f32 v183, v100, v108
	s_waitcnt vmcnt(30)
	v_cvt_pk_bf16_f32 v188, v116, v124
	s_waitcnt vmcnt(28)
	v_cvt_pk_bf16_f32 v189, v136, v144
	s_waitcnt vmcnt(26)
	v_cvt_pk_bf16_f32 v190, v152, v160
	s_waitcnt vmcnt(24)
	v_cvt_pk_bf16_f32 v191, v168, v176
	global_store_dwordx4 v[184:185], v[180:183], off nt
	global_store_dwordx4 v[184:185], v[188:191], off offset:16 nt
	v_lshl_add_u64 v[184:185], v[128:129], 0, v[8:9]
	v_cvt_pk_bf16_f32 v180, v53, v61
	v_cvt_pk_bf16_f32 v181, v69, v77
	v_cvt_pk_bf16_f32 v182, v85, v93
	v_cvt_pk_bf16_f32 v183, v101, v109
	v_cvt_pk_bf16_f32 v188, v117, v125
	v_cvt_pk_bf16_f32 v189, v137, v145
	v_cvt_pk_bf16_f32 v190, v153, v161
	v_cvt_pk_bf16_f32 v191, v169, v177
	global_store_dwordx4 v[184:185], v[180:183], off nt
	global_store_dwordx4 v[184:185], v[188:191], off offset:16 nt
	v_lshl_add_u64 v[52:53], v[128:129], 0, v[10:11]
	v_cvt_pk_bf16_f32 v180, v54, v62
	v_cvt_pk_bf16_f32 v181, v70, v78
	v_cvt_pk_bf16_f32 v182, v86, v94
	v_cvt_pk_bf16_f32 v183, v102, v110
	v_cvt_pk_bf16_f32 v188, v118, v126
	v_cvt_pk_bf16_f32 v189, v138, v146
	v_cvt_pk_bf16_f32 v190, v154, v162
	v_cvt_pk_bf16_f32 v191, v170, v178
	global_store_dwordx4 v[52:53], v[180:183], off nt
	global_store_dwordx4 v[52:53], v[188:191], off offset:16 nt
	v_lshl_add_u64 v[68:69], v[128:129], 0, v[12:13]
	v_cvt_pk_bf16_f32 v52, v55, v63
	v_cvt_pk_bf16_f32 v53, v71, v79
	v_cvt_pk_bf16_f32 v54, v87, v95
	v_cvt_pk_bf16_f32 v55, v103, v111
	v_cvt_pk_bf16_f32 v60, v119, v127
	v_cvt_pk_bf16_f32 v61, v139, v147
	v_cvt_pk_bf16_f32 v62, v155, v163
	v_cvt_pk_bf16_f32 v63, v171, v179
	global_store_dwordx4 v[68:69], v[52:55], off nt
	global_store_dwordx4 v[68:69], v[60:63], off offset:16 nt
	global_load_dwordx4 v[52:55], v[16:17], off offset:2816 nt
	s_nop 0
	global_load_dwordx4 v[60:63], v[18:19], off offset:2816 nt
	global_load_dwordx4 v[68:71], v[20:21], off offset:2816 nt
	global_load_dwordx4 v[76:79], v[22:23], off offset:2816 nt
	global_load_dwordx4 v[84:87], v[24:25], off offset:2816 nt
	global_load_dwordx4 v[92:95], v[26:27], off offset:2816 nt
	global_load_dwordx4 v[100:103], v[28:29], off offset:2816 nt
	global_load_dwordx4 v[108:111], v[30:31], off offset:2816 nt
	global_load_dwordx4 v[116:119], v[32:33], off offset:2816 nt
	global_load_dwordx4 v[124:127], v[34:35], off offset:2816 nt
	global_load_dwordx4 v[136:139], v[36:37], off offset:2816 nt
	global_load_dwordx4 v[144:147], v[38:39], off offset:2816 nt
	global_load_dwordx4 v[152:155], v[40:41], off offset:2816 nt
	global_load_dwordx4 v[160:163], v[42:43], off offset:2816 nt
	global_load_dwordx4 v[168:171], v[44:45], off offset:2816 nt
	global_load_dwordx4 v[176:179], v[46:47], off offset:2816 nt
	s_add_u32 s24, s18, s24
	s_addc_u32 s25, s19, 0
	v_lshl_add_u64 v[128:129], s[24:25], 0, v[4:5]
	v_lshl_add_u64 v[184:185], v[128:129], 0, v[6:7]
	s_waitcnt vmcnt(38)
; #define WTILE_LOAD(T, v) do { const float* s_ = (T).src + (size_t)(16 * kq) * (T).ldw + 4 * n4; \
;     _Pragma("unroll") for (int j = 0; j < 16; ++j) v[j] = __builtin_nontemporal_load((const f32x4*)(s_ + (size_t)j * (T).ldw)); } while (0)
; __device__ __forceinline__ void expert_copy_share(const ExpertCopy& X, unsigned* qhead, int lane) {
;     ...
;         for (int k = 0; k < GRP; k += 2) {
;             __builtin_amdgcn_sched_barrier(0);
;             WTILE_STORE(ta, va);
;             if (k + 2 < GRP) { ta.src = t0.src + 64 * (k + 2); ta.dst = t0.dst + (size_t)(w13 ? 256 * ((k + 2) >> 1) : 64 * (k + 2)) * D; WTILE_LOAD(ta, va); }
;             __builtin_amdgcn_sched_barrier(0);
;             WTILE_STORE(tb, vb);
;             if (k + 3 < GRP) { tb.src = t0.src + 64 * (k + 3); tb.dst = t0.dst + (size_t)(w13 ? 256 * ((k + 3) >> 1) + 64 : 64 * (k + 3)) * D; WTILE_LOAD(tb, vb); }
	v_cvt_pk_bf16_f32 v180, v48, v56
	s_waitcnt vmcnt(36)
	v_cvt_pk_bf16_f32 v181, v64, v72
	s_waitcnt vmcnt(34)
	v_cvt_pk_bf16_f32 v182, v80, v88
	s_waitcnt vmcnt(32)
	v_cvt_pk_bf16_f32 v183, v96, v104
	s_waitcnt vmcnt(30)
	v_cvt_pk_bf16_f32 v188, v112, v120
	s_waitcnt vmcnt(28)
	v_cvt_pk_bf16_f32 v189, v132, v140
	s_waitcnt vmcnt(26)
	v_cvt_pk_bf16_f32 v190, v148, v156
	s_waitcnt vmcnt(24)
	v_cvt_pk_bf16_f32 v191, v164, v172
	global_store_dwordx4 v[184:185], v[180:183], off nt
	global_store_dwordx4 v[184:185], v[188:191], off offset:16 nt
	v_lshl_add_u64 v[184:185], v[128:129], 0, v[8:9]
	v_cvt_pk_bf16_f32 v180, v49, v57
	v_cvt_pk_bf16_f32 v181, v65, v73
	v_cvt_pk_bf16_f32 v182, v81, v89
	v_cvt_pk_bf16_f32 v183, v97, v105
	v_cvt_pk_bf16_f32 v188, v113, v121
	v_cvt_pk_bf16_f32 v189, v133, v141
	v_cvt_pk_bf16_f32 v190, v149, v157
	v_cvt_pk_bf16_f32 v191, v165, v173
	global_store_dwordx4 v[184:185], v[180:183], off nt
	global_store_dwordx4 v[184:185], v[188:191], off offset:16 nt
	v_lshl_add_u64 v[48:49], v[128:129], 0, v[10:11]
	v_cvt_pk_bf16_f32 v180, v50, v58
	v_cvt_pk_bf16_f32 v181, v66, v74
	v_cvt_pk_bf16_f32 v182, v82, v90
	v_cvt_pk_bf16_f32 v183, v98, v106
	v_cvt_pk_bf16_f32 v188, v114, v122
	v_cvt_pk_bf16_f32 v189, v134, v142
	v_cvt_pk_bf16_f32 v190, v150, v158
	v_cvt_pk_bf16_f32 v191, v166, v174
	global_store_dwordx4 v[48:49], v[180:183], off nt
	global_store_dwordx4 v[48:49], v[188:191], off offset:16 nt
	v_lshl_add_u64 v[64:65], v[128:129], 0, v[12:13]
	v_cvt_pk_bf16_f32 v48, v51, v59
	v_cvt_pk_bf16_f32 v49, v67, v75
	v_cvt_pk_bf16_f32 v50, v83, v91
	v_cvt_pk_bf16_f32 v51, v99, v107
	v_cvt_pk_bf16_f32 v56, v115, v123
	v_cvt_pk_bf16_f32 v57, v135, v143
	v_cvt_pk_bf16_f32 v58, v151, v159
	v_cvt_pk_bf16_f32 v59, v167, v175
	global_store_dwordx4 v[64:65], v[48:51], off nt
	global_store_dwordx4 v[64:65], v[56:59], off offset:16 nt
	global_load_dwordx4 v[48:51], v[16:17], off offset:3072 nt
	s_nop 0
	global_load_dwordx4 v[56:59], v[18:19], off offset:3072 nt
	global_load_dwordx4 v[64:67], v[20:21], off offset:3072 nt
	global_load_dwordx4 v[72:75], v[22:23], off offset:3072 nt
	global_load_dwordx4 v[80:83], v[24:25], off offset:3072 nt
	global_load_dwordx4 v[88:91], v[26:27], off offset:3072 nt
	global_load_dwordx4 v[96:99], v[28:29], off offset:3072 nt
	global_load_dwordx4 v[104:107], v[30:31], off offset:3072 nt
	global_load_dwordx4 v[112:115], v[32:33], off offset:3072 nt
	global_load_dwordx4 v[120:123], v[34:35], off offset:3072 nt
	global_load_dwordx4 v[132:135], v[36:37], off offset:3072 nt
	global_load_dwordx4 v[140:143], v[38:39], off offset:3072 nt
	global_load_dwordx4 v[148:151], v[40:41], off offset:3072 nt
	global_load_dwordx4 v[156:159], v[42:43], off offset:3072 nt
	global_load_dwordx4 v[164:167], v[44:45], off offset:3072 nt
	global_load_dwordx4 v[172:175], v[46:47], off offset:3072 nt
	s_add_u32 s24, s18, s23
	s_addc_u32 s25, s19, 0
	v_lshl_add_u64 v[128:129], s[24:25], 0, v[4:5]
	v_lshl_add_u64 v[184:185], v[128:129], 0, v[6:7]
	s_waitcnt vmcnt(38)
	v_cvt_pk_bf16_f32 v180, v52, v60
	s_waitcnt vmcnt(36)
	v_cvt_pk_bf16_f32 v181, v68, v76
	s_waitcnt vmcnt(34)
	v_cvt_pk_bf16_f32 v182, v84, v92
	s_waitcnt vmcnt(32)
	v_cvt_pk_bf16_f32 v183, v100, v108
	s_waitcnt vmcnt(30)
	v_cvt_pk_bf16_f32 v188, v116, v124
	s_waitcnt vmcnt(28)
	v_cvt_pk_bf16_f32 v189, v136, v144
	s_waitcnt vmcnt(26)
	v_cvt_pk_bf16_f32 v190, v152, v160
	s_waitcnt vmcnt(24)
	v_cvt_pk_bf16_f32 v191, v168, v176
	global_store_dwordx4 v[184:185], v[180:183], off nt
	global_store_dwordx4 v[184:185], v[188:191], off offset:16 nt
	v_lshl_add_u64 v[184:185], v[128:129], 0, v[8:9]
	v_cvt_pk_bf16_f32 v180, v53, v61
	v_cvt_pk_bf16_f32 v181, v69, v77
	v_cvt_pk_bf16_f32 v182, v85, v93
	v_cvt_pk_bf16_f32 v183, v101, v109
	v_cvt_pk_bf16_f32 v188, v117, v125
	v_cvt_pk_bf16_f32 v189, v137, v145
	v_cvt_pk_bf16_f32 v190, v153, v161
	v_cvt_pk_bf16_f32 v191, v169, v177
	global_store_dwordx4 v[184:185], v[180:183], off nt
	global_store_dwordx4 v[184:185], v[188:191], off offset:16 nt
	v_lshl_add_u64 v[52:53], v[128:129], 0, v[10:11]
	v_cvt_pk_bf16_f32 v180, v54, v62
	v_cvt_pk_bf16_f32 v181, v70, v78
	v_cvt_pk_bf16_f32 v182, v86, v94
	v_cvt_pk_bf16_f32 v183, v102, v110
	v_cvt_pk_bf16_f32 v188, v118, v126
	v_cvt_pk_bf16_f32 v189, v138, v146
	v_cvt_pk_bf16_f32 v190, v154, v162
	v_cvt_pk_bf16_f32 v191, v170, v178
	global_store_dwordx4 v[52:53], v[180:183], off nt
	global_store_dwordx4 v[52:53], v[188:191], off offset:16 nt
	v_lshl_add_u64 v[68:69], v[128:129], 0, v[12:13]
	v_cvt_pk_bf16_f32 v52, v55, v63
	v_cvt_pk_bf16_f32 v53, v71, v79
	v_cvt_pk_bf16_f32 v54, v87, v95
	v_cvt_pk_bf16_f32 v55, v103, v111
	v_cvt_pk_bf16_f32 v60, v119, v127
	v_cvt_pk_bf16_f32 v61, v139, v147
	v_cvt_pk_bf16_f32 v62, v155, v163
	v_cvt_pk_bf16_f32 v63, v171, v179
	global_store_dwordx4 v[68:69], v[52:55], off nt
	global_store_dwordx4 v[68:69], v[60:63], off offset:16 nt
	global_load_dwordx4 v[52:55], v[16:17], off offset:3328 nt
	s_nop 0
	global_load_dwordx4 v[60:63], v[18:19], off offset:3328 nt
	global_load_dwordx4 v[68:71], v[20:21], off offset:3328 nt
	global_load_dwordx4 v[76:79], v[22:23], off offset:3328 nt
	global_load_dwordx4 v[84:87], v[24:25], off offset:3328 nt
	global_load_dwordx4 v[92:95], v[26:27], off offset:3328 nt
	global_load_dwordx4 v[100:103], v[28:29], off offset:3328 nt
	global_load_dwordx4 v[108:111], v[30:31], off offset:3328 nt
	global_load_dwordx4 v[116:119], v[32:33], off offset:3328 nt
	global_load_dwordx4 v[124:127], v[34:35], off offset:3328 nt
	global_load_dwordx4 v[136:139], v[36:37], off offset:3328 nt
	global_load_dwordx4 v[144:147], v[38:39], off offset:3328 nt
	global_load_dwordx4 v[152:155], v[40:41], off offset:3328 nt
	global_load_dwordx4 v[160:163], v[42:43], off offset:3328 nt
	global_load_dwordx4 v[168:171], v[44:45], off offset:3328 nt
	global_load_dwordx4 v[176:179], v[46:47], off offset:3328 nt
	s_add_u32 s22, s18, s22
	s_addc_u32 s23, s19, 0
	v_lshl_add_u64 v[128:129], s[22:23], 0, v[4:5]
	v_lshl_add_u64 v[184:185], v[128:129], 0, v[6:7]
	s_waitcnt vmcnt(38)
; #define WTILE_LOAD(T, v) do { const float* s_ = (T).src + (size_t)(16 * kq) * (T).ldw + 4 * n4; \
;     _Pragma("unroll") for (int j = 0; j < 16; ++j) v[j] = __builtin_nontemporal_load((const f32x4*)(s_ + (size_t)j * (T).ldw)); } while (0)
; __device__ __forceinline__ void expert_copy_share(const ExpertCopy& X, unsigned* qhead, int lane) {
;     ...
;         for (int k = 0; k < GRP; k += 2) {
;             __builtin_amdgcn_sched_barrier(0);
;             WTILE_STORE(ta, va);
;             if (k + 2 < GRP) { ta.src = t0.src + 64 * (k + 2); ta.dst = t0.dst + (size_t)(w13 ? 256 * ((k + 2) >> 1) : 64 * (k + 2)) * D; WTILE_LOAD(ta, va); }
;             __builtin_amdgcn_sched_barrier(0);
;             WTILE_STORE(tb, vb);
;             if (k + 3 < GRP) { tb.src = t0.src + 64 * (k + 3); tb.dst = t0.dst + (size_t)(w13 ? 256 * ((k + 3) >> 1) + 64 : 64 * (k + 3)) * D; WTILE_LOAD(tb, vb); }
	v_cvt_pk_bf16_f32 v180, v48, v56
	s_waitcnt vmcnt(36)
	v_cvt_pk_bf16_f32 v181, v64, v72
	s_waitcnt vmcnt(34)
	v_cvt_pk_bf16_f32 v182, v80, v88
	s_waitcnt vmcnt(32)
	v_cvt_pk_bf16_f32 v183, v96, v104
	s_waitcnt vmcnt(30)
	v_cvt_pk_bf16_f32 v188, v112, v120
	s_waitcnt vmcnt(28)
	v_cvt_pk_bf16_f32 v189, v132, v140
	s_waitcnt vmcnt(26)
	v_cvt_pk_bf16_f32 v190, v148, v156
	s_waitcnt vmcnt(24)
	v_cvt_pk_bf16_f32 v191, v164, v172
	global_store_dwordx4 v[184:185], v[180:183], off nt
	global_store_dwordx4 v[184:185], v[188:191], off offset:16 nt
	v_lshl_add_u64 v[184:185], v[128:129], 0, v[8:9]
	v_cvt_pk_bf16_f32 v180, v49, v57
	v_cvt_pk_bf16_f32 v181, v65, v73
	v_cvt_pk_bf16_f32 v182, v81, v89
	v_cvt_pk_bf16_f32 v183, v97, v105
	v_cvt_pk_bf16_f32 v188, v113, v121
	v_cvt_pk_bf16_f32 v189, v133, v141
	v_cvt_pk_bf16_f32 v190, v149, v157
	v_cvt_pk_bf16_f32 v191, v165, v173
	global_store_dwordx4 v[184:185], v[180:183], off nt
	global_store_dwordx4 v[184:185], v[188:191], off offset:16 nt
	v_lshl_add_u64 v[48:49], v[128:129], 0, v[10:11]
	v_cvt_pk_bf16_f32 v180, v50, v58
	v_cvt_pk_bf16_f32 v181, v66, v74
	v_cvt_pk_bf16_f32 v182, v82, v90
	v_cvt_pk_bf16_f32 v183, v98, v106
	v_cvt_pk_bf16_f32 v188, v114, v122
	v_cvt_pk_bf16_f32 v189, v134, v142
	v_cvt_pk_bf16_f32 v190, v150, v158
	v_cvt_pk_bf16_f32 v191, v166, v174
	global_store_dwordx4 v[48:49], v[180:183], off nt
	global_store_dwordx4 v[48:49], v[188:191], off offset:16 nt
	v_lshl_add_u64 v[64:65], v[128:129], 0, v[12:13]
	v_cvt_pk_bf16_f32 v48, v51, v59
	v_cvt_pk_bf16_f32 v49, v67, v75
	v_cvt_pk_bf16_f32 v50, v83, v91
	v_cvt_pk_bf16_f32 v51, v99, v107
	v_cvt_pk_bf16_f32 v56, v115, v123
	v_cvt_pk_bf16_f32 v57, v135, v143
	v_cvt_pk_bf16_f32 v58, v151, v159
	v_cvt_pk_bf16_f32 v59, v167, v175
	global_store_dwordx4 v[64:65], v[48:51], off nt
	global_store_dwordx4 v[64:65], v[56:59], off offset:16 nt
	global_load_dwordx4 v[48:51], v[16:17], off offset:3584 nt
	s_nop 0
	global_load_dwordx4 v[56:59], v[18:19], off offset:3584 nt
	global_load_dwordx4 v[64:67], v[20:21], off offset:3584 nt
	global_load_dwordx4 v[72:75], v[22:23], off offset:3584 nt
	global_load_dwordx4 v[80:83], v[24:25], off offset:3584 nt
	global_load_dwordx4 v[88:91], v[26:27], off offset:3584 nt
	global_load_dwordx4 v[96:99], v[28:29], off offset:3584 nt
	global_load_dwordx4 v[104:107], v[30:31], off offset:3584 nt
	global_load_dwordx4 v[112:115], v[32:33], off offset:3584 nt
	global_load_dwordx4 v[120:123], v[34:35], off offset:3584 nt
	global_load_dwordx4 v[132:135], v[36:37], off offset:3584 nt
	global_load_dwordx4 v[140:143], v[38:39], off offset:3584 nt
	global_load_dwordx4 v[148:151], v[40:41], off offset:3584 nt
	global_load_dwordx4 v[156:159], v[42:43], off offset:3584 nt
	global_load_dwordx4 v[164:167], v[44:45], off offset:3584 nt
	global_load_dwordx4 v[172:175], v[46:47], off offset:3584 nt
	s_add_u32 s22, s18, s21
	s_addc_u32 s23, s19, 0
	v_lshl_add_u64 v[128:129], s[22:23], 0, v[4:5]
	v_lshl_add_u64 v[184:185], v[128:129], 0, v[6:7]
	s_waitcnt vmcnt(38)
	v_cvt_pk_bf16_f32 v180, v52, v60
	s_waitcnt vmcnt(36)
	v_cvt_pk_bf16_f32 v181, v68, v76
	s_waitcnt vmcnt(34)
	v_cvt_pk_bf16_f32 v182, v84, v92
	s_waitcnt vmcnt(32)
	v_cvt_pk_bf16_f32 v183, v100, v108
	s_waitcnt vmcnt(30)
	v_cvt_pk_bf16_f32 v188, v116, v124
	s_waitcnt vmcnt(28)
	v_cvt_pk_bf16_f32 v189, v136, v144
	s_waitcnt vmcnt(26)
	v_cvt_pk_bf16_f32 v190, v152, v160
	s_waitcnt vmcnt(24)
	v_cvt_pk_bf16_f32 v191, v168, v176
	global_store_dwordx4 v[184:185], v[180:183], off nt
	global_store_dwordx4 v[184:185], v[188:191], off offset:16 nt
	v_lshl_add_u64 v[184:185], v[128:129], 0, v[8:9]
	v_cvt_pk_bf16_f32 v180, v53, v61
	v_cvt_pk_bf16_f32 v181, v69, v77
	v_cvt_pk_bf16_f32 v182, v85, v93
	v_cvt_pk_bf16_f32 v183, v101, v109
	v_cvt_pk_bf16_f32 v188, v117, v125
	v_cvt_pk_bf16_f32 v189, v137, v145
	v_cvt_pk_bf16_f32 v190, v153, v161
	v_cvt_pk_bf16_f32 v191, v169, v177
	global_store_dwordx4 v[184:185], v[180:183], off nt
	global_store_dwordx4 v[184:185], v[188:191], off offset:16 nt
	v_lshl_add_u64 v[52:53], v[128:129], 0, v[10:11]
	v_cvt_pk_bf16_f32 v180, v54, v62
	v_cvt_pk_bf16_f32 v181, v70, v78
	v_cvt_pk_bf16_f32 v182, v86, v94
	v_cvt_pk_bf16_f32 v183, v102, v110
	v_cvt_pk_bf16_f32 v188, v118, v126
	v_cvt_pk_bf16_f32 v189, v138, v146
	v_cvt_pk_bf16_f32 v190, v154, v162
	v_cvt_pk_bf16_f32 v191, v170, v178
	global_store_dwordx4 v[52:53], v[180:183], off nt
	global_store_dwordx4 v[52:53], v[188:191], off offset:16 nt
	v_lshl_add_u64 v[68:69], v[128:129], 0, v[12:13]
	v_cvt_pk_bf16_f32 v52, v55, v63
	v_cvt_pk_bf16_f32 v53, v71, v79
	v_cvt_pk_bf16_f32 v54, v87, v95
	v_cvt_pk_bf16_f32 v55, v103, v111
	v_cvt_pk_bf16_f32 v60, v119, v127
	v_cvt_pk_bf16_f32 v61, v139, v147
	v_cvt_pk_bf16_f32 v62, v155, v163
	v_cvt_pk_bf16_f32 v63, v171, v179
	global_store_dwordx4 v[68:69], v[52:55], off nt
	global_store_dwordx4 v[68:69], v[60:63], off offset:16 nt
	global_load_dwordx4 v[52:55], v[16:17], off offset:3840 nt
	s_nop 0
	global_load_dwordx4 v[16:19], v[18:19], off offset:3840 nt
	s_nop 0
	global_load_dwordx4 v[60:63], v[20:21], off offset:3840 nt
	s_nop 0
	global_load_dwordx4 v[20:23], v[22:23], off offset:3840 nt
	s_nop 0
	global_load_dwordx4 v[68:71], v[24:25], off offset:3840 nt
	s_nop 0
	global_load_dwordx4 v[24:27], v[26:27], off offset:3840 nt
	s_nop 0
	global_load_dwordx4 v[76:79], v[28:29], off offset:3840 nt
	s_nop 0
	global_load_dwordx4 v[28:31], v[30:31], off offset:3840 nt
	s_nop 0
	global_load_dwordx4 v[84:87], v[32:33], off offset:3840 nt
	s_nop 0
	global_load_dwordx4 v[32:35], v[34:35], off offset:3840 nt
	s_nop 0
	global_load_dwordx4 v[92:95], v[36:37], off offset:3840 nt
	s_nop 0
	global_load_dwordx4 v[36:39], v[38:39], off offset:3840 nt
	s_nop 0
	global_load_dwordx4 v[100:103], v[40:41], off offset:3840 nt
	s_nop 0
	global_load_dwordx4 v[40:43], v[42:43], off offset:3840 nt
	s_nop 0
	global_load_dwordx4 v[108:111], v[44:45], off offset:3840 nt
	s_nop 0
	global_load_dwordx4 v[44:47], v[46:47], off offset:3840 nt
	s_add_u32 s20, s18, s20
	s_addc_u32 s21, s19, 0
	s_add_u32 s18, s18, s10
	s_addc_u32 s19, s19, 0
	v_lshl_add_u64 v[128:129], s[20:21], 0, v[4:5]
	v_lshl_add_u64 v[136:137], v[128:129], 0, v[6:7]
	s_waitcnt vmcnt(38)
; #define WTILE_LOAD(T, v) do { const float* s_ = (T).src + (size_t)(16 * kq) * (T).ldw + 4 * n4; \
;     _Pragma("unroll") for (int j = 0; j < 16; ++j) v[j] = __builtin_nontemporal_load((const f32x4*)(s_ + (size_t)j * (T).ldw)); } while (0)
; __device__ __forceinline__ void expert_copy_share(const ExpertCopy& X, unsigned* qhead, int lane) {
;     ...
;         for (int k = 0; k < GRP; k += 2) {
;             __builtin_amdgcn_sched_barrier(0);
;             WTILE_STORE(ta, va);
;             if (k + 2 < GRP) { ta.src = t0.src + 64 * (k + 2); ta.dst = t0.dst + (size_t)(w13 ? 256 * ((k + 2) >> 1) : 64 * (k + 2)) * D; WTILE_LOAD(ta, va); }
;             __builtin_amdgcn_sched_barrier(0);
;             WTILE_STORE(tb, vb);
;             if (k + 3 < GRP) { tb.src = t0.src + 64 * (k + 3); tb.dst = t0.dst + (size_t)(w13 ? 256 * ((k + 3) >> 1) + 64 : 64 * (k + 3)) * D; WTILE_LOAD(tb, vb); }
;         }
	v_cvt_pk_bf16_f32 v116, v48, v56
	s_waitcnt vmcnt(36)
	v_cvt_pk_bf16_f32 v117, v64, v72
	s_waitcnt vmcnt(34)
	v_cvt_pk_bf16_f32 v118, v80, v88
	s_waitcnt vmcnt(32)
	v_cvt_pk_bf16_f32 v119, v96, v104
	s_waitcnt vmcnt(30)
	v_cvt_pk_bf16_f32 v124, v112, v120
	s_waitcnt vmcnt(28)
	v_cvt_pk_bf16_f32 v125, v132, v140
	s_waitcnt vmcnt(26)
	v_cvt_pk_bf16_f32 v126, v148, v156
	s_waitcnt vmcnt(24)
	v_cvt_pk_bf16_f32 v127, v164, v172
	global_store_dwordx4 v[136:137], v[116:119], off nt
	global_store_dwordx4 v[136:137], v[124:127], off offset:16 nt
	v_lshl_add_u64 v[136:137], v[128:129], 0, v[8:9]
	v_cvt_pk_bf16_f32 v116, v49, v57
	v_cvt_pk_bf16_f32 v117, v65, v73
	v_cvt_pk_bf16_f32 v118, v81, v89
	v_cvt_pk_bf16_f32 v119, v97, v105
	v_cvt_pk_bf16_f32 v124, v113, v121
	v_cvt_pk_bf16_f32 v125, v133, v141
	v_cvt_pk_bf16_f32 v126, v149, v157
	v_cvt_pk_bf16_f32 v127, v165, v173
	global_store_dwordx4 v[136:137], v[116:119], off nt
	global_store_dwordx4 v[136:137], v[124:127], off offset:16 nt
	v_lshl_add_u64 v[48:49], v[128:129], 0, v[10:11]
	v_cvt_pk_bf16_f32 v116, v50, v58
	v_cvt_pk_bf16_f32 v117, v66, v74
	v_cvt_pk_bf16_f32 v118, v82, v90
	v_cvt_pk_bf16_f32 v119, v98, v106
	v_cvt_pk_bf16_f32 v124, v114, v122
	v_cvt_pk_bf16_f32 v125, v134, v142
	v_cvt_pk_bf16_f32 v126, v150, v158
	v_cvt_pk_bf16_f32 v127, v166, v174
	global_store_dwordx4 v[48:49], v[116:119], off nt
	global_store_dwordx4 v[48:49], v[124:127], off offset:16 nt
	v_lshl_add_u64 v[64:65], v[128:129], 0, v[12:13]
	v_cvt_pk_bf16_f32 v48, v51, v59
	v_cvt_pk_bf16_f32 v49, v67, v75
	v_cvt_pk_bf16_f32 v50, v83, v91
	v_cvt_pk_bf16_f32 v51, v99, v107
	v_cvt_pk_bf16_f32 v56, v115, v123
	v_cvt_pk_bf16_f32 v57, v135, v143
	v_cvt_pk_bf16_f32 v58, v151, v159
	v_cvt_pk_bf16_f32 v59, v167, v175
	global_store_dwordx4 v[64:65], v[48:51], off nt
	global_store_dwordx4 v[64:65], v[56:59], off offset:16 nt
	v_lshl_add_u64 v[64:65], s[18:19], 0, v[4:5]
	v_lshl_add_u64 v[66:67], v[64:65], 0, v[6:7]
	s_waitcnt vmcnt(22)
	v_cvt_pk_bf16_f32 v48, v52, v16
	s_waitcnt vmcnt(20)
	v_cvt_pk_bf16_f32 v49, v60, v20
	s_waitcnt vmcnt(18)
	v_cvt_pk_bf16_f32 v50, v68, v24
	s_waitcnt vmcnt(16)
	v_cvt_pk_bf16_f32 v51, v76, v28
	s_waitcnt vmcnt(14)
	v_cvt_pk_bf16_f32 v56, v84, v32
	s_waitcnt vmcnt(12)
	v_cvt_pk_bf16_f32 v57, v92, v36
	s_waitcnt vmcnt(10)
	v_cvt_pk_bf16_f32 v58, v100, v40
	s_waitcnt vmcnt(8)
	v_cvt_pk_bf16_f32 v59, v108, v44
	global_store_dwordx4 v[66:67], v[48:51], off nt
	global_store_dwordx4 v[66:67], v[56:59], off offset:16 nt
	v_lshl_add_u64 v[66:67], v[64:65], 0, v[8:9]
	v_cvt_pk_bf16_f32 v48, v53, v17
	v_cvt_pk_bf16_f32 v49, v61, v21
	v_cvt_pk_bf16_f32 v50, v69, v25
	v_cvt_pk_bf16_f32 v51, v77, v29
	v_cvt_pk_bf16_f32 v56, v85, v33
	v_cvt_pk_bf16_f32 v57, v93, v37
	v_cvt_pk_bf16_f32 v58, v101, v41
	v_cvt_pk_bf16_f32 v59, v109, v45
	global_store_dwordx4 v[66:67], v[48:51], off nt
	global_store_dwordx4 v[66:67], v[56:59], off offset:16 nt
	v_lshl_add_u64 v[16:17], v[64:65], 0, v[10:11]
	v_cvt_pk_bf16_f32 v48, v54, v18
	v_cvt_pk_bf16_f32 v49, v62, v22
	v_cvt_pk_bf16_f32 v50, v70, v26
	v_cvt_pk_bf16_f32 v51, v78, v30
	v_cvt_pk_bf16_f32 v56, v86, v34
	v_cvt_pk_bf16_f32 v57, v94, v38
	v_cvt_pk_bf16_f32 v58, v102, v42
	v_cvt_pk_bf16_f32 v59, v110, v46
	global_store_dwordx4 v[16:17], v[48:51], off nt
	global_store_dwordx4 v[16:17], v[56:59], off offset:16 nt
	v_lshl_add_u64 v[24:25], v[64:65], 0, v[12:13]
	v_cvt_pk_bf16_f32 v16, v55, v19
	v_cvt_pk_bf16_f32 v17, v63, v23
	v_cvt_pk_bf16_f32 v18, v71, v27
	v_cvt_pk_bf16_f32 v19, v79, v31
	s_mov_b64 s[18:19], 0
	v_cvt_pk_bf16_f32 v20, v87, v35
	v_cvt_pk_bf16_f32 v21, v95, v39
	v_cvt_pk_bf16_f32 v22, v103, v43
	v_cvt_pk_bf16_f32 v23, v111, v47
	global_store_dwordx4 v[24:25], v[16:19], off nt
	global_store_dwordx4 v[24:25], v[20:23], off offset:16 nt

; __device__ __forceinline__ float softplusf(float x) { return x > 20.f ? x : log1pf(expf(x)); }
;     __device__ __forceinline__ void operator()(const f32x4 (&acc)[2][2][4][2], const pg8::Unit& u, int wr, int wc, int fr, int fq_in) const {
;     ...
;         } else {
;             if (wc < 2) {
;                 const int col0 = wc * 32 + 8 * fq; const f32x4 b0 = *(const f32x4*)(dtb + col0), b1 = *(const f32x4*)(dtb + col0 + 4);
; #pragma unroll
;                 for (int ai = 0; ai < 2; ++ai)
; #pragma unroll
;                     for (int m = 0; m < 4; ++m) { float* rowp = DTS + (size_t)(row0 + ai * 128 + m * 16) * 64 + col0; f32x4 o0, o1;
; #pragma unroll
;                         for (int q = 0; q < 4; ++q) { o0[q] = softplusf(acc[ai][0][m][0][q] + b0[q]); o1[q] = softplusf(acc[ai][0][m][1][q] + b1[q]); }
;                         *(f32x4*)(rowp) = o0; *(f32x4*)(rowp + 4) = o1; }
;             }
.LBB0_357:
	s_or_b64 exec, exec, s[0:1]
	v_ashrrev_i32_e32 v179, 31, v178
	v_lshlrev_b64 v[150:151], 8, v[178:179]
	v_lshl_add_u64 v[150:151], s[38:39], 0, v[150:151]
	v_lshl_add_u64 v[150:151], v[146:147], 2, v[150:151]
	global_store_dwordx4 v[150:151], v[138:141], off nt
	global_store_dwordx4 v[150:151], v[142:145], off offset:16 nt
	s_nop 0
	v_add_f32_e32 v138, v118, v134
	v_cmp_nlt_f32_e32 vcc, s83, v138
	s_and_saveexec_b64 s[0:1], vcc
	s_cbranch_execz .LBB0_359
	v_mul_f32_e32 v139, 0x3fb8aa3b, v138
	v_rndne_f32_e32 v140, v139
	v_sub_f32_e32 v141, v139, v140
	v_fma_f32 v139, v138, s86, -v139
	v_fmac_f32_e32 v139, 0x32a5705f, v138
	v_add_f32_e32 v139, v141, v139
	v_cvt_i32_f32_e32 v140, v140
	v_exp_f32_e32 v139, v139
	v_cmp_ngt_f32_e32 vcc, s87, v138
	v_ldexp_f32 v139, v139, v140
	s_nop 0
	v_cndmask_b32_e32 v139, 0, v139, vcc
	v_cmp_nlt_f32_e32 vcc, s88, v138
	s_nop 1
	v_cndmask_b32_e32 v149, v217, v139, vcc
	v_add_f32_e32 v140, 1.0, v149
	v_add_f32_e32 v138, -1.0, v140
	v_sub_f32_e32 v139, v138, v140
	v_add_f32_e32 v139, 1.0, v139
	v_sub_f32_e32 v138, v149, v138
	v_add_f32_e32 v141, v138, v139
	v_frexp_mant_f32_e32 v142, v140
	v_cvt_f64_f32_e32 v[138:139], v140
	v_frexp_exp_i32_f64_e32 v138, v[138:139]
	v_cmp_gt_f32_e32 vcc, s90, v142
	s_nop 1
	v_subbrev_co_u32_e32 v150, vcc, 0, v138, vcc
	v_sub_u32_e32 v138, 0, v150
	v_ldexp_f32 v139, v140, v138
	v_add_f32_e32 v140, -1.0, v139
	v_add_f32_e32 v142, 1.0, v139
	v_ldexp_f32 v138, v141, v138
	v_add_f32_e32 v141, 1.0, v140
	v_add_f32_e32 v143, -1.0, v142
	v_sub_f32_e32 v141, v139, v141
	v_sub_f32_e32 v139, v139, v143
	v_add_f32_e32 v141, v138, v141
	v_add_f32_e32 v138, v138, v139
	v_add_f32_e32 v151, v142, v138
	v_rcp_f32_e32 v153, v151
	v_sub_f32_e32 v139, v142, v151
	v_add_f32_e32 v152, v138, v139
	v_add_f32_e32 v139, v140, v141
	v_mul_f32_e32 v155, v139, v153
	v_sub_f32_e32 v138, v140, v139
	v_mul_f32_e32 v140, v151, v155
	v_fma_f32 v142, v155, v151, -v140
	v_fmac_f32_e32 v142, v155, v152
	v_add_f32_e32 v154, v141, v138
	v_add_f32_e32 v138, v140, v142
	v_sub_f32_e32 v141, v139, v138
	v_pk_add_f32 v[144:145], v[138:139], v[140:141] neg_lo:[0,1] neg_hi:[0,1]
	v_mov_b32_e32 v143, v138
	v_pk_add_f32 v[138:139], v[144:145], v[142:143] neg_lo:[0,1] neg_hi:[0,1]
	v_cmp_neq_f32_e32 vcc, s89, v149
	v_add_f32_e32 v139, v154, v139
	v_add_f32_e32 v138, v138, v139
	v_add_f32_e32 v139, v141, v138
	v_mul_f32_e32 v154, v153, v139
	v_mul_f32_e32 v140, v151, v154
	v_fma_f32 v142, v154, v151, -v140
	v_fmac_f32_e32 v142, v154, v152
	v_sub_f32_e32 v141, v141, v139
	v_add_f32_e32 v151, v138, v141
	v_add_f32_e32 v138, v140, v142
	v_sub_f32_e32 v141, v139, v138
	v_pk_add_f32 v[144:145], v[138:139], v[140:141] neg_lo:[0,1] neg_hi:[0,1]
	v_mov_b32_e32 v143, v138
	v_pk_add_f32 v[138:139], v[144:145], v[142:143] neg_lo:[0,1] neg_hi:[0,1]
	s_nop 0
	v_add_f32_e32 v139, v151, v139
	v_add_f32_e32 v138, v138, v139
	v_add_f32_e32 v139, v155, v154
	v_add_f32_e32 v138, v141, v138
	v_sub_f32_e32 v140, v139, v155
	v_mul_f32_e32 v138, v153, v138
	v_sub_f32_e32 v140, v154, v140
	v_add_f32_e32 v140, v140, v138
	v_add_f32_e32 v142, v139, v140
	v_mul_f32_e32 v143, v142, v142
	v_fmamk_f32 v138, v143, 0x3e9b6dac, v216
	v_fmaak_f32 v177, v143, v138, 0x3f2aaada
	v_cvt_f32_i32_e32 v138, v150
	v_sub_f32_e32 v139, v142, v139
	v_sub_f32_e32 v139, v140, v139
	v_ldexp_f32 v144, v139, 1
	v_mul_f32_e32 v139, v142, v143
	v_ldexp_f32 v141, v142, 1
	v_pk_mul_f32 v[142:143], v[138:139], v[176:177]
	s_nop 0
	v_fma_f32 v140, v138, s91, -v142
	v_fmac_f32_e32 v140, 0xb102e308, v138
	v_pk_add_f32 v[138:139], v[142:143], v[140:141]
	s_nop 0
	v_sub_f32_e32 v141, v139, v141
	v_sub_f32_e32 v141, v143, v141
	v_add_f32_e32 v145, v144, v141
	v_mov_b32_e32 v144, v142
	v_pk_add_f32 v[142:143], v[138:139], v[142:143] neg_lo:[0,1] neg_hi:[0,1]
	v_pk_add_f32 v[150:151], v[138:139], v[144:145]
	v_mov_b32_e32 v141, v138
	v_mov_b32_e32 v143, v151
	v_pk_add_f32 v[152:153], v[140:141], v[142:143] neg_lo:[0,1] neg_hi:[0,1]
	v_pk_add_f32 v[140:141], v[140:141], v[142:143]
	v_mov_b32_e32 v144, v145
	v_pk_add_f32 v[142:143], v[140:141], v[138:139] op_sel:[1,0] op_sel_hi:[0,1] neg_lo:[0,1] neg_hi:[0,1]
	v_pk_add_f32 v[154:155], v[150:151], v[142:143] op_sel_hi:[1,0] neg_lo:[0,1] neg_hi:[0,1]
	v_mov_b32_e32 v150, v151
	v_mov_b32_e32 v151, v141
	v_pk_mov_b32 v[142:143], v[138:139], v[142:143] op_sel:[1,0]
	v_mov_b32_e32 v145, v138
	v_pk_add_f32 v[142:143], v[150:151], v[142:143] neg_lo:[0,1] neg_hi:[0,1]
	v_mov_b32_e32 v154, v152
	v_pk_add_f32 v[138:139], v[144:145], v[142:143] neg_lo:[0,1] neg_hi:[0,1]
	v_mov_b32_e32 v153, v141
	v_pk_add_f32 v[142:143], v[154:155], v[138:139]
	s_nop 0
	v_pk_add_f32 v[144:145], v[142:143], v[142:143] op_sel:[0,1] op_sel_hi:[1,0]
	s_nop 0
	v_pk_add_f32 v[140:141], v[140:141], v[144:145] op_sel:[1,0] op_sel_hi:[0,1]
	v_mov_b32_e32 v143, v140
	v_pk_add_f32 v[150:151], v[142:143], v[152:153] neg_lo:[0,1] neg_hi:[0,1]
	v_mov_b32_e32 v139, v144
	v_sub_f32_e32 v141, v142, v150
	v_pk_add_f32 v[138:139], v[138:139], v[150:151] neg_lo:[0,1] neg_hi:[0,1]
	v_sub_f32_e32 v141, v152, v141
	v_add_f32_e32 v138, v138, v141
	v_add_f32_e32 v138, v138, v139
	v_add_f32_e32 v138, v140, v138
	v_cndmask_b32_e32 v138, v217, v138, vcc
	v_cmp_lt_f32_e64 vcc, |v149|, s92
	s_nop 1
	v_cndmask_b32_e32 v138, v138, v149, vcc

; __device__ __forceinline__ float softplusf(float x) { return x > 20.f ? x : log1pf(expf(x)); }
;     __device__ __forceinline__ void operator()(const f32x4 (&acc)[2][2][4][2], const pg8::Unit& u, int wr, int wc, int fr, int fq_in) const {
;     ...
;         } else {
;             if (wc < 2) {
;                 const int col0 = wc * 32 + 8 * fq; const f32x4 b0 = *(const f32x4*)(dtb + col0), b1 = *(const f32x4*)(dtb + col0 + 4);
; #pragma unroll
;                 for (int ai = 0; ai < 2; ++ai)
; #pragma unroll
;                     for (int m = 0; m < 4; ++m) { float* rowp = DTS + (size_t)(row0 + ai * 128 + m * 16) * 64 + col0; f32x4 o0, o1;
; #pragma unroll
;                         for (int q = 0; q < 4; ++q) { o0[q] = softplusf(acc[ai][0][m][0][q] + b0[q]); o1[q] = softplusf(acc[ai][0][m][1][q] + b1[q]); }
;                         *(f32x4*)(rowp) = o0; *(f32x4*)(rowp + 4) = o1; }
;             }
.LBB0_373:
	s_or_b64 exec, exec, s[0:1]
	v_or_b32_e32 v150, 16, v178
	v_ashrrev_i32_e32 v151, 31, v150
	v_lshlrev_b64 v[150:151], 8, v[150:151]
	v_lshl_add_u64 v[150:151], s[38:39], 0, v[150:151]
	v_lshl_add_u64 v[150:151], v[146:147], 2, v[150:151]
	global_store_dwordx4 v[150:151], v[138:141], off nt
	global_store_dwordx4 v[150:151], v[142:145], off offset:16 nt
	s_nop 0
	v_add_f32_e32 v138, v102, v134
	v_cmp_nlt_f32_e32 vcc, s83, v138
	s_and_saveexec_b64 s[0:1], vcc
	s_cbranch_execz .LBB0_375
	v_mul_f32_e32 v139, 0x3fb8aa3b, v138
	v_rndne_f32_e32 v140, v139
	v_sub_f32_e32 v141, v139, v140
	v_fma_f32 v139, v138, s86, -v139
	v_fmac_f32_e32 v139, 0x32a5705f, v138
	v_add_f32_e32 v139, v141, v139
	v_cvt_i32_f32_e32 v140, v140
	v_exp_f32_e32 v139, v139
	v_cmp_ngt_f32_e32 vcc, s87, v138
	v_ldexp_f32 v139, v139, v140
	s_nop 0
	v_cndmask_b32_e32 v139, 0, v139, vcc
	v_cmp_nlt_f32_e32 vcc, s88, v138
	s_nop 1
	v_cndmask_b32_e32 v149, v217, v139, vcc
	v_add_f32_e32 v140, 1.0, v149
	v_add_f32_e32 v138, -1.0, v140
	v_sub_f32_e32 v139, v138, v140
	v_add_f32_e32 v139, 1.0, v139
	v_sub_f32_e32 v138, v149, v138
	v_add_f32_e32 v141, v138, v139
	v_frexp_mant_f32_e32 v142, v140
	v_cvt_f64_f32_e32 v[138:139], v140
	v_frexp_exp_i32_f64_e32 v138, v[138:139]
	v_cmp_gt_f32_e32 vcc, s90, v142
	s_nop 1
	v_subbrev_co_u32_e32 v150, vcc, 0, v138, vcc
	v_sub_u32_e32 v138, 0, v150
	v_ldexp_f32 v139, v140, v138
	v_add_f32_e32 v140, -1.0, v139
	v_add_f32_e32 v142, 1.0, v139
	v_ldexp_f32 v138, v141, v138
	v_add_f32_e32 v141, 1.0, v140
	v_add_f32_e32 v143, -1.0, v142
	v_sub_f32_e32 v141, v139, v141
	v_sub_f32_e32 v139, v139, v143
	v_add_f32_e32 v141, v138, v141
	v_add_f32_e32 v138, v138, v139
	v_add_f32_e32 v151, v142, v138
	v_rcp_f32_e32 v153, v151
	v_sub_f32_e32 v139, v142, v151
	v_add_f32_e32 v152, v138, v139
	v_add_f32_e32 v139, v140, v141
	v_mul_f32_e32 v155, v139, v153
	v_sub_f32_e32 v138, v140, v139
	v_mul_f32_e32 v140, v151, v155
	v_fma_f32 v142, v155, v151, -v140
	v_fmac_f32_e32 v142, v155, v152
	v_add_f32_e32 v154, v141, v138
	v_add_f32_e32 v138, v140, v142
	v_sub_f32_e32 v141, v139, v138
	v_pk_add_f32 v[144:145], v[138:139], v[140:141] neg_lo:[0,1] neg_hi:[0,1]
	v_mov_b32_e32 v143, v138
	v_pk_add_f32 v[138:139], v[144:145], v[142:143] neg_lo:[0,1] neg_hi:[0,1]
	v_cmp_neq_f32_e32 vcc, s89, v149
	v_add_f32_e32 v139, v154, v139
	v_add_f32_e32 v138, v138, v139
	v_add_f32_e32 v139, v141, v138
	v_mul_f32_e32 v154, v153, v139
	v_mul_f32_e32 v140, v151, v154
	v_fma_f32 v142, v154, v151, -v140
	v_fmac_f32_e32 v142, v154, v152
	v_sub_f32_e32 v141, v141, v139
	v_add_f32_e32 v151, v138, v141
	v_add_f32_e32 v138, v140, v142
	v_sub_f32_e32 v141, v139, v138
	v_pk_add_f32 v[144:145], v[138:139], v[140:141] neg_lo:[0,1] neg_hi:[0,1]
	v_mov_b32_e32 v143, v138
	v_pk_add_f32 v[138:139], v[144:145], v[142:143] neg_lo:[0,1] neg_hi:[0,1]
	s_nop 0
	v_add_f32_e32 v139, v151, v139
	v_add_f32_e32 v138, v138, v139
	v_add_f32_e32 v139, v155, v154
	v_add_f32_e32 v138, v141, v138
	v_sub_f32_e32 v140, v139, v155
	v_mul_f32_e32 v138, v153, v138
	v_sub_f32_e32 v140, v154, v140
	v_add_f32_e32 v140, v140, v138
	v_add_f32_e32 v142, v139, v140
	v_mul_f32_e32 v143, v142, v142
	v_fmamk_f32 v138, v143, 0x3e9b6dac, v216
	v_fmaak_f32 v177, v143, v138, 0x3f2aaada
	v_cvt_f32_i32_e32 v138, v150
	v_sub_f32_e32 v139, v142, v139
	v_sub_f32_e32 v139, v140, v139
	v_ldexp_f32 v144, v139, 1
	v_mul_f32_e32 v139, v142, v143
	v_ldexp_f32 v141, v142, 1
	v_pk_mul_f32 v[142:143], v[138:139], v[176:177]
	s_nop 0
	v_fma_f32 v140, v138, s91, -v142
	v_fmac_f32_e32 v140, 0xb102e308, v138
	v_pk_add_f32 v[138:139], v[142:143], v[140:141]
	s_nop 0
	v_sub_f32_e32 v141, v139, v141
	v_sub_f32_e32 v141, v143, v141
	v_add_f32_e32 v145, v144, v141
	v_mov_b32_e32 v144, v142
	v_pk_add_f32 v[142:143], v[138:139], v[142:143] neg_lo:[0,1] neg_hi:[0,1]
	v_pk_add_f32 v[150:151], v[138:139], v[144:145]
	v_mov_b32_e32 v141, v138
	v_mov_b32_e32 v143, v151
	v_pk_add_f32 v[152:153], v[140:141], v[142:143] neg_lo:[0,1] neg_hi:[0,1]
	v_pk_add_f32 v[140:141], v[140:141], v[142:143]
	v_mov_b32_e32 v144, v145
	v_pk_add_f32 v[142:143], v[140:141], v[138:139] op_sel:[1,0] op_sel_hi:[0,1] neg_lo:[0,1] neg_hi:[0,1]
	v_pk_add_f32 v[154:155], v[150:151], v[142:143] op_sel_hi:[1,0] neg_lo:[0,1] neg_hi:[0,1]
	v_mov_b32_e32 v150, v151
	v_mov_b32_e32 v151, v141
	v_pk_mov_b32 v[142:143], v[138:139], v[142:143] op_sel:[1,0]
	v_mov_b32_e32 v145, v138
	v_pk_add_f32 v[142:143], v[150:151], v[142:143] neg_lo:[0,1] neg_hi:[0,1]
	v_mov_b32_e32 v154, v152
	v_pk_add_f32 v[138:139], v[144:145], v[142:143] neg_lo:[0,1] neg_hi:[0,1]
	v_mov_b32_e32 v153, v141
	v_pk_add_f32 v[142:143], v[154:155], v[138:139]
	s_nop 0
	v_pk_add_f32 v[144:145], v[142:143], v[142:143] op_sel:[0,1] op_sel_hi:[1,0]
	s_nop 0
	v_pk_add_f32 v[140:141], v[140:141], v[144:145] op_sel:[1,0] op_sel_hi:[0,1]
	v_mov_b32_e32 v143, v140
	v_pk_add_f32 v[150:151], v[142:143], v[152:153] neg_lo:[0,1] neg_hi:[0,1]
	v_mov_b32_e32 v139, v144
	v_sub_f32_e32 v141, v142, v150
	v_pk_add_f32 v[138:139], v[138:139], v[150:151] neg_lo:[0,1] neg_hi:[0,1]
	v_sub_f32_e32 v141, v152, v141
	v_add_f32_e32 v138, v138, v141
	v_add_f32_e32 v138, v138, v139
	v_add_f32_e32 v138, v140, v138
	v_cndmask_b32_e32 v138, v217, v138, vcc
	v_cmp_lt_f32_e64 vcc, |v149|, s92
	s_nop 1
	v_cndmask_b32_e32 v138, v138, v149, vcc

; __device__ __forceinline__ float softplusf(float x) { return x > 20.f ? x : log1pf(expf(x)); }
;     __device__ __forceinline__ void operator()(const f32x4 (&acc)[2][2][4][2], const pg8::Unit& u, int wr, int wc, int fr, int fq_in) const {
;     ...
;         } else {
;             if (wc < 2) {
;                 const int col0 = wc * 32 + 8 * fq; const f32x4 b0 = *(const f32x4*)(dtb + col0), b1 = *(const f32x4*)(dtb + col0 + 4);
; #pragma unroll
;                 for (int ai = 0; ai < 2; ++ai)
; #pragma unroll
;                     for (int m = 0; m < 4; ++m) { float* rowp = DTS + (size_t)(row0 + ai * 128 + m * 16) * 64 + col0; f32x4 o0, o1;
; #pragma unroll
;                         for (int q = 0; q < 4; ++q) { o0[q] = softplusf(acc[ai][0][m][0][q] + b0[q]); o1[q] = softplusf(acc[ai][0][m][1][q] + b1[q]); }
;                         *(f32x4*)(rowp) = o0; *(f32x4*)(rowp + 4) = o1; }
;             }
.LBB0_389:
	s_or_b64 exec, exec, s[0:1]
	v_or_b32_e32 v150, 32, v178
	v_ashrrev_i32_e32 v151, 31, v150
	v_lshlrev_b64 v[150:151], 8, v[150:151]
	v_lshl_add_u64 v[150:151], s[38:39], 0, v[150:151]
	v_lshl_add_u64 v[150:151], v[146:147], 2, v[150:151]
	global_store_dwordx4 v[150:151], v[138:141], off nt
	global_store_dwordx4 v[150:151], v[142:145], off offset:16 nt
	s_nop 0
	v_add_f32_e32 v138, v86, v134
	v_cmp_nlt_f32_e32 vcc, s83, v138
	s_and_saveexec_b64 s[0:1], vcc
	s_cbranch_execz .LBB0_391
	v_mul_f32_e32 v139, 0x3fb8aa3b, v138
	v_rndne_f32_e32 v140, v139
	v_sub_f32_e32 v141, v139, v140
	v_fma_f32 v139, v138, s86, -v139
	v_fmac_f32_e32 v139, 0x32a5705f, v138
	v_add_f32_e32 v139, v141, v139
	v_cvt_i32_f32_e32 v140, v140
	v_exp_f32_e32 v139, v139
	v_cmp_ngt_f32_e32 vcc, s87, v138
	v_ldexp_f32 v139, v139, v140
	s_nop 0
	v_cndmask_b32_e32 v139, 0, v139, vcc
	v_cmp_nlt_f32_e32 vcc, s88, v138
	s_nop 1
	v_cndmask_b32_e32 v149, v217, v139, vcc
	v_add_f32_e32 v140, 1.0, v149
	v_add_f32_e32 v138, -1.0, v140
	v_sub_f32_e32 v139, v138, v140
	v_add_f32_e32 v139, 1.0, v139
	v_sub_f32_e32 v138, v149, v138
	v_add_f32_e32 v141, v138, v139
	v_frexp_mant_f32_e32 v142, v140
	v_cvt_f64_f32_e32 v[138:139], v140
	v_frexp_exp_i32_f64_e32 v138, v[138:139]
	v_cmp_gt_f32_e32 vcc, s90, v142
	s_nop 1
	v_subbrev_co_u32_e32 v150, vcc, 0, v138, vcc
	v_sub_u32_e32 v138, 0, v150
	v_ldexp_f32 v139, v140, v138
	v_add_f32_e32 v140, -1.0, v139
	v_add_f32_e32 v142, 1.0, v139
	v_ldexp_f32 v138, v141, v138
	v_add_f32_e32 v141, 1.0, v140
	v_add_f32_e32 v143, -1.0, v142
	v_sub_f32_e32 v141, v139, v141
	v_sub_f32_e32 v139, v139, v143
	v_add_f32_e32 v141, v138, v141
	v_add_f32_e32 v138, v138, v139
	v_add_f32_e32 v151, v142, v138
	v_rcp_f32_e32 v153, v151
	v_sub_f32_e32 v139, v142, v151
	v_add_f32_e32 v152, v138, v139
	v_add_f32_e32 v139, v140, v141
	v_mul_f32_e32 v155, v139, v153
	v_sub_f32_e32 v138, v140, v139
	v_mul_f32_e32 v140, v151, v155
	v_fma_f32 v142, v155, v151, -v140
	v_fmac_f32_e32 v142, v155, v152
	v_add_f32_e32 v154, v141, v138
	v_add_f32_e32 v138, v140, v142
	v_sub_f32_e32 v141, v139, v138
	v_pk_add_f32 v[144:145], v[138:139], v[140:141] neg_lo:[0,1] neg_hi:[0,1]
	v_mov_b32_e32 v143, v138
	v_pk_add_f32 v[138:139], v[144:145], v[142:143] neg_lo:[0,1] neg_hi:[0,1]
	v_cmp_neq_f32_e32 vcc, s89, v149
	v_add_f32_e32 v139, v154, v139
	v_add_f32_e32 v138, v138, v139
	v_add_f32_e32 v139, v141, v138
	v_mul_f32_e32 v154, v153, v139
	v_mul_f32_e32 v140, v151, v154
	v_fma_f32 v142, v154, v151, -v140
	v_fmac_f32_e32 v142, v154, v152
	v_sub_f32_e32 v141, v141, v139
	v_add_f32_e32 v151, v138, v141
	v_add_f32_e32 v138, v140, v142
	v_sub_f32_e32 v141, v139, v138
	v_pk_add_f32 v[144:145], v[138:139], v[140:141] neg_lo:[0,1] neg_hi:[0,1]
	v_mov_b32_e32 v143, v138
	v_pk_add_f32 v[138:139], v[144:145], v[142:143] neg_lo:[0,1] neg_hi:[0,1]
	s_nop 0
	v_add_f32_e32 v139, v151, v139
	v_add_f32_e32 v138, v138, v139
	v_add_f32_e32 v139, v155, v154
	v_add_f32_e32 v138, v141, v138
	v_sub_f32_e32 v140, v139, v155
	v_mul_f32_e32 v138, v153, v138
	v_sub_f32_e32 v140, v154, v140
	v_add_f32_e32 v140, v140, v138
	v_add_f32_e32 v142, v139, v140
	v_mul_f32_e32 v143, v142, v142
	v_fmamk_f32 v138, v143, 0x3e9b6dac, v216
	v_fmaak_f32 v177, v143, v138, 0x3f2aaada
	v_cvt_f32_i32_e32 v138, v150
	v_sub_f32_e32 v139, v142, v139
	v_sub_f32_e32 v139, v140, v139
	v_ldexp_f32 v144, v139, 1
	v_mul_f32_e32 v139, v142, v143
	v_ldexp_f32 v141, v142, 1
	v_pk_mul_f32 v[142:143], v[138:139], v[176:177]
	s_nop 0
	v_fma_f32 v140, v138, s91, -v142
	v_fmac_f32_e32 v140, 0xb102e308, v138
	v_pk_add_f32 v[138:139], v[142:143], v[140:141]
	s_nop 0
	v_sub_f32_e32 v141, v139, v141
	v_sub_f32_e32 v141, v143, v141
	v_add_f32_e32 v145, v144, v141
	v_mov_b32_e32 v144, v142
	v_pk_add_f32 v[142:143], v[138:139], v[142:143] neg_lo:[0,1] neg_hi:[0,1]
	v_pk_add_f32 v[150:151], v[138:139], v[144:145]
	v_mov_b32_e32 v141, v138
	v_mov_b32_e32 v143, v151
	v_pk_add_f32 v[152:153], v[140:141], v[142:143] neg_lo:[0,1] neg_hi:[0,1]
	v_pk_add_f32 v[140:141], v[140:141], v[142:143]
	v_mov_b32_e32 v144, v145
	v_pk_add_f32 v[142:143], v[140:141], v[138:139] op_sel:[1,0] op_sel_hi:[0,1] neg_lo:[0,1] neg_hi:[0,1]
	v_pk_add_f32 v[154:155], v[150:151], v[142:143] op_sel_hi:[1,0] neg_lo:[0,1] neg_hi:[0,1]
	v_mov_b32_e32 v150, v151
	v_mov_b32_e32 v151, v141
	v_pk_mov_b32 v[142:143], v[138:139], v[142:143] op_sel:[1,0]
	v_mov_b32_e32 v145, v138
	v_pk_add_f32 v[142:143], v[150:151], v[142:143] neg_lo:[0,1] neg_hi:[0,1]
	v_mov_b32_e32 v154, v152
	v_pk_add_f32 v[138:139], v[144:145], v[142:143] neg_lo:[0,1] neg_hi:[0,1]
	v_mov_b32_e32 v153, v141
	v_pk_add_f32 v[142:143], v[154:155], v[138:139]
	s_nop 0
	v_pk_add_f32 v[144:145], v[142:143], v[142:143] op_sel:[0,1] op_sel_hi:[1,0]
	s_nop 0
	v_pk_add_f32 v[140:141], v[140:141], v[144:145] op_sel:[1,0] op_sel_hi:[0,1]
	v_mov_b32_e32 v143, v140
	v_pk_add_f32 v[150:151], v[142:143], v[152:153] neg_lo:[0,1] neg_hi:[0,1]
	v_mov_b32_e32 v139, v144
	v_sub_f32_e32 v141, v142, v150
	v_pk_add_f32 v[138:139], v[138:139], v[150:151] neg_lo:[0,1] neg_hi:[0,1]
	v_sub_f32_e32 v141, v152, v141
	v_add_f32_e32 v138, v138, v141
	v_add_f32_e32 v138, v138, v139
	v_add_f32_e32 v138, v140, v138
	v_cndmask_b32_e32 v138, v217, v138, vcc
	v_cmp_lt_f32_e64 vcc, |v149|, s92
	s_nop 1
	v_cndmask_b32_e32 v138, v138, v149, vcc

; __device__ __forceinline__ float softplusf(float x) { return x > 20.f ? x : log1pf(expf(x)); }
;     __device__ __forceinline__ void operator()(const f32x4 (&acc)[2][2][4][2], const pg8::Unit& u, int wr, int wc, int fr, int fq_in) const {
;     ...
;         } else {
;             if (wc < 2) {
;                 const int col0 = wc * 32 + 8 * fq; const f32x4 b0 = *(const f32x4*)(dtb + col0), b1 = *(const f32x4*)(dtb + col0 + 4);
; #pragma unroll
;                 for (int ai = 0; ai < 2; ++ai)
; #pragma unroll
;                     for (int m = 0; m < 4; ++m) { float* rowp = DTS + (size_t)(row0 + ai * 128 + m * 16) * 64 + col0; f32x4 o0, o1;
; #pragma unroll
;                         for (int q = 0; q < 4; ++q) { o0[q] = softplusf(acc[ai][0][m][0][q] + b0[q]); o1[q] = softplusf(acc[ai][0][m][1][q] + b1[q]); }
;                         *(f32x4*)(rowp) = o0; *(f32x4*)(rowp + 4) = o1; }
;             }
.LBB0_405:
	s_or_b64 exec, exec, s[0:1]
	v_or_b32_e32 v150, 48, v178
	v_ashrrev_i32_e32 v151, 31, v150
	v_lshlrev_b64 v[150:151], 8, v[150:151]
	v_lshl_add_u64 v[150:151], s[38:39], 0, v[150:151]
	v_lshl_add_u64 v[150:151], v[146:147], 2, v[150:151]
	global_store_dwordx4 v[150:151], v[138:141], off nt
	global_store_dwordx4 v[150:151], v[142:145], off offset:16 nt
	s_nop 0
	v_add_f32_e32 v138, v62, v134
	v_cmp_nlt_f32_e32 vcc, s83, v138
	s_and_saveexec_b64 s[0:1], vcc
	s_cbranch_execz .LBB0_407
	v_mul_f32_e32 v139, 0x3fb8aa3b, v138
	v_rndne_f32_e32 v140, v139
	v_sub_f32_e32 v141, v139, v140
	v_fma_f32 v139, v138, s86, -v139
	v_fmac_f32_e32 v139, 0x32a5705f, v138
	v_add_f32_e32 v139, v141, v139
	v_cvt_i32_f32_e32 v140, v140
	v_exp_f32_e32 v139, v139
	v_cmp_ngt_f32_e32 vcc, s87, v138
	v_ldexp_f32 v139, v139, v140
	s_nop 0
	v_cndmask_b32_e32 v139, 0, v139, vcc
	v_cmp_nlt_f32_e32 vcc, s88, v138
	s_nop 1
	v_cndmask_b32_e32 v149, v217, v139, vcc
	v_add_f32_e32 v140, 1.0, v149
	v_add_f32_e32 v138, -1.0, v140
	v_sub_f32_e32 v139, v138, v140
	v_add_f32_e32 v139, 1.0, v139
	v_sub_f32_e32 v138, v149, v138
	v_add_f32_e32 v141, v138, v139
	v_frexp_mant_f32_e32 v142, v140
	v_cvt_f64_f32_e32 v[138:139], v140
	v_frexp_exp_i32_f64_e32 v138, v[138:139]
	v_cmp_gt_f32_e32 vcc, s90, v142
	s_nop 1
	v_subbrev_co_u32_e32 v150, vcc, 0, v138, vcc
	v_sub_u32_e32 v138, 0, v150
	v_ldexp_f32 v139, v140, v138
	v_add_f32_e32 v140, -1.0, v139
	v_add_f32_e32 v142, 1.0, v139
	v_ldexp_f32 v138, v141, v138
	v_add_f32_e32 v141, 1.0, v140
	v_add_f32_e32 v143, -1.0, v142
	v_sub_f32_e32 v141, v139, v141
	v_sub_f32_e32 v139, v139, v143
	v_add_f32_e32 v141, v138, v141
	v_add_f32_e32 v138, v138, v139
	v_add_f32_e32 v151, v142, v138
	v_rcp_f32_e32 v153, v151
	v_sub_f32_e32 v139, v142, v151
	v_add_f32_e32 v152, v138, v139
	v_add_f32_e32 v139, v140, v141
	v_mul_f32_e32 v155, v139, v153
	v_sub_f32_e32 v138, v140, v139
	v_mul_f32_e32 v140, v151, v155
	v_fma_f32 v142, v155, v151, -v140
	v_fmac_f32_e32 v142, v155, v152
	v_add_f32_e32 v154, v141, v138
	v_add_f32_e32 v138, v140, v142
	v_sub_f32_e32 v141, v139, v138
	v_pk_add_f32 v[144:145], v[138:139], v[140:141] neg_lo:[0,1] neg_hi:[0,1]
	v_mov_b32_e32 v143, v138
	v_pk_add_f32 v[138:139], v[144:145], v[142:143] neg_lo:[0,1] neg_hi:[0,1]
	v_cmp_neq_f32_e32 vcc, s89, v149
	v_add_f32_e32 v139, v154, v139
	v_add_f32_e32 v138, v138, v139
	v_add_f32_e32 v139, v141, v138
	v_mul_f32_e32 v154, v153, v139
	v_mul_f32_e32 v140, v151, v154
	v_fma_f32 v142, v154, v151, -v140
	v_fmac_f32_e32 v142, v154, v152
	v_sub_f32_e32 v141, v141, v139
	v_add_f32_e32 v151, v138, v141
	v_add_f32_e32 v138, v140, v142
	v_sub_f32_e32 v141, v139, v138
	v_pk_add_f32 v[144:145], v[138:139], v[140:141] neg_lo:[0,1] neg_hi:[0,1]
	v_mov_b32_e32 v143, v138
	v_pk_add_f32 v[138:139], v[144:145], v[142:143] neg_lo:[0,1] neg_hi:[0,1]
	s_nop 0
	v_add_f32_e32 v139, v151, v139
	v_add_f32_e32 v138, v138, v139
	v_add_f32_e32 v139, v155, v154
	v_add_f32_e32 v138, v141, v138
	v_sub_f32_e32 v140, v139, v155
	v_mul_f32_e32 v138, v153, v138
	v_sub_f32_e32 v140, v154, v140
	v_add_f32_e32 v140, v140, v138
	v_add_f32_e32 v142, v139, v140
	v_mul_f32_e32 v143, v142, v142
	v_fmamk_f32 v138, v143, 0x3e9b6dac, v216
	v_fmaak_f32 v177, v143, v138, 0x3f2aaada
	v_cvt_f32_i32_e32 v138, v150
	v_sub_f32_e32 v139, v142, v139
	v_sub_f32_e32 v139, v140, v139
	v_ldexp_f32 v144, v139, 1
	v_mul_f32_e32 v139, v142, v143
	v_ldexp_f32 v141, v142, 1
	v_pk_mul_f32 v[142:143], v[138:139], v[176:177]
	s_nop 0
	v_fma_f32 v140, v138, s91, -v142
	v_fmac_f32_e32 v140, 0xb102e308, v138
	v_pk_add_f32 v[138:139], v[142:143], v[140:141]
	s_nop 0
	v_sub_f32_e32 v141, v139, v141
	v_sub_f32_e32 v141, v143, v141
	v_add_f32_e32 v145, v144, v141
	v_mov_b32_e32 v144, v142
	v_pk_add_f32 v[142:143], v[138:139], v[142:143] neg_lo:[0,1] neg_hi:[0,1]
	v_pk_add_f32 v[150:151], v[138:139], v[144:145]
	v_mov_b32_e32 v141, v138
	v_mov_b32_e32 v143, v151
	v_pk_add_f32 v[152:153], v[140:141], v[142:143] neg_lo:[0,1] neg_hi:[0,1]
	v_pk_add_f32 v[140:141], v[140:141], v[142:143]
	v_mov_b32_e32 v144, v145
	v_pk_add_f32 v[142:143], v[140:141], v[138:139] op_sel:[1,0] op_sel_hi:[0,1] neg_lo:[0,1] neg_hi:[0,1]
	v_pk_add_f32 v[154:155], v[150:151], v[142:143] op_sel_hi:[1,0] neg_lo:[0,1] neg_hi:[0,1]
	v_mov_b32_e32 v150, v151
	v_mov_b32_e32 v151, v141
	v_pk_mov_b32 v[142:143], v[138:139], v[142:143] op_sel:[1,0]
	v_mov_b32_e32 v145, v138
	v_pk_add_f32 v[142:143], v[150:151], v[142:143] neg_lo:[0,1] neg_hi:[0,1]
	v_mov_b32_e32 v154, v152
	v_pk_add_f32 v[138:139], v[144:145], v[142:143] neg_lo:[0,1] neg_hi:[0,1]
	v_mov_b32_e32 v153, v141
	v_pk_add_f32 v[142:143], v[154:155], v[138:139]
	s_nop 0
	v_pk_add_f32 v[144:145], v[142:143], v[142:143] op_sel:[0,1] op_sel_hi:[1,0]
	s_nop 0
	v_pk_add_f32 v[140:141], v[140:141], v[144:145] op_sel:[1,0] op_sel_hi:[0,1]
	v_mov_b32_e32 v143, v140
	v_pk_add_f32 v[150:151], v[142:143], v[152:153] neg_lo:[0,1] neg_hi:[0,1]
	v_mov_b32_e32 v139, v144
	v_sub_f32_e32 v141, v142, v150
	v_pk_add_f32 v[138:139], v[138:139], v[150:151] neg_lo:[0,1] neg_hi:[0,1]
	v_sub_f32_e32 v141, v152, v141
	v_add_f32_e32 v138, v138, v141
	v_add_f32_e32 v138, v138, v139
	v_add_f32_e32 v138, v140, v138
	v_cndmask_b32_e32 v138, v217, v138, vcc
	v_cmp_lt_f32_e64 vcc, |v149|, s92
	s_nop 1
	v_cndmask_b32_e32 v138, v138, v149, vcc

; __device__ __forceinline__ float softplusf(float x) { return x > 20.f ? x : log1pf(expf(x)); }
;     __device__ __forceinline__ void operator()(const f32x4 (&acc)[2][2][4][2], const pg8::Unit& u, int wr, int wc, int fr, int fq_in) const {
;     ...
;         } else {
;             if (wc < 2) {
;                 const int col0 = wc * 32 + 8 * fq; const f32x4 b0 = *(const f32x4*)(dtb + col0), b1 = *(const f32x4*)(dtb + col0 + 4);
; #pragma unroll
;                 for (int ai = 0; ai < 2; ++ai)
; #pragma unroll
;                     for (int m = 0; m < 4; ++m) { float* rowp = DTS + (size_t)(row0 + ai * 128 + m * 16) * 64 + col0; f32x4 o0, o1;
; #pragma unroll
;                         for (int q = 0; q < 4; ++q) { o0[q] = softplusf(acc[ai][0][m][0][q] + b0[q]); o1[q] = softplusf(acc[ai][0][m][1][q] + b1[q]); }
;                         *(f32x4*)(rowp) = o0; *(f32x4*)(rowp + 4) = o1; }
;             }
.LBB0_421:
	s_or_b64 exec, exec, s[0:1]
	v_lshlrev_b64 v[150:151], 8, v[178:179]
	v_lshl_add_u64 v[150:151], s[38:39], 0, v[150:151]
	v_lshl_add_u64 v[150:151], v[146:147], 2, v[150:151]
	s_mov_b64 s[0:1], 0x8000
	v_lshl_add_u64 v[152:153], v[150:151], 0, s[0:1]
	v_add_co_u32_e32 v150, vcc, 0x8000, v150
	s_nop 1
	v_addc_co_u32_e32 v151, vcc, 0, v151, vcc
	global_store_dwordx4 v[150:151], v[138:141], off nt
	global_store_dwordx4 v[152:153], v[142:145], off offset:16 nt
	s_nop 0
	v_add_f32_e32 v138, v54, v134
	v_cmp_nlt_f32_e32 vcc, s83, v138
	s_and_saveexec_b64 s[0:1], vcc
	s_cbranch_execz .LBB0_423
	v_mul_f32_e32 v139, 0x3fb8aa3b, v138
	v_rndne_f32_e32 v140, v139
	v_sub_f32_e32 v141, v139, v140
	v_fma_f32 v139, v138, s86, -v139
	v_fmac_f32_e32 v139, 0x32a5705f, v138
	v_add_f32_e32 v139, v141, v139
	v_cvt_i32_f32_e32 v140, v140
	v_exp_f32_e32 v139, v139
	v_cmp_ngt_f32_e32 vcc, s87, v138
	v_ldexp_f32 v139, v139, v140
	s_nop 0
	v_cndmask_b32_e32 v139, 0, v139, vcc
	v_cmp_nlt_f32_e32 vcc, s88, v138
	s_nop 1
	v_cndmask_b32_e32 v149, v217, v139, vcc
	v_add_f32_e32 v140, 1.0, v149
	v_add_f32_e32 v138, -1.0, v140
	v_sub_f32_e32 v139, v138, v140
	v_add_f32_e32 v139, 1.0, v139
	v_sub_f32_e32 v138, v149, v138
	v_add_f32_e32 v141, v138, v139
	v_frexp_mant_f32_e32 v142, v140
	v_cvt_f64_f32_e32 v[138:139], v140
	v_frexp_exp_i32_f64_e32 v138, v[138:139]
	v_cmp_gt_f32_e32 vcc, s90, v142
	s_nop 1
	v_subbrev_co_u32_e32 v150, vcc, 0, v138, vcc
	v_sub_u32_e32 v138, 0, v150
	v_ldexp_f32 v139, v140, v138
	v_add_f32_e32 v140, -1.0, v139
	v_add_f32_e32 v142, 1.0, v139
	v_ldexp_f32 v138, v141, v138
	v_add_f32_e32 v141, 1.0, v140
	v_add_f32_e32 v143, -1.0, v142
	v_sub_f32_e32 v141, v139, v141
	v_sub_f32_e32 v139, v139, v143
	v_add_f32_e32 v141, v138, v141
	v_add_f32_e32 v138, v138, v139
	v_add_f32_e32 v151, v142, v138
	v_rcp_f32_e32 v153, v151
	v_sub_f32_e32 v139, v142, v151
	v_add_f32_e32 v152, v138, v139
	v_add_f32_e32 v139, v140, v141
	v_mul_f32_e32 v155, v139, v153
	v_sub_f32_e32 v138, v140, v139
	v_mul_f32_e32 v140, v151, v155
	v_fma_f32 v142, v155, v151, -v140
	v_fmac_f32_e32 v142, v155, v152
	v_add_f32_e32 v154, v141, v138
	v_add_f32_e32 v138, v140, v142
	v_sub_f32_e32 v141, v139, v138
	v_pk_add_f32 v[144:145], v[138:139], v[140:141] neg_lo:[0,1] neg_hi:[0,1]
	v_mov_b32_e32 v143, v138
	v_pk_add_f32 v[138:139], v[144:145], v[142:143] neg_lo:[0,1] neg_hi:[0,1]
	v_cmp_neq_f32_e32 vcc, s89, v149
	v_add_f32_e32 v139, v154, v139
	v_add_f32_e32 v138, v138, v139
	v_add_f32_e32 v139, v141, v138
	v_mul_f32_e32 v154, v153, v139
	v_mul_f32_e32 v140, v151, v154
	v_fma_f32 v142, v154, v151, -v140
	v_fmac_f32_e32 v142, v154, v152
	v_sub_f32_e32 v141, v141, v139
	v_add_f32_e32 v151, v138, v141
	v_add_f32_e32 v138, v140, v142
	v_sub_f32_e32 v141, v139, v138
	v_pk_add_f32 v[144:145], v[138:139], v[140:141] neg_lo:[0,1] neg_hi:[0,1]
	v_mov_b32_e32 v143, v138
	v_pk_add_f32 v[138:139], v[144:145], v[142:143] neg_lo:[0,1] neg_hi:[0,1]
	s_nop 0
	v_add_f32_e32 v139, v151, v139
	v_add_f32_e32 v138, v138, v139
	v_add_f32_e32 v139, v155, v154
	v_add_f32_e32 v138, v141, v138
	v_sub_f32_e32 v140, v139, v155
	v_mul_f32_e32 v138, v153, v138
	v_sub_f32_e32 v140, v154, v140
	v_add_f32_e32 v140, v140, v138
	v_add_f32_e32 v142, v139, v140
	v_mul_f32_e32 v143, v142, v142
	v_fmamk_f32 v138, v143, 0x3e9b6dac, v216
	v_fmaak_f32 v177, v143, v138, 0x3f2aaada
	v_cvt_f32_i32_e32 v138, v150
	v_sub_f32_e32 v139, v142, v139
	v_sub_f32_e32 v139, v140, v139
	v_ldexp_f32 v144, v139, 1
	v_mul_f32_e32 v139, v142, v143
	v_ldexp_f32 v141, v142, 1
	v_pk_mul_f32 v[142:143], v[138:139], v[176:177]
	s_nop 0
	v_fma_f32 v140, v138, s91, -v142
	v_fmac_f32_e32 v140, 0xb102e308, v138
	v_pk_add_f32 v[138:139], v[142:143], v[140:141]
	s_nop 0
	v_sub_f32_e32 v141, v139, v141
	v_sub_f32_e32 v141, v143, v141
	v_add_f32_e32 v145, v144, v141
	v_mov_b32_e32 v144, v142
	v_pk_add_f32 v[142:143], v[138:139], v[142:143] neg_lo:[0,1] neg_hi:[0,1]
	v_pk_add_f32 v[150:151], v[138:139], v[144:145]
	v_mov_b32_e32 v141, v138
	v_mov_b32_e32 v143, v151
	v_pk_add_f32 v[152:153], v[140:141], v[142:143] neg_lo:[0,1] neg_hi:[0,1]
	v_pk_add_f32 v[140:141], v[140:141], v[142:143]
	v_mov_b32_e32 v144, v145
	v_pk_add_f32 v[142:143], v[140:141], v[138:139] op_sel:[1,0] op_sel_hi:[0,1] neg_lo:[0,1] neg_hi:[0,1]
	v_pk_add_f32 v[154:155], v[150:151], v[142:143] op_sel_hi:[1,0] neg_lo:[0,1] neg_hi:[0,1]
	v_mov_b32_e32 v150, v151
	v_mov_b32_e32 v151, v141
	v_pk_mov_b32 v[142:143], v[138:139], v[142:143] op_sel:[1,0]
	v_mov_b32_e32 v145, v138
	v_pk_add_f32 v[142:143], v[150:151], v[142:143] neg_lo:[0,1] neg_hi:[0,1]
	v_mov_b32_e32 v154, v152
	v_pk_add_f32 v[138:139], v[144:145], v[142:143] neg_lo:[0,1] neg_hi:[0,1]
	v_mov_b32_e32 v153, v141
	v_pk_add_f32 v[142:143], v[154:155], v[138:139]
	s_nop 0
	v_pk_add_f32 v[144:145], v[142:143], v[142:143] op_sel:[0,1] op_sel_hi:[1,0]
	s_nop 0
	v_pk_add_f32 v[140:141], v[140:141], v[144:145] op_sel:[1,0] op_sel_hi:[0,1]
	v_mov_b32_e32 v143, v140
	v_pk_add_f32 v[150:151], v[142:143], v[152:153] neg_lo:[0,1] neg_hi:[0,1]
	v_mov_b32_e32 v139, v144
	v_sub_f32_e32 v141, v142, v150
	v_pk_add_f32 v[138:139], v[138:139], v[150:151] neg_lo:[0,1] neg_hi:[0,1]
	v_sub_f32_e32 v141, v152, v141
	v_add_f32_e32 v138, v138, v141
	v_add_f32_e32 v138, v138, v139
	v_add_f32_e32 v138, v140, v138
	v_cndmask_b32_e32 v138, v217, v138, vcc
	v_cmp_lt_f32_e64 vcc, |v149|, s92
	s_nop 1
	v_cndmask_b32_e32 v138, v138, v149, vcc

; __device__ __forceinline__ float softplusf(float x) { return x > 20.f ? x : log1pf(expf(x)); }
;     __device__ __forceinline__ void operator()(const f32x4 (&acc)[2][2][4][2], const pg8::Unit& u, int wr, int wc, int fr, int fq_in) const {
;     ...
;         } else {
;             if (wc < 2) {
;                 const int col0 = wc * 32 + 8 * fq; const f32x4 b0 = *(const f32x4*)(dtb + col0), b1 = *(const f32x4*)(dtb + col0 + 4);
; #pragma unroll
;                 for (int ai = 0; ai < 2; ++ai)
; #pragma unroll
;                     for (int m = 0; m < 4; ++m) { float* rowp = DTS + (size_t)(row0 + ai * 128 + m * 16) * 64 + col0; f32x4 o0, o1;
; #pragma unroll
;                         for (int q = 0; q < 4; ++q) { o0[q] = softplusf(acc[ai][0][m][0][q] + b0[q]); o1[q] = softplusf(acc[ai][0][m][1][q] + b1[q]); }
;                         *(f32x4*)(rowp) = o0; *(f32x4*)(rowp + 4) = o1; }
;             }
.LBB0_437:
	s_or_b64 exec, exec, s[0:1]
	v_lshlrev_b64 v[150:151], 8, v[178:179]
	v_lshl_add_u64 v[150:151], s[38:39], 0, v[150:151]
	v_lshl_add_u64 v[150:151], v[146:147], 2, v[150:151]
	s_mov_b64 s[0:1], 0x9000
	v_lshl_add_u64 v[152:153], v[150:151], 0, s[0:1]
	v_add_co_u32_e32 v150, vcc, 0x9000, v150
	s_nop 1
	v_addc_co_u32_e32 v151, vcc, 0, v151, vcc
	global_store_dwordx4 v[150:151], v[138:141], off nt
	global_store_dwordx4 v[152:153], v[142:145], off offset:16 nt
	s_nop 0
	v_add_f32_e32 v138, v38, v134
	v_cmp_nlt_f32_e32 vcc, s83, v138
	s_and_saveexec_b64 s[0:1], vcc
	s_cbranch_execz .LBB0_439
	v_mul_f32_e32 v139, 0x3fb8aa3b, v138
	v_rndne_f32_e32 v140, v139
	v_sub_f32_e32 v141, v139, v140
	v_fma_f32 v139, v138, s86, -v139
	v_fmac_f32_e32 v139, 0x32a5705f, v138
	v_add_f32_e32 v139, v141, v139
	v_cvt_i32_f32_e32 v140, v140
	v_exp_f32_e32 v139, v139
	v_cmp_ngt_f32_e32 vcc, s87, v138
	v_ldexp_f32 v139, v139, v140
	s_nop 0
	v_cndmask_b32_e32 v139, 0, v139, vcc
	v_cmp_nlt_f32_e32 vcc, s88, v138
	s_nop 1
	v_cndmask_b32_e32 v149, v217, v139, vcc
	v_add_f32_e32 v140, 1.0, v149
	v_add_f32_e32 v138, -1.0, v140
	v_sub_f32_e32 v139, v138, v140
	v_add_f32_e32 v139, 1.0, v139
	v_sub_f32_e32 v138, v149, v138
	v_add_f32_e32 v141, v138, v139
	v_frexp_mant_f32_e32 v142, v140
	v_cvt_f64_f32_e32 v[138:139], v140
	v_frexp_exp_i32_f64_e32 v138, v[138:139]
	v_cmp_gt_f32_e32 vcc, s90, v142
	s_nop 1
	v_subbrev_co_u32_e32 v150, vcc, 0, v138, vcc
	v_sub_u32_e32 v138, 0, v150
	v_ldexp_f32 v139, v140, v138
	v_add_f32_e32 v140, -1.0, v139
	v_add_f32_e32 v142, 1.0, v139
	v_ldexp_f32 v138, v141, v138
	v_add_f32_e32 v141, 1.0, v140
	v_add_f32_e32 v143, -1.0, v142
	v_sub_f32_e32 v141, v139, v141
	v_sub_f32_e32 v139, v139, v143
	v_add_f32_e32 v141, v138, v141
	v_add_f32_e32 v138, v138, v139
	v_add_f32_e32 v151, v142, v138
	v_rcp_f32_e32 v153, v151
	v_sub_f32_e32 v139, v142, v151
	v_add_f32_e32 v152, v138, v139
	v_add_f32_e32 v139, v140, v141
	v_mul_f32_e32 v155, v139, v153
	v_sub_f32_e32 v138, v140, v139
	v_mul_f32_e32 v140, v151, v155
	v_fma_f32 v142, v155, v151, -v140
	v_fmac_f32_e32 v142, v155, v152
	v_add_f32_e32 v154, v141, v138
	v_add_f32_e32 v138, v140, v142
	v_sub_f32_e32 v141, v139, v138
	v_pk_add_f32 v[144:145], v[138:139], v[140:141] neg_lo:[0,1] neg_hi:[0,1]
	v_mov_b32_e32 v143, v138
	v_pk_add_f32 v[138:139], v[144:145], v[142:143] neg_lo:[0,1] neg_hi:[0,1]
	v_cmp_neq_f32_e32 vcc, s89, v149
	v_add_f32_e32 v139, v154, v139
	v_add_f32_e32 v138, v138, v139
	v_add_f32_e32 v139, v141, v138
	v_mul_f32_e32 v154, v153, v139
	v_mul_f32_e32 v140, v151, v154
	v_fma_f32 v142, v154, v151, -v140
	v_fmac_f32_e32 v142, v154, v152
	v_sub_f32_e32 v141, v141, v139
	v_add_f32_e32 v151, v138, v141
	v_add_f32_e32 v138, v140, v142
	v_sub_f32_e32 v141, v139, v138
	v_pk_add_f32 v[144:145], v[138:139], v[140:141] neg_lo:[0,1] neg_hi:[0,1]
	v_mov_b32_e32 v143, v138
	v_pk_add_f32 v[138:139], v[144:145], v[142:143] neg_lo:[0,1] neg_hi:[0,1]
	s_nop 0
	v_add_f32_e32 v139, v151, v139
	v_add_f32_e32 v138, v138, v139
	v_add_f32_e32 v139, v155, v154
	v_add_f32_e32 v138, v141, v138
	v_sub_f32_e32 v140, v139, v155
	v_mul_f32_e32 v138, v153, v138
	v_sub_f32_e32 v140, v154, v140
	v_add_f32_e32 v140, v140, v138
	v_add_f32_e32 v142, v139, v140
	v_mul_f32_e32 v143, v142, v142
	v_fmamk_f32 v138, v143, 0x3e9b6dac, v216
	v_fmaak_f32 v177, v143, v138, 0x3f2aaada
	v_cvt_f32_i32_e32 v138, v150
	v_sub_f32_e32 v139, v142, v139
	v_sub_f32_e32 v139, v140, v139
	v_ldexp_f32 v144, v139, 1
	v_mul_f32_e32 v139, v142, v143
	v_ldexp_f32 v141, v142, 1
	v_pk_mul_f32 v[142:143], v[138:139], v[176:177]
	s_nop 0
	v_fma_f32 v140, v138, s91, -v142
	v_fmac_f32_e32 v140, 0xb102e308, v138
	v_pk_add_f32 v[138:139], v[142:143], v[140:141]
	s_nop 0
	v_sub_f32_e32 v141, v139, v141
	v_sub_f32_e32 v141, v143, v141
	v_add_f32_e32 v145, v144, v141
	v_mov_b32_e32 v144, v142
	v_pk_add_f32 v[142:143], v[138:139], v[142:143] neg_lo:[0,1] neg_hi:[0,1]
	v_pk_add_f32 v[150:151], v[138:139], v[144:145]
	v_mov_b32_e32 v141, v138
	v_mov_b32_e32 v143, v151
	v_pk_add_f32 v[152:153], v[140:141], v[142:143] neg_lo:[0,1] neg_hi:[0,1]
	v_pk_add_f32 v[140:141], v[140:141], v[142:143]
	v_mov_b32_e32 v144, v145
	v_pk_add_f32 v[142:143], v[140:141], v[138:139] op_sel:[1,0] op_sel_hi:[0,1] neg_lo:[0,1] neg_hi:[0,1]
	v_pk_add_f32 v[154:155], v[150:151], v[142:143] op_sel_hi:[1,0] neg_lo:[0,1] neg_hi:[0,1]
	v_mov_b32_e32 v150, v151
	v_mov_b32_e32 v151, v141
	v_pk_mov_b32 v[142:143], v[138:139], v[142:143] op_sel:[1,0]
	v_mov_b32_e32 v145, v138
	v_pk_add_f32 v[142:143], v[150:151], v[142:143] neg_lo:[0,1] neg_hi:[0,1]
	v_mov_b32_e32 v154, v152
	v_pk_add_f32 v[138:139], v[144:145], v[142:143] neg_lo:[0,1] neg_hi:[0,1]
	v_mov_b32_e32 v153, v141
	v_pk_add_f32 v[142:143], v[154:155], v[138:139]
	s_nop 0
	v_pk_add_f32 v[144:145], v[142:143], v[142:143] op_sel:[0,1] op_sel_hi:[1,0]
	s_nop 0
	v_pk_add_f32 v[140:141], v[140:141], v[144:145] op_sel:[1,0] op_sel_hi:[0,1]
	v_mov_b32_e32 v143, v140
	v_pk_add_f32 v[150:151], v[142:143], v[152:153] neg_lo:[0,1] neg_hi:[0,1]
	v_mov_b32_e32 v139, v144
	v_sub_f32_e32 v141, v142, v150
	v_pk_add_f32 v[138:139], v[138:139], v[150:151] neg_lo:[0,1] neg_hi:[0,1]
	v_sub_f32_e32 v141, v152, v141
	v_add_f32_e32 v138, v138, v141
	v_add_f32_e32 v138, v138, v139
	v_add_f32_e32 v138, v140, v138
	v_cndmask_b32_e32 v138, v217, v138, vcc
	v_cmp_lt_f32_e64 vcc, |v149|, s92
	s_nop 1
	v_cndmask_b32_e32 v138, v138, v149, vcc

; __device__ __forceinline__ float softplusf(float x) { return x > 20.f ? x : log1pf(expf(x)); }
;     __device__ __forceinline__ void operator()(const f32x4 (&acc)[2][2][4][2], const pg8::Unit& u, int wr, int wc, int fr, int fq_in) const {
;     ...
;         } else {
;             if (wc < 2) {
;                 const int col0 = wc * 32 + 8 * fq; const f32x4 b0 = *(const f32x4*)(dtb + col0), b1 = *(const f32x4*)(dtb + col0 + 4);
; #pragma unroll
;                 for (int ai = 0; ai < 2; ++ai)
; #pragma unroll
;                     for (int m = 0; m < 4; ++m) { float* rowp = DTS + (size_t)(row0 + ai * 128 + m * 16) * 64 + col0; f32x4 o0, o1;
; #pragma unroll
;                         for (int q = 0; q < 4; ++q) { o0[q] = softplusf(acc[ai][0][m][0][q] + b0[q]); o1[q] = softplusf(acc[ai][0][m][1][q] + b1[q]); }
;                         *(f32x4*)(rowp) = o0; *(f32x4*)(rowp + 4) = o1; }
;             }
.LBB0_453:
	s_or_b64 exec, exec, s[0:1]
	v_lshlrev_b64 v[150:151], 8, v[178:179]
	v_lshl_add_u64 v[150:151], s[38:39], 0, v[150:151]
	v_lshl_add_u64 v[150:151], v[146:147], 2, v[150:151]
	s_mov_b64 s[0:1], 0xa000
	v_lshl_add_u64 v[152:153], v[150:151], 0, s[0:1]
	v_add_co_u32_e32 v150, vcc, 0xa000, v150
	v_add_f32_e32 v134, v22, v134
	s_nop 0
	v_addc_co_u32_e32 v151, vcc, 0, v151, vcc
	v_cmp_nlt_f32_e32 vcc, s83, v134
	global_store_dwordx4 v[150:151], v[138:141], off nt
	global_store_dwordx4 v[152:153], v[142:145], off offset:16 nt
	s_and_saveexec_b64 s[0:1], vcc
	s_cbranch_execz .LBB0_455
	v_mul_f32_e32 v138, 0x3fb8aa3b, v134
	v_rndne_f32_e32 v139, v138
	v_sub_f32_e32 v140, v138, v139
	v_fma_f32 v138, v134, s86, -v138
	v_fmac_f32_e32 v138, 0x32a5705f, v134
	v_add_f32_e32 v138, v140, v138
	v_cvt_i32_f32_e32 v139, v139
	v_exp_f32_e32 v138, v138
	v_cmp_ngt_f32_e32 vcc, s87, v134
	v_ldexp_f32 v138, v138, v139
	s_nop 0
	v_cndmask_b32_e32 v138, 0, v138, vcc
	v_cmp_nlt_f32_e32 vcc, s88, v134
	s_nop 1
	v_cndmask_b32_e32 v134, v217, v138, vcc
	v_add_f32_e32 v140, 1.0, v134
	v_add_f32_e32 v138, -1.0, v140
	v_sub_f32_e32 v139, v138, v140
	v_add_f32_e32 v139, 1.0, v139
	v_sub_f32_e32 v138, v134, v138
	v_add_f32_e32 v141, v138, v139
	v_frexp_mant_f32_e32 v142, v140
	v_cvt_f64_f32_e32 v[138:139], v140
	v_frexp_exp_i32_f64_e32 v138, v[138:139]
	v_cmp_gt_f32_e32 vcc, s90, v142
	s_nop 1
	v_subbrev_co_u32_e32 v149, vcc, 0, v138, vcc
	v_sub_u32_e32 v138, 0, v149
	v_ldexp_f32 v139, v140, v138
	v_add_f32_e32 v140, -1.0, v139
	v_add_f32_e32 v142, 1.0, v139
	v_ldexp_f32 v138, v141, v138
	v_add_f32_e32 v141, 1.0, v140
	v_add_f32_e32 v143, -1.0, v142
	v_sub_f32_e32 v141, v139, v141
	v_sub_f32_e32 v139, v139, v143
	v_add_f32_e32 v141, v138, v141
	v_add_f32_e32 v138, v138, v139
	v_add_f32_e32 v150, v142, v138
	v_rcp_f32_e32 v152, v150
	v_sub_f32_e32 v139, v142, v150
	v_add_f32_e32 v151, v138, v139
	v_add_f32_e32 v139, v140, v141
	v_mul_f32_e32 v154, v139, v152
	v_sub_f32_e32 v138, v140, v139
	v_mul_f32_e32 v140, v150, v154
	v_fma_f32 v142, v154, v150, -v140
	v_fmac_f32_e32 v142, v154, v151
	v_add_f32_e32 v153, v141, v138
	v_add_f32_e32 v138, v140, v142
	v_sub_f32_e32 v141, v139, v138
	v_pk_add_f32 v[144:145], v[138:139], v[140:141] neg_lo:[0,1] neg_hi:[0,1]
	v_mov_b32_e32 v143, v138
	v_pk_add_f32 v[138:139], v[144:145], v[142:143] neg_lo:[0,1] neg_hi:[0,1]
	v_cmp_neq_f32_e32 vcc, s89, v134
	v_add_f32_e32 v139, v153, v139
	v_add_f32_e32 v138, v138, v139
	v_add_f32_e32 v139, v141, v138
	v_mul_f32_e32 v153, v152, v139
	v_mul_f32_e32 v140, v150, v153
	v_fma_f32 v142, v153, v150, -v140
	v_fmac_f32_e32 v142, v153, v151
	v_sub_f32_e32 v141, v141, v139
	v_add_f32_e32 v150, v138, v141
	v_add_f32_e32 v138, v140, v142
	v_sub_f32_e32 v141, v139, v138
	v_pk_add_f32 v[144:145], v[138:139], v[140:141] neg_lo:[0,1] neg_hi:[0,1]
	v_mov_b32_e32 v143, v138
	v_pk_add_f32 v[138:139], v[144:145], v[142:143] neg_lo:[0,1] neg_hi:[0,1]
	s_nop 0
	v_add_f32_e32 v139, v150, v139
	v_add_f32_e32 v138, v138, v139
	v_add_f32_e32 v139, v154, v153
	v_add_f32_e32 v138, v141, v138
	v_sub_f32_e32 v140, v139, v154
	v_mul_f32_e32 v138, v152, v138
	v_sub_f32_e32 v140, v153, v140
	v_add_f32_e32 v140, v140, v138
	v_add_f32_e32 v142, v139, v140
	v_mul_f32_e32 v143, v142, v142
	v_fmamk_f32 v138, v143, 0x3e9b6dac, v216
	v_fmaak_f32 v177, v143, v138, 0x3f2aaada
	v_cvt_f32_i32_e32 v138, v149
	v_sub_f32_e32 v139, v142, v139
	v_sub_f32_e32 v139, v140, v139
	v_ldexp_f32 v144, v139, 1
	v_mul_f32_e32 v139, v142, v143
	v_ldexp_f32 v141, v142, 1
	v_pk_mul_f32 v[142:143], v[138:139], v[176:177]
	s_nop 0
	v_fma_f32 v140, v138, s91, -v142
	v_fmac_f32_e32 v140, 0xb102e308, v138
	v_pk_add_f32 v[138:139], v[142:143], v[140:141]
	s_nop 0
	v_sub_f32_e32 v141, v139, v141
	v_sub_f32_e32 v141, v143, v141
	v_add_f32_e32 v145, v144, v141
	v_mov_b32_e32 v144, v142
	v_pk_add_f32 v[142:143], v[138:139], v[142:143] neg_lo:[0,1] neg_hi:[0,1]
	v_pk_add_f32 v[150:151], v[138:139], v[144:145]
	v_mov_b32_e32 v141, v138
	v_mov_b32_e32 v143, v151
	v_pk_add_f32 v[152:153], v[140:141], v[142:143] neg_lo:[0,1] neg_hi:[0,1]
	v_pk_add_f32 v[140:141], v[140:141], v[142:143]
	v_mov_b32_e32 v144, v145
	v_pk_add_f32 v[142:143], v[140:141], v[138:139] op_sel:[1,0] op_sel_hi:[0,1] neg_lo:[0,1] neg_hi:[0,1]
	v_pk_add_f32 v[154:155], v[150:151], v[142:143] op_sel_hi:[1,0] neg_lo:[0,1] neg_hi:[0,1]
	v_mov_b32_e32 v150, v151
	v_mov_b32_e32 v151, v141
	v_pk_mov_b32 v[142:143], v[138:139], v[142:143] op_sel:[1,0]
	v_mov_b32_e32 v145, v138
	v_pk_add_f32 v[142:143], v[150:151], v[142:143] neg_lo:[0,1] neg_hi:[0,1]
	v_mov_b32_e32 v154, v152
	v_pk_add_f32 v[138:139], v[144:145], v[142:143] neg_lo:[0,1] neg_hi:[0,1]
	v_mov_b32_e32 v153, v141
	v_pk_add_f32 v[142:143], v[154:155], v[138:139]
	s_nop 0
	v_pk_add_f32 v[144:145], v[142:143], v[142:143] op_sel:[0,1] op_sel_hi:[1,0]
	s_nop 0
	v_pk_add_f32 v[140:141], v[140:141], v[144:145] op_sel:[1,0] op_sel_hi:[0,1]
	v_mov_b32_e32 v143, v140
	v_pk_add_f32 v[150:151], v[142:143], v[152:153] neg_lo:[0,1] neg_hi:[0,1]
	v_mov_b32_e32 v139, v144
	v_sub_f32_e32 v141, v142, v150
	v_pk_add_f32 v[138:139], v[138:139], v[150:151] neg_lo:[0,1] neg_hi:[0,1]
	v_sub_f32_e32 v141, v152, v141
	v_add_f32_e32 v138, v138, v141
	v_add_f32_e32 v138, v138, v139
	v_add_f32_e32 v138, v140, v138
	v_cndmask_b32_e32 v138, v217, v138, vcc
	v_cmp_lt_f32_e64 vcc, |v134|, s92
	s_nop 1
	v_cndmask_b32_e32 v134, v138, v134, vcc

;     __device__ __forceinline__ void operator()(const f32x4 (&acc)[2][2][4][2], const pg8::Unit& u, int wr, int wc, int fr, int fq_in) const {
;     ...
;                         *(f32x4*)(rowp) = o0; *(f32x4*)(rowp + 4) = o1; }
.LBB0_469:
	s_or_b64 exec, exec, s[0:1]
	v_lshlrev_b64 v[138:139], 8, v[178:179]
	v_lshl_add_u64 v[138:139], s[38:39], 0, v[138:139]
	v_lshl_add_u64 v[138:139], v[146:147], 2, v[138:139]
	s_mov_b64 s[0:1], 0xb000
	v_lshl_add_u64 v[140:141], v[138:139], 0, s[0:1]
	v_add_co_u32_e32 v138, vcc, 0xb000, v138
	s_nop 1
	v_addc_co_u32_e32 v139, vcc, 0, v139, vcc
	global_store_dwordx4 v[138:139], v[134:137], off nt
	global_store_dwordx4 v[140:141], v[130:133], off offset:16 nt

; __device__ __forceinline__ unsigned cvt_pk_bf16(float lo, float hi) { unsigned r; asm volatile("v_cvt_pk_bf16_f32 %0, %1, %2" : "=v"(r) : "v"(lo), "v"(hi)); return r; }
;     __device__ __forceinline__ void operator()(const f32x4 (&acc)[2][2][4][2], const pg8::Unit& u, int wr, int wc, int fr, int fq_in) const {
;     ...
;         } else if (pn < 60) {
;             const int col0 = (pn - 44) * 256 + wc * 32 + 8 * fq;
; #pragma unroll
;             for (int ai = 0; ai < 2; ++ai)
; #pragma unroll
;                 for (int m = 0; m < 4; ++m) { bf16* rowp = Gt + (size_t)(row0 + ai * 128 + m * 16) * (2 * D) + col0;
; #pragma unroll
;                     for (int bj = 0; bj < 2; ++bj) { const f32x4 v0 = acc[ai][bj][m][0], v1 = acc[ai][bj][m][1];
;                         u32x4 w; w.x = pg8::cvt_pk_bf16(v0[0], v0[1]); w.y = pg8::cvt_pk_bf16(v0[2], v0[3]); w.z = pg8::cvt_pk_bf16(v1[0], v1[1]); w.w = pg8::cvt_pk_bf16(v1[2], v1[3]);
;                         *(u32x4*)(rowp + bj * 128) = w; } }
.LBB0_471:
	s_andn2_b64 vcc, exec, s[0:1]
	s_cbranch_vccnz .LBB0_473
	s_lshl_b32 s0, s62, 4
	s_add_i32 s0, s0, s64
	s_add_i32 s0, s0, 0xffffffd4
	s_lshl_b32 s0, s0, 17
	v_lshl_add_u32 v130, v0, 4, s0
	v_ashrrev_i32_e32 v179, 31, v178
	v_cvt_pk_bf16_f32 v132, v126, v127
	v_cvt_pk_bf16_f32 v133, v128, v129
	v_cvt_pk_bf16_f32 v134, v122, v123
	v_cvt_pk_bf16_f32 v135, v124, v125
	global_store_dwordx4 v130, v[132:135], s[36:37] nt
	s_nop 1
	v_cvt_pk_bf16_f32 v132, v114, v115
	v_cvt_pk_bf16_f32 v133, v116, v117
	v_cvt_pk_bf16_f32 v134, v106, v107
	v_cvt_pk_bf16_f32 v135, v108, v109
	v_add_u32_e32 v131, 0x2000, v130
	global_store_dwordx4 v131, v[132:135], s[36:37] nt
	s_nop 1
	v_cvt_pk_bf16_f32 v132, v118, v119
	v_cvt_pk_bf16_f32 v133, v120, v121
	v_cvt_pk_bf16_f32 v134, v110, v111
	v_cvt_pk_bf16_f32 v135, v112, v113
	v_add_u32_e32 v131, 0x4000, v130
	global_store_dwordx4 v131, v[132:135], s[36:37] nt
	s_nop 1
	v_cvt_pk_bf16_f32 v132, v98, v99
	v_cvt_pk_bf16_f32 v133, v100, v101
	v_cvt_pk_bf16_f32 v134, v90, v91
	v_cvt_pk_bf16_f32 v135, v92, v93
	v_add_u32_e32 v131, 0x6000, v130
	global_store_dwordx4 v131, v[132:135], s[36:37] nt
	s_nop 1
	v_cvt_pk_bf16_f32 v132, v102, v103
	v_cvt_pk_bf16_f32 v133, v104, v105
	v_cvt_pk_bf16_f32 v134, v94, v95
	v_cvt_pk_bf16_f32 v135, v96, v97
	v_add_u32_e32 v131, 0x8000, v130
	global_store_dwordx4 v131, v[132:135], s[36:37] nt
	s_nop 1
	v_cvt_pk_bf16_f32 v132, v82, v83
	v_cvt_pk_bf16_f32 v133, v84, v85
	v_cvt_pk_bf16_f32 v134, v74, v75
	v_cvt_pk_bf16_f32 v135, v76, v77
	v_add_u32_e32 v131, 0xa000, v130
	global_store_dwordx4 v131, v[132:135], s[36:37] nt
	s_nop 1
	v_cvt_pk_bf16_f32 v132, v86, v87
	v_cvt_pk_bf16_f32 v133, v88, v89
	v_cvt_pk_bf16_f32 v134, v78, v79
	v_cvt_pk_bf16_f32 v135, v80, v81
	v_add_u32_e32 v131, 0xc000, v130
	global_store_dwordx4 v131, v[132:135], s[36:37] nt
	s_nop 1
	v_cvt_pk_bf16_f32 v132, v70, v71
	v_cvt_pk_bf16_f32 v133, v72, v73
	v_cvt_pk_bf16_f32 v134, v66, v67
	v_cvt_pk_bf16_f32 v135, v68, v69
	v_add_u32_e32 v131, 0xe000, v130
	global_store_dwordx4 v131, v[132:135], s[36:37] nt
	s_nop 1
	v_cvt_pk_bf16_f32 v132, v62, v63
	v_cvt_pk_bf16_f32 v133, v64, v65
	v_cvt_pk_bf16_f32 v134, v58, v59
	v_cvt_pk_bf16_f32 v135, v60, v61
	v_add_u32_e32 v131, 0x10000, v130
	global_store_dwordx4 v131, v[132:135], s[36:37] nt
	s_nop 1
	v_cvt_pk_bf16_f32 v132, v50, v51
	v_cvt_pk_bf16_f32 v133, v52, v53
	v_cvt_pk_bf16_f32 v134, v42, v43
	v_cvt_pk_bf16_f32 v135, v44, v45
	v_add_u32_e32 v131, 0x12000, v130
	global_store_dwordx4 v131, v[132:135], s[36:37] nt
	s_nop 1
	v_cvt_pk_bf16_f32 v132, v54, v55
	v_cvt_pk_bf16_f32 v133, v56, v57
	v_cvt_pk_bf16_f32 v134, v46, v47
	v_cvt_pk_bf16_f32 v135, v48, v49
	v_add_u32_e32 v131, 0x14000, v130
	global_store_dwordx4 v131, v[132:135], s[36:37] nt
	s_nop 1
	v_cvt_pk_bf16_f32 v132, v34, v35
	v_cvt_pk_bf16_f32 v133, v36, v37
	v_cvt_pk_bf16_f32 v134, v26, v27
	v_cvt_pk_bf16_f32 v135, v28, v29
	v_add_u32_e32 v131, 0x16000, v130
	global_store_dwordx4 v131, v[132:135], s[36:37] nt
	s_nop 1
	v_cvt_pk_bf16_f32 v132, v38, v39
	v_cvt_pk_bf16_f32 v133, v40, v41
	v_cvt_pk_bf16_f32 v134, v30, v31
	v_cvt_pk_bf16_f32 v135, v32, v33
	v_add_u32_e32 v131, 0x18000, v130
	global_store_dwordx4 v131, v[132:135], s[36:37] nt
	s_nop 1
	v_cvt_pk_bf16_f32 v132, v18, v19
	v_cvt_pk_bf16_f32 v133, v20, v21
	v_cvt_pk_bf16_f32 v134, v10, v11
	v_cvt_pk_bf16_f32 v135, v12, v13
	v_add_u32_e32 v131, 0x1a000, v130
	global_store_dwordx4 v131, v[132:135], s[36:37] nt
	s_nop 1
	v_cvt_pk_bf16_f32 v132, v22, v23
	v_cvt_pk_bf16_f32 v133, v24, v25
	v_cvt_pk_bf16_f32 v134, v14, v15
	v_cvt_pk_bf16_f32 v135, v16, v17
	v_add_u32_e32 v131, 0x1c000, v130
	global_store_dwordx4 v131, v[132:135], s[36:37] nt
	s_nop 1
	v_cvt_pk_bf16_f32 v132, v6, v7
	v_cvt_pk_bf16_f32 v133, v8, v9
	v_cvt_pk_bf16_f32 v134, v2, v3
	v_cvt_pk_bf16_f32 v135, v4, v5
	v_add_u32_e32 v131, 0x1e000, v130
	global_store_dwordx4 v131, v[132:135], s[36:37] nt

; #define LAS __attribute__((address_space(3)))
; __device__ __forceinline__ float dpp_ror1(float v) { return __builtin_bit_cast(float, __builtin_amdgcn_update_dpp(0, __builtin_bit_cast(int, v), 0x121, 0xf, 0xf, false)); }
; __device__ __forceinline__ float dpp_ror15(float v) { return __builtin_bit_cast(float, __builtin_amdgcn_update_dpp(0, __builtin_bit_cast(int, v), 0x12F, 0xf, 0xf, false)); }
;     __device__ __forceinline__ void operator()(const f32x4 (&acc)[2][2][4][2], const pg8::Unit& u, int wr, int wc, int fr, int fq_in) const {
;     ...
;         } else if (pn < 44) {
;             const int ch = (pn - 12) * 64 + wc * 16 + 4 * fq;
;             const f32x4 w0 = *(const LAS f32x4*)(scw_lds + ch), w1 = *(const LAS f32x4*)(scw_lds + D + ch), w2 = *(const LAS f32x4*)(scw_lds + 2 * D + ch);
; #pragma unroll
;             for (int ai = 0; ai < 2; ++ai) {
;                 f32x4 cv[4];
; #pragma unroll
;                 for (int m = 0; m < 4; ++m) cv[m] = acc[ai][0][m][1] * acc[ai][1][m][0];
;                 f32x4 o[4];
; #pragma unroll
;                 for (int q = 0; q < 4; ++q) { float A[4], B[4];
; #pragma unroll
;                     for (int m = 0; m < 4; ++m) { A[m] = dpp_ror1(cv[m][q]); B[m] = dpp_ror15(cv[m][q]); }
; #pragma unroll
;                     for (int m = 0; m < 4; ++m) { const float pv = fr > 0 ? A[m] : (m > 0 ? A[m > 0 ? m - 1 : 0] : 0.f), nv = fr < 15 ? B[m] : (m < 3 ? B[m < 3 ? m + 1 : 3] : 0.f);
;                         o[m][q] = acc[ai][0][m][0][q] * (w0[q] * pv + w1[q] * cv[m][q] + w2[q] * nv); } }
.LBB0_474:
	s_andn2_b64 vcc, exec, s[0:1]
	s_cbranch_vccnz .LBB0_476
	s_lshl_b32 s0, s64, 6
	s_add_i32 s0, s78, s0
	v_lshl_add_u32 v146, v148, 2, s0
	v_lshl_add_u32 v134, v146, 2, 0
	v_add_u32_e32 v130, 0x20000, v134
	v_add_u32_e32 v131, 0x22000, v134
	v_add_u32_e32 v134, 0x24000, v134
	ds_read_b128 v[138:141], v130
	ds_read_b128 v[130:133], v131
	ds_read_b128 v[134:137], v134
	v_pk_mul_f32 v[144:145], v[122:123], v[114:115]
	v_pk_mul_f32 v[154:155], v[110:111], v[98:99]
	v_mov_b32_e32 v149, v171
	v_mov_b32_e32 v170, v171
	v_mov_b32_e32 v179, v171
	v_mov_b32_dpp v149, v144 row_ror:1 row_mask:0xf bank_mask:0xf
	v_mov_b32_dpp v170, v144 row_ror:15 row_mask:0xf bank_mask:0xf
	v_mov_b32_dpp v179, v154 row_ror:15 row_mask:0xf bank_mask:0xf
	s_waitcnt lgkmcnt(2)
	v_mov_b32_e32 v142, v138
	s_waitcnt lgkmcnt(0)
	v_mov_b32_e32 v143, v134
	v_cndmask_b32_e64 v183, v170, v179, s[12:13]
	v_cndmask_b32_e64 v182, v149, 0, s[14:15]
	v_pk_mul_f32 v[158:159], v[94:95], v[82:83]
	v_mov_b32_e32 v177, v171
	v_mov_b32_e32 v185, v171
	v_pk_mul_f32 v[182:183], v[142:143], v[182:183]
	v_mov_b32_dpp v177, v154 row_ror:1 row_mask:0xf bank_mask:0xf
	v_mov_b32_dpp v185, v158 row_ror:15 row_mask:0xf bank_mask:0xf
	v_fma_f32 v134, v144, v130, v182
	v_add_f32_e32 v134, v134, v183
	v_cndmask_b32_e64 v183, v179, v185, s[12:13]
	v_cndmask_b32_e64 v182, v177, v149, s[14:15]
	v_pk_mul_f32 v[180:181], v[78:79], v[70:71]
	v_mov_b32_e32 v184, v171
	v_mov_b32_e32 v189, v171
	v_pk_mul_f32 v[182:183], v[142:143], v[182:183]
	v_mov_b32_dpp v184, v158 row_ror:1 row_mask:0xf bank_mask:0xf
	v_mov_b32_dpp v189, v180 row_ror:15 row_mask:0xf bank_mask:0xf
	v_mul_f32_e32 v170, v126, v134
	v_fma_f32 v134, v154, v130, v182
	v_add_f32_e32 v134, v134, v183
	v_cndmask_b32_e64 v183, v185, v189, s[12:13]
	v_cndmask_b32_e64 v182, v184, v177, s[14:15]
	v_mov_b32_e32 v188, v171
	v_pk_mul_f32 v[182:183], v[142:143], v[182:183]
	v_mul_f32_e32 v149, v118, v134
	v_mov_b32_dpp v188, v180 row_ror:1 row_mask:0xf bank_mask:0xf
	v_fma_f32 v134, v158, v130, v182
	v_add_f32_e32 v134, v134, v183
	v_cndmask_b32_e64 v182, v188, v184, s[14:15]
	v_cndmask_b32_e64 v183, v189, 0, s[12:13]
	v_pk_mul_f32 v[182:183], v[142:143], v[182:183]
	v_mul_f32_e32 v154, v102, v134
	v_fma_f32 v134, v180, v130, v182
	v_mov_b32_e32 v144, v171
	v_mov_b32_e32 v138, v171
	v_mov_b32_e32 v179, v171
	v_add_f32_e32 v134, v183, v134
	v_mov_b32_dpp v144, v145 row_ror:1 row_mask:0xf bank_mask:0xf
	v_mov_b32_dpp v138, v145 row_ror:15 row_mask:0xf bank_mask:0xf
	v_mov_b32_dpp v179, v155 row_ror:15 row_mask:0xf bank_mask:0xf
	v_mul_f32_e32 v158, v86, v134
	v_mov_b32_e32 v134, v139
	v_cndmask_b32_e64 v139, v138, v179, s[12:13]
	v_cndmask_b32_e64 v138, v144, 0, s[14:15]
	v_pk_mul_f32 v[138:139], v[134:135], v[138:139]
	v_mov_b32_e32 v177, v171
	v_mov_b32_e32 v182, v171
	v_fma_f32 v138, v145, v131, v138
	v_mov_b32_dpp v177, v155 row_ror:1 row_mask:0xf bank_mask:0xf
	v_mov_b32_dpp v182, v159 row_ror:15 row_mask:0xf bank_mask:0xf
	v_add_f32_e32 v138, v138, v139
	v_mul_f32_e32 v185, v127, v138
	v_cndmask_b32_e64 v139, v179, v182, s[12:13]
	v_cndmask_b32_e64 v138, v177, v144, s[14:15]
	v_pk_mul_f32 v[138:139], v[134:135], v[138:139]
	v_mov_b32_e32 v180, v171
	v_mov_b32_e32 v184, v171
	v_fma_f32 v138, v155, v131, v138
	v_mov_b32_dpp v180, v159 row_ror:1 row_mask:0xf bank_mask:0xf
	v_mov_b32_dpp v184, v181 row_ror:15 row_mask:0xf bank_mask:0xf
	v_add_f32_e32 v138, v138, v139
	v_mul_f32_e32 v155, v119, v138
	v_cndmask_b32_e64 v139, v182, v184, s[12:13]
	v_cndmask_b32_e64 v138, v180, v177, s[14:15]
	v_pk_mul_f32 v[138:139], v[134:135], v[138:139]
	v_mov_b32_e32 v183, v171
	v_fma_f32 v138, v159, v131, v138
	v_add_f32_e32 v138, v138, v139
	v_mov_b32_dpp v183, v181 row_ror:1 row_mask:0xf bank_mask:0xf
	v_mul_f32_e32 v159, v103, v138
	v_cndmask_b32_e64 v138, v183, v180, s[14:15]
	v_cndmask_b32_e64 v139, v184, 0, s[12:13]
	v_pk_mul_f32 v[138:139], v[134:135], v[138:139]
	v_pk_mul_f32 v[150:151], v[124:125], v[116:117]
	v_fma_f32 v138, v181, v131, v138
	v_add_f32_e32 v138, v139, v138
	v_pk_mul_f32 v[152:153], v[112:113], v[100:101]
	v_mul_f32_e32 v177, v87, v138
	v_mov_b32_e32 v179, v171
	v_mov_b32_e32 v138, v171
	v_mov_b32_e32 v181, v171
	v_mov_b32_dpp v179, v150 row_ror:1 row_mask:0xf bank_mask:0xf
	v_mov_b32_dpp v138, v150 row_ror:15 row_mask:0xf bank_mask:0xf
	v_mov_b32_dpp v181, v152 row_ror:15 row_mask:0xf bank_mask:0xf
	v_mov_b32_e32 v144, v140
	v_mov_b32_e32 v145, v136
	v_cndmask_b32_e64 v139, v138, v181, s[12:13]
	v_cndmask_b32_e64 v138, v179, 0, s[14:15]
	v_pk_mul_f32 v[156:157], v[96:97], v[84:85]
	v_mov_b32_e32 v180, v171
	v_mov_b32_e32 v183, v171
	v_pk_mul_f32 v[138:139], v[144:145], v[138:139]
	v_mov_b32_dpp v180, v152 row_ror:1 row_mask:0xf bank_mask:0xf
	v_mov_b32_dpp v183, v156 row_ror:15 row_mask:0xf bank_mask:0xf
	v_fma_f32 v136, v150, v132, v138
	v_add_f32_e32 v136, v136, v139
	v_cndmask_b32_e64 v139, v181, v183, s[12:13]
	v_cndmask_b32_e64 v138, v180, v179, s[14:15]
	v_pk_mul_f32 v[160:161], v[80:81], v[72:73]
	v_mov_b32_e32 v182, v171
	v_mov_b32_e32 v188, v171
	v_pk_mul_f32 v[138:139], v[144:145], v[138:139]
	v_mov_b32_dpp v182, v156 row_ror:1 row_mask:0xf bank_mask:0xf
	v_mov_b32_dpp v188, v160 row_ror:15 row_mask:0xf bank_mask:0xf
	v_mul_f32_e32 v140, v128, v136
	v_fma_f32 v136, v152, v132, v138
	v_add_f32_e32 v136, v136, v139
	v_cndmask_b32_e64 v139, v183, v188, s[12:13]
	v_cndmask_b32_e64 v138, v182, v180, s[14:15]
	v_mov_b32_e32 v184, v171
	v_pk_mul_f32 v[138:139], v[144:145], v[138:139]
	v_mul_f32_e32 v181, v120, v136
	v_mov_b32_dpp v184, v160 row_ror:1 row_mask:0xf bank_mask:0xf
	v_fma_f32 v136, v156, v132, v138
; __device__ __forceinline__ unsigned cvt_pk_bf16(float lo, float hi) { unsigned r; asm volatile("v_cvt_pk_bf16_f32 %0, %1, %2" : "=v"(r) : "v"(lo), "v"(hi)); return r; }
; __device__ __forceinline__ float dpp_ror1(float v) { return __builtin_bit_cast(float, __builtin_amdgcn_update_dpp(0, __builtin_bit_cast(int, v), 0x121, 0xf, 0xf, false)); }
; __device__ __forceinline__ float dpp_ror15(float v) { return __builtin_bit_cast(float, __builtin_amdgcn_update_dpp(0, __builtin_bit_cast(int, v), 0x12F, 0xf, 0xf, false)); }
;     __device__ __forceinline__ void operator()(const f32x4 (&acc)[2][2][4][2], const pg8::Unit& u, int wr, int wc, int fr, int fq_in) const {
;     ...
;                 for (int q = 0; q < 4; ++q) { float A[4], B[4];
; #pragma unroll
;                     for (int m = 0; m < 4; ++m) { A[m] = dpp_ror1(cv[m][q]); B[m] = dpp_ror15(cv[m][q]); }
; #pragma unroll
;                     for (int m = 0; m < 4; ++m) { const float pv = fr > 0 ? A[m] : (m > 0 ? A[m > 0 ? m - 1 : 0] : 0.f), nv = fr < 15 ? B[m] : (m < 3 ? B[m < 3 ? m + 1 : 3] : 0.f);
;                         o[m][q] = acc[ai][0][m][0][q] * (w0[q] * pv + w1[q] * cv[m][q] + w2[q] * nv); } }
; #pragma unroll
;                 for (int m = 0; m < 4; ++m) { const size_t row = (size_t)(row0 + ai * 128 + m * 16); const f32x4 zz = acc[ai][1][m][1];
;                     v2u ws_; ws_.x = pg8::cvt_pk_bf16(o[m][0], o[m][1]); ws_.y = pg8::cvt_pk_bf16(o[m][2], o[m][3]); *(v2u*)(SCY + row * D + ch) = ws_;
;                     v2u wz; wz.x = pg8::cvt_pk_bf16(zz[0], zz[1]); wz.y = pg8::cvt_pk_bf16(zz[2], zz[3]); *(v2u*)(Z + row * D + ch) = wz; }
	v_add_f32_e32 v136, v136, v139
	v_cndmask_b32_e64 v138, v184, v182, s[14:15]
	v_cndmask_b32_e64 v139, v188, 0, s[12:13]
	v_pk_mul_f32 v[138:139], v[144:145], v[138:139]
	v_mul_f32_e32 v156, v104, v136
	v_fma_f32 v136, v160, v132, v138
	v_mov_b32_e32 v150, v171
	v_mov_b32_e32 v138, v171
	v_mov_b32_e32 v179, v171
	v_add_f32_e32 v136, v139, v136
	v_mov_b32_dpp v150, v151 row_ror:1 row_mask:0xf bank_mask:0xf
	v_mov_b32_dpp v138, v151 row_ror:15 row_mask:0xf bank_mask:0xf
	v_mov_b32_dpp v179, v153 row_ror:15 row_mask:0xf bank_mask:0xf
	v_mul_f32_e32 v160, v88, v136
	v_mov_b32_e32 v136, v141
	v_cndmask_b32_e64 v139, v138, v179, s[12:13]
	v_cndmask_b32_e64 v138, v150, 0, s[14:15]
	v_pk_mul_f32 v[138:139], v[136:137], v[138:139]
	v_mov_b32_e32 v152, v171
	v_mov_b32_e32 v182, v171
	v_fma_f32 v138, v151, v133, v138
	v_mov_b32_dpp v152, v153 row_ror:1 row_mask:0xf bank_mask:0xf
	v_mov_b32_dpp v182, v157 row_ror:15 row_mask:0xf bank_mask:0xf
	v_add_f32_e32 v138, v138, v139
	v_mul_f32_e32 v141, v129, v138
	v_cndmask_b32_e64 v139, v179, v182, s[12:13]
	v_cndmask_b32_e64 v138, v152, v150, s[14:15]
	v_pk_mul_f32 v[138:139], v[136:137], v[138:139]
	v_mov_b32_e32 v180, v171
	v_mov_b32_e32 v184, v171
	v_fma_f32 v138, v153, v133, v138
	v_mov_b32_dpp v180, v157 row_ror:1 row_mask:0xf bank_mask:0xf
	v_mov_b32_dpp v184, v161 row_ror:15 row_mask:0xf bank_mask:0xf
	v_add_f32_e32 v138, v138, v139
	v_mul_f32_e32 v188, v121, v138
	v_cndmask_b32_e64 v139, v182, v184, s[12:13]
	v_cndmask_b32_e64 v138, v180, v152, s[14:15]
	v_pk_mul_f32 v[138:139], v[136:137], v[138:139]
	v_mov_b32_e32 v183, v171
	v_fma_f32 v138, v157, v133, v138
	v_add_f32_e32 v138, v138, v139
	v_mov_b32_dpp v183, v161 row_ror:1 row_mask:0xf bank_mask:0xf
	v_mul_f32_e32 v157, v105, v138
	v_cndmask_b32_e64 v138, v183, v180, s[14:15]
	v_cndmask_b32_e64 v139, v184, 0, s[12:13]
	v_pk_mul_f32 v[138:139], v[136:137], v[138:139]
	v_ashrrev_i32_e32 v179, 31, v178
	v_fma_f32 v138, v161, v133, v138
	v_ashrrev_i32_e32 v147, 31, v146
	v_add_f32_e32 v138, v139, v138
	v_cvt_pk_bf16_f32 v150, v170, v185
	v_cvt_pk_bf16_f32 v151, v140, v141
	v_lshlrev_b64 v[140:141], 12, v[178:179]
	v_mul_f32_e32 v161, v89, v138
	v_lshl_add_u64 v[152:153], s[34:35], 0, v[140:141]
	v_lshlrev_b64 v[138:139], 1, v[146:147]
	v_lshl_add_u64 v[146:147], v[152:153], 0, v[138:139]
	global_store_dwordx2 v[146:147], v[150:151], off nt
	v_lshl_add_u64 v[150:151], s[26:27], 0, v[140:141]
	v_cvt_pk_bf16_f32 v146, v106, v107
	v_lshl_add_u64 v[150:151], v[150:151], 0, v[138:139]
	v_cvt_pk_bf16_f32 v147, v108, v109
	global_store_dwordx2 v[150:151], v[146:147], off nt
	v_or_b32_e32 v146, 16, v178
	v_ashrrev_i32_e32 v147, 31, v146
	v_lshlrev_b64 v[146:147], 12, v[146:147]
	v_lshl_add_u64 v[152:153], s[34:35], 0, v[146:147]
	v_lshl_add_u64 v[146:147], s[26:27], 0, v[146:147]
	v_cvt_pk_bf16_f32 v150, v149, v155
	v_cvt_pk_bf16_f32 v151, v181, v188
	v_lshl_add_u64 v[152:153], v[152:153], 0, v[138:139]
	v_lshl_add_u64 v[146:147], v[146:147], 0, v[138:139]
	global_store_dwordx2 v[152:153], v[150:151], off nt
	v_cvt_pk_bf16_f32 v150, v90, v91
	v_cvt_pk_bf16_f32 v151, v92, v93
	global_store_dwordx2 v[146:147], v[150:151], off nt
	v_or_b32_e32 v146, 32, v178
	v_ashrrev_i32_e32 v147, 31, v146
	v_lshlrev_b64 v[146:147], 12, v[146:147]
	v_lshl_add_u64 v[152:153], s[34:35], 0, v[146:147]
	v_lshl_add_u64 v[146:147], s[26:27], 0, v[146:147]
	v_cvt_pk_bf16_f32 v150, v154, v159
	v_cvt_pk_bf16_f32 v151, v156, v157
	v_lshl_add_u64 v[152:153], v[152:153], 0, v[138:139]
	v_lshl_add_u64 v[146:147], v[146:147], 0, v[138:139]
	global_store_dwordx2 v[152:153], v[150:151], off nt
	v_cvt_pk_bf16_f32 v150, v74, v75
	v_cvt_pk_bf16_f32 v151, v76, v77
	global_store_dwordx2 v[146:147], v[150:151], off nt
	v_or_b32_e32 v146, 48, v178
	v_ashrrev_i32_e32 v147, 31, v146
	v_lshlrev_b64 v[146:147], 12, v[146:147]
	v_lshl_add_u64 v[152:153], s[34:35], 0, v[146:147]
	v_cvt_pk_bf16_f32 v150, v158, v177
	v_cvt_pk_bf16_f32 v151, v160, v161
	v_lshl_add_u64 v[152:153], v[152:153], 0, v[138:139]
	v_lshl_add_u64 v[146:147], s[26:27], 0, v[146:147]
	global_store_dwordx2 v[152:153], v[150:151], off nt
	v_cvt_pk_bf16_f32 v150, v66, v67
	v_cvt_pk_bf16_f32 v151, v68, v69
	v_lshl_add_u64 v[146:147], v[146:147], 0, v[138:139]
	global_store_dwordx2 v[146:147], v[150:151], off nt
	v_pk_mul_f32 v[150:151], v[58:59], v[50:51]
	v_pk_mul_f32 v[154:155], v[46:47], v[34:35]
	v_mov_b32_e32 v149, v171
	v_mov_b32_e32 v170, v171
	v_mov_b32_e32 v179, v171
	v_mov_b32_dpp v149, v150 row_ror:1 row_mask:0xf bank_mask:0xf
	v_mov_b32_dpp v170, v150 row_ror:15 row_mask:0xf bank_mask:0xf
	v_mov_b32_dpp v179, v154 row_ror:15 row_mask:0xf bank_mask:0xf
	v_cndmask_b32_e64 v183, v170, v179, s[12:13]
	v_cndmask_b32_e64 v182, v149, 0, s[14:15]
	v_pk_mul_f32 v[158:159], v[30:31], v[18:19]
	v_mov_b32_e32 v177, v171
	v_mov_b32_e32 v185, v171
	v_pk_mul_f32 v[182:183], v[142:143], v[182:183]
	v_mov_b32_dpp v177, v154 row_ror:1 row_mask:0xf bank_mask:0xf
	v_mov_b32_dpp v185, v158 row_ror:15 row_mask:0xf bank_mask:0xf
	v_fma_f32 v150, v150, v130, v182
	v_add_f32_e32 v150, v150, v183
	v_cndmask_b32_e64 v183, v179, v185, s[12:13]
	v_cndmask_b32_e64 v182, v177, v149, s[14:15]
	v_pk_mul_f32 v[180:181], v[14:15], v[6:7]
	v_mov_b32_e32 v184, v171
	v_mov_b32_e32 v189, v171
	v_pk_mul_f32 v[182:183], v[142:143], v[182:183]
	v_mov_b32_dpp v184, v158 row_ror:1 row_mask:0xf bank_mask:0xf
	v_mov_b32_dpp v189, v180 row_ror:15 row_mask:0xf bank_mask:0xf
	v_fma_f32 v149, v154, v130, v182
	v_add_f32_e32 v149, v149, v183
	v_cndmask_b32_e64 v183, v185, v189, s[12:13]
	v_cndmask_b32_e64 v182, v184, v177, s[14:15]
	v_mov_b32_e32 v188, v171
; __device__ __forceinline__ float dpp_ror1(float v) { return __builtin_bit_cast(float, __builtin_amdgcn_update_dpp(0, __builtin_bit_cast(int, v), 0x121, 0xf, 0xf, false)); }
; __device__ __forceinline__ float dpp_ror15(float v) { return __builtin_bit_cast(float, __builtin_amdgcn_update_dpp(0, __builtin_bit_cast(int, v), 0x12F, 0xf, 0xf, false)); }
;     __device__ __forceinline__ void operator()(const f32x4 (&acc)[2][2][4][2], const pg8::Unit& u, int wr, int wc, int fr, int fq_in) const {
;     ...
;                 f32x4 cv[4];
; #pragma unroll
;                 for (int m = 0; m < 4; ++m) cv[m] = acc[ai][0][m][1] * acc[ai][1][m][0];
;                 f32x4 o[4];
; #pragma unroll
;                 for (int q = 0; q < 4; ++q) { float A[4], B[4];
; #pragma unroll
;                     for (int m = 0; m < 4; ++m) { A[m] = dpp_ror1(cv[m][q]); B[m] = dpp_ror15(cv[m][q]); }
; #pragma unroll
;                     for (int m = 0; m < 4; ++m) { const float pv = fr > 0 ? A[m] : (m > 0 ? A[m > 0 ? m - 1 : 0] : 0.f), nv = fr < 15 ? B[m] : (m < 3 ? B[m < 3 ? m + 1 : 3] : 0.f);
;                         o[m][q] = acc[ai][0][m][0][q] * (w0[q] * pv + w1[q] * cv[m][q] + w2[q] * nv); } }
	v_pk_mul_f32 v[182:183], v[142:143], v[182:183]
	v_mov_b32_e32 v177, v171
	v_mov_b32_dpp v188, v180 row_ror:1 row_mask:0xf bank_mask:0xf
	v_fma_f32 v154, v158, v130, v182
	v_add_f32_e32 v154, v154, v183
	v_cndmask_b32_e64 v182, v188, v184, s[14:15]
	v_cndmask_b32_e64 v183, v189, 0, s[12:13]
	v_pk_mul_f32 v[142:143], v[142:143], v[182:183]
	v_mov_b32_dpp v177, v155 row_ror:15 row_mask:0xf bank_mask:0xf
	v_fma_f32 v130, v180, v130, v142
	v_add_f32_e32 v130, v143, v130
	v_mul_f32_e32 v158, v22, v130
	v_mov_b32_e32 v130, v171
	v_mov_b32_e32 v142, v171
	v_mov_b32_e32 v170, v171
	v_mov_b32_dpp v130, v151 row_ror:1 row_mask:0xf bank_mask:0xf
	v_mov_b32_dpp v142, v151 row_ror:15 row_mask:0xf bank_mask:0xf
	v_cndmask_b32_e64 v143, v142, v177, s[12:13]
	v_cndmask_b32_e64 v142, v130, 0, s[14:15]
	v_pk_mul_f32 v[142:143], v[134:135], v[142:143]
	v_mov_b32_e32 v180, v171
	v_fma_f32 v142, v151, v131, v142
	v_mov_b32_dpp v170, v155 row_ror:1 row_mask:0xf bank_mask:0xf
	v_mov_b32_dpp v180, v159 row_ror:15 row_mask:0xf bank_mask:0xf
	v_add_f32_e32 v142, v142, v143
	v_mul_f32_e32 v151, v63, v142
	v_cndmask_b32_e64 v143, v177, v180, s[12:13]
	v_cndmask_b32_e64 v142, v170, v130, s[14:15]
	v_mov_b32_e32 v179, v171
	v_mov_b32_e32 v183, v171
	v_pk_mul_f32 v[142:143], v[134:135], v[142:143]
	v_mov_b32_dpp v179, v159 row_ror:1 row_mask:0xf bank_mask:0xf
	v_mov_b32_dpp v183, v181 row_ror:15 row_mask:0xf bank_mask:0xf
	v_fma_f32 v130, v155, v131, v142
	v_add_f32_e32 v130, v130, v143
	v_cndmask_b32_e64 v143, v180, v183, s[12:13]
	v_cndmask_b32_e64 v142, v179, v170, s[14:15]
	v_mov_b32_e32 v182, v171
	v_pk_mul_f32 v[142:143], v[134:135], v[142:143]
	v_mul_f32_e32 v155, v55, v130
	v_mov_b32_dpp v182, v181 row_ror:1 row_mask:0xf bank_mask:0xf
	v_fma_f32 v130, v159, v131, v142
	v_add_f32_e32 v130, v130, v143
	v_cndmask_b32_e64 v142, v182, v179, s[14:15]
	v_cndmask_b32_e64 v143, v183, 0, s[12:13]
	v_pk_mul_f32 v[134:135], v[134:135], v[142:143]
	v_mul_f32_e32 v159, v39, v130
	v_fma_f32 v130, v181, v131, v134
	v_add_f32_e32 v130, v135, v130
	v_pk_mul_f32 v[146:147], v[60:61], v[52:53]
	v_pk_mul_f32 v[152:153], v[48:49], v[36:37]
	v_mul_f32_e32 v142, v23, v130
	v_mov_b32_e32 v134, v171
	v_mov_b32_e32 v130, v171
	v_mov_b32_e32 v143, v171
	v_mov_b32_dpp v134, v146 row_ror:1 row_mask:0xf bank_mask:0xf
	v_mov_b32_dpp v130, v146 row_ror:15 row_mask:0xf bank_mask:0xf
	v_mov_b32_dpp v143, v152 row_ror:15 row_mask:0xf bank_mask:0xf
	v_cndmask_b32_e64 v131, v130, v143, s[12:13]
	v_cndmask_b32_e64 v130, v134, 0, s[14:15]
	v_pk_mul_f32 v[130:131], v[144:145], v[130:131]
	v_pk_mul_f32 v[156:157], v[32:33], v[20:21]
	v_mov_b32_e32 v135, v171
	v_mov_b32_e32 v177, v171
	v_fma_f32 v130, v146, v132, v130
	v_mov_b32_dpp v135, v152 row_ror:1 row_mask:0xf bank_mask:0xf
	v_mov_b32_dpp v177, v156 row_ror:15 row_mask:0xf bank_mask:0xf
	v_add_f32_e32 v130, v130, v131
	v_mul_f32_e32 v146, v64, v130
	v_cndmask_b32_e64 v131, v143, v177, s[12:13]
	v_cndmask_b32_e64 v130, v135, v134, s[14:15]
	v_pk_mul_f32 v[130:131], v[144:145], v[130:131]
	v_pk_mul_f32 v[160:161], v[16:17], v[8:9]
	v_mov_b32_e32 v170, v171
	v_mov_b32_e32 v180, v171
	v_fma_f32 v130, v152, v132, v130
	v_mov_b32_dpp v170, v156 row_ror:1 row_mask:0xf bank_mask:0xf
	v_mov_b32_dpp v180, v160 row_ror:15 row_mask:0xf bank_mask:0xf
	v_add_f32_e32 v130, v130, v131
	v_mul_f32_e32 v143, v56, v130
	v_cndmask_b32_e64 v131, v177, v180, s[12:13]
	v_cndmask_b32_e64 v130, v170, v135, s[14:15]
	v_pk_mul_f32 v[130:131], v[144:145], v[130:131]
	v_mov_b32_e32 v179, v171
	v_fma_f32 v130, v156, v132, v130
	v_add_f32_e32 v130, v130, v131
	v_mov_b32_dpp v179, v160 row_ror:1 row_mask:0xf bank_mask:0xf
	v_mul_f32_e32 v152, v40, v130
	v_cndmask_b32_e64 v130, v179, v170, s[14:15]
	v_cndmask_b32_e64 v131, v180, 0, s[12:13]
	v_pk_mul_f32 v[130:131], v[144:145], v[130:131]
	v_mov_b32_e32 v135, v171
	v_fma_f32 v130, v160, v132, v130
	v_add_f32_e32 v130, v131, v130
; __device__ __forceinline__ unsigned cvt_pk_bf16(float lo, float hi) { unsigned r; asm volatile("v_cvt_pk_bf16_f32 %0, %1, %2" : "=v"(r) : "v"(lo), "v"(hi)); return r; }
; __device__ __forceinline__ float dpp_ror1(float v) { return __builtin_bit_cast(float, __builtin_amdgcn_update_dpp(0, __builtin_bit_cast(int, v), 0x121, 0xf, 0xf, false)); }
; __device__ __forceinline__ float dpp_ror15(float v) { return __builtin_bit_cast(float, __builtin_amdgcn_update_dpp(0, __builtin_bit_cast(int, v), 0x12F, 0xf, 0xf, false)); }
;     __device__ __forceinline__ void operator()(const f32x4 (&acc)[2][2][4][2], const pg8::Unit& u, int wr, int wc, int fr, int fq_in) const {
;     ...
;                 for (int q = 0; q < 4; ++q) { float A[4], B[4];
; #pragma unroll
;                     for (int m = 0; m < 4; ++m) { A[m] = dpp_ror1(cv[m][q]); B[m] = dpp_ror15(cv[m][q]); }
; #pragma unroll
;                     for (int m = 0; m < 4; ++m) { const float pv = fr > 0 ? A[m] : (m > 0 ? A[m > 0 ? m - 1 : 0] : 0.f), nv = fr < 15 ? B[m] : (m < 3 ? B[m < 3 ? m + 1 : 3] : 0.f);
;                         o[m][q] = acc[ai][0][m][0][q] * (w0[q] * pv + w1[q] * cv[m][q] + w2[q] * nv); } }
; #pragma unroll
;                 for (int m = 0; m < 4; ++m) { const size_t row = (size_t)(row0 + ai * 128 + m * 16); const f32x4 zz = acc[ai][1][m][1];
;                     v2u ws_; ws_.x = pg8::cvt_pk_bf16(o[m][0], o[m][1]); ws_.y = pg8::cvt_pk_bf16(o[m][2], o[m][3]); *(v2u*)(SCY + row * D + ch) = ws_;
;                     v2u wz; wz.x = pg8::cvt_pk_bf16(zz[0], zz[1]); wz.y = pg8::cvt_pk_bf16(zz[2], zz[3]); *(v2u*)(Z + row * D + ch) = wz; }
	v_mul_f32_e32 v144, v24, v130
	v_mov_b32_e32 v132, v171
	v_mov_b32_e32 v130, v171
	v_mov_b32_dpp v135, v153 row_ror:15 row_mask:0xf bank_mask:0xf
	v_mov_b32_dpp v132, v147 row_ror:1 row_mask:0xf bank_mask:0xf
	v_mov_b32_dpp v130, v147 row_ror:15 row_mask:0xf bank_mask:0xf
	v_cndmask_b32_e64 v131, v130, v135, s[12:13]
	v_cndmask_b32_e64 v130, v132, 0, s[14:15]
	v_pk_mul_f32 v[130:131], v[136:137], v[130:131]
	v_mov_b32_e32 v134, v171
	v_mov_b32_e32 v156, v171
	v_fma_f32 v130, v147, v133, v130
	v_mov_b32_dpp v134, v153 row_ror:1 row_mask:0xf bank_mask:0xf
	v_mov_b32_dpp v156, v157 row_ror:15 row_mask:0xf bank_mask:0xf
	v_add_f32_e32 v130, v130, v131
	v_mul_f32_e32 v147, v65, v130
	v_cndmask_b32_e64 v131, v135, v156, s[12:13]
	v_cndmask_b32_e64 v130, v134, v132, s[14:15]
	v_pk_mul_f32 v[130:131], v[136:137], v[130:131]
	v_mov_b32_e32 v145, v171
	v_mov_b32_e32 v170, v171
	v_fma_f32 v130, v153, v133, v130
	v_mov_b32_dpp v145, v157 row_ror:1 row_mask:0xf bank_mask:0xf
	v_mov_b32_dpp v170, v161 row_ror:15 row_mask:0xf bank_mask:0xf
	v_add_f32_e32 v130, v130, v131
	v_mul_f32_e32 v153, v57, v130
	v_cndmask_b32_e64 v131, v156, v170, s[12:13]
	v_cndmask_b32_e64 v130, v145, v134, s[14:15]
	v_pk_mul_f32 v[130:131], v[136:137], v[130:131]
	v_mov_b32_e32 v160, v171
	v_fma_f32 v130, v157, v133, v130
	v_add_f32_e32 v130, v130, v131
	v_mov_b32_dpp v160, v161 row_ror:1 row_mask:0xf bank_mask:0xf
	v_mul_f32_e32 v156, v41, v130
	v_cndmask_b32_e64 v130, v160, v145, s[14:15]
	v_cndmask_b32_e64 v131, v170, 0, s[12:13]
	v_pk_mul_f32 v[130:131], v[136:137], v[130:131]
	s_mov_b64 s[0:1], 0x80000
	v_fma_f32 v130, v161, v133, v130
	v_add_f32_e32 v130, v131, v130
	v_mul_f32_e32 v136, v25, v130
	v_lshl_add_u64 v[130:131], v[140:141], 0, s[0:1]
	v_lshl_add_u64 v[134:135], s[34:35], 0, v[130:131]
	v_lshl_add_u64 v[130:131], s[26:27], 0, v[130:131]
	v_mul_f32_e32 v150, v62, v150
	v_cvt_pk_bf16_f32 v132, v150, v151
	v_cvt_pk_bf16_f32 v133, v146, v147
	v_lshl_add_u64 v[134:135], v[134:135], 0, v[138:139]
	v_lshl_add_u64 v[130:131], v[130:131], 0, v[138:139]
	s_mov_b64 s[0:1], 0x90000
	global_store_dwordx2 v[134:135], v[132:133], off nt
	v_cvt_pk_bf16_f32 v132, v42, v43
	v_cvt_pk_bf16_f32 v133, v44, v45
	global_store_dwordx2 v[130:131], v[132:133], off nt
	v_lshl_add_u64 v[130:131], v[140:141], 0, s[0:1]
	v_lshl_add_u64 v[134:135], s[34:35], 0, v[130:131]
	v_lshl_add_u64 v[130:131], s[26:27], 0, v[130:131]
	v_mul_f32_e32 v149, v54, v149
	v_cvt_pk_bf16_f32 v132, v149, v155
	v_cvt_pk_bf16_f32 v133, v143, v153
	v_lshl_add_u64 v[134:135], v[134:135], 0, v[138:139]
	v_lshl_add_u64 v[130:131], v[130:131], 0, v[138:139]
	s_mov_b64 s[0:1], 0xa0000
	global_store_dwordx2 v[134:135], v[132:133], off nt
	v_cvt_pk_bf16_f32 v132, v26, v27
	v_cvt_pk_bf16_f32 v133, v28, v29
	global_store_dwordx2 v[130:131], v[132:133], off nt
	v_lshl_add_u64 v[130:131], v[140:141], 0, s[0:1]
	v_lshl_add_u64 v[134:135], s[34:35], 0, v[130:131]
	v_lshl_add_u64 v[130:131], s[26:27], 0, v[130:131]
	v_mul_f32_e32 v154, v38, v154
	v_cvt_pk_bf16_f32 v132, v154, v159
	v_cvt_pk_bf16_f32 v133, v152, v156
	v_lshl_add_u64 v[134:135], v[134:135], 0, v[138:139]
	v_lshl_add_u64 v[130:131], v[130:131], 0, v[138:139]
	s_mov_b64 s[0:1], 0xb0000
	global_store_dwordx2 v[134:135], v[132:133], off nt
	v_cvt_pk_bf16_f32 v132, v10, v11
	v_cvt_pk_bf16_f32 v133, v12, v13
	global_store_dwordx2 v[130:131], v[132:133], off nt
	v_lshl_add_u64 v[130:131], v[140:141], 0, s[0:1]
	v_lshl_add_u64 v[134:135], s[34:35], 0, v[130:131]
	v_lshl_add_u64 v[130:131], s[26:27], 0, v[130:131]
	v_cvt_pk_bf16_f32 v132, v158, v142
	v_cvt_pk_bf16_f32 v133, v144, v136
	v_lshl_add_u64 v[134:135], v[134:135], 0, v[138:139]
	v_lshl_add_u64 v[130:131], v[130:131], 0, v[138:139]
	global_store_dwordx2 v[134:135], v[132:133], off nt
	v_cvt_pk_bf16_f32 v132, v2, v3
	v_cvt_pk_bf16_f32 v133, v4, v5
	global_store_dwordx2 v[130:131], v[132:133], off nt

; __device__ __forceinline__ float siluf(float x) { return x * __builtin_amdgcn_rcpf(1.f + __expf(-x)); }
; __device__ __forceinline__ float dpp_ror1(float v) { return __builtin_bit_cast(float, __builtin_amdgcn_update_dpp(0, __builtin_bit_cast(int, v), 0x121, 0xf, 0xf, false)); }
; __device__ __forceinline__ float dpp_ror15(float v) { return __builtin_bit_cast(float, __builtin_amdgcn_update_dpp(0, __builtin_bit_cast(int, v), 0x12F, 0xf, 0xf, false)); }
;     __device__ __forceinline__ void operator()(const f32x4 (&acc)[2][2][4][2], const pg8::Unit& u, int wr, int wc, int fr, int fq_in) const {
;     ...
;             } else {
; #pragma unroll
;                 for (int bj = 0; bj < 2; ++bj) {
;                     const int col = col0 + bj * 128;
;                     f32x4 w0[2], w1[2], w2[2], bb[2];
; #pragma unroll
;                     for (int n = 0; n < 2; ++n) { w0[n] = *(const f32x4*)(cw + col + 4 * n); w1[n] = *(const f32x4*)(cw + XBCW + col + 4 * n); w2[n] = *(const f32x4*)(cw + 2 * XBCW + col + 4 * n); bb[n] = *(const f32x4*)(cb + col + 4 * n); }
; #pragma unroll
;                     for (int ai = 0; ai < 2; ++ai) {
;                         f32x4 o[4][2];
; #pragma unroll
;                         for (int n = 0; n < 2; ++n)
; #pragma unroll
;                             for (int q = 0; q < 4; ++q) { float A[4], B[4];
; #pragma unroll
;                                 for (int m = 0; m < 4; ++m) { A[m] = dpp_ror1(acc[ai][bj][m][n][q]); B[m] = dpp_ror15(acc[ai][bj][m][n][q]); }
; #pragma unroll
;                                 for (int m = 0; m < 4; ++m) { const float pv = fr > 0 ? A[m] : (m > 0 ? A[m > 0 ? m - 1 : 0] : 0.f), nv = fr < 15 ? B[m] : (m < 3 ? B[m < 3 ? m + 1 : 3] : 0.f);
;                                     o[m][n][q] = siluf(bb[n][q] + w0[n][q] * pv + w1[n][q] * acc[ai][bj][m][n][q] + w2[n][q] * nv); } }
.LBB0_477:
	s_andn2_b64 vcc, exec, s[0:1]
	s_cbranch_vccnz .LBB0_482
	s_lshl_b32 s0, s64, 8
	s_or_b32 s0, s0, s73
	v_lshl_add_u32 v180, v148, 3, s0
	s_cmp_gt_i32 s62, 63
	v_ashrrev_i32_e32 v181, 31, v180
	s_mov_b64 s[0:1], -1
	s_cbranch_scc1 .LBB0_480
	v_lshlrev_b64 v[130:131], 2, v[180:181]
	v_lshl_add_u64 v[182:183], s[16:17], 0, v[130:131]
	v_lshl_add_u64 v[184:185], s[48:49], 0, v[130:131]
	v_lshl_add_u64 v[188:189], s[50:51], 0, v[130:131]
	v_lshl_add_u64 v[190:191], s[18:19], 0, v[130:131]
	global_load_dwordx4 v[146:149], v[182:183], off
	global_load_dwordx4 v[150:153], v[190:191], off
	global_load_dwordx4 v[158:161], v[188:189], off
	global_load_dwordx4 v[154:157], v[184:185], off
	v_mov_b32_e32 v170, v171
	v_mov_b32_e32 v177, v171
	v_mov_b32_e32 v179, v171
	v_mov_b32_e32 v193, v171
	v_mov_b32_e32 v195, v171
	v_mov_b32_e32 v197, v171
	v_mov_b32_e32 v198, v171
	v_mov_b32_e32 v200, v171
	v_mov_b32_dpp v170, v126 row_ror:1 row_mask:0xf bank_mask:0xf
	v_mov_b32_dpp v177, v126 row_ror:15 row_mask:0xf bank_mask:0xf
	v_mov_b32_dpp v179, v118 row_ror:1 row_mask:0xf bank_mask:0xf
	v_mov_b32_dpp v193, v118 row_ror:15 row_mask:0xf bank_mask:0xf
	v_mov_b32_dpp v195, v102 row_ror:1 row_mask:0xf bank_mask:0xf
	v_mov_b32_dpp v197, v102 row_ror:15 row_mask:0xf bank_mask:0xf
	v_mov_b32_dpp v198, v86 row_ror:1 row_mask:0xf bank_mask:0xf
	v_mov_b32_dpp v200, v86 row_ror:15 row_mask:0xf bank_mask:0xf
	v_cndmask_b32_e64 v202, v170, 0, s[14:15]
	v_mov_b32_e32 v192, v126
	v_mov_b32_e32 v194, v118
	v_cndmask_b32_e64 v201, v177, v193, s[12:13]
	v_cndmask_b32_e64 v170, v179, v170, s[14:15]
	v_cndmask_b32_e64 v203, v193, v197, s[12:13]
	v_cndmask_b32_e64 v177, v195, v179, s[14:15]
	v_cndmask_b32_e64 v205, v197, v200, s[12:13]
	v_cndmask_b32_e64 v179, v198, v195, s[14:15]
	v_cndmask_b32_e64 v206, v200, 0, s[12:13]
	v_mov_b32_e32 v196, v102
	v_mov_b32_e32 v199, v86
	v_mov_b32_e32 v208, v171
	v_mov_b32_e32 v209, v171
	v_mov_b32_e32 v219, v171
	v_mov_b32_dpp v208, v127 row_ror:1 row_mask:0xf bank_mask:0xf
	v_mov_b32_dpp v209, v127 row_ror:15 row_mask:0xf bank_mask:0xf
	v_mov_b32_dpp v219, v119 row_ror:15 row_mask:0xf bank_mask:0xf
	v_mov_b32_e32 v218, v171
	v_mov_b32_e32 v221, v171
	v_mov_b32_e32 v220, v171
	v_mov_b32_dpp v218, v119 row_ror:1 row_mask:0xf bank_mask:0xf
	v_mov_b32_dpp v221, v103 row_ror:15 row_mask:0xf bank_mask:0xf
	v_mov_b32_dpp v220, v103 row_ror:1 row_mask:0xf bank_mask:0xf
	global_load_dwordx4 v[138:141], v[182:183], off offset:16
	global_load_dwordx4 v[130:133], v[184:185], off offset:16
	global_load_dwordx4 v[142:145], v[188:189], off offset:16
	global_load_dwordx4 v[134:137], v[190:191], off offset:16
	v_mov_b32_e32 v223, v171
	v_mov_b32_e32 v227, v171
	v_mov_b32_e32 v226, v171
	v_mov_b32_dpp v223, v78 row_ror:15 row_mask:0xf bank_mask:0xf
	v_mov_b32_dpp v227, v79 row_ror:15 row_mask:0xf bank_mask:0xf
	v_mov_b32_dpp v226, v79 row_ror:1 row_mask:0xf bank_mask:0xf
	v_mov_b32_e32 v231, v171
	v_mov_b32_e32 v230, v171
	v_mov_b32_e32 v235, v171
	v_mov_b32_dpp v231, v80 row_ror:15 row_mask:0xf bank_mask:0xf
	v_mov_b32_dpp v230, v80 row_ror:1 row_mask:0xf bank_mask:0xf
	v_mov_b32_dpp v235, v81 row_ror:15 row_mask:0xf bank_mask:0xf
	v_mov_b32_e32 v234, v171
	v_mov_b32_e32 v239, v171
	v_mov_b32_e32 v238, v171
	v_mov_b32_dpp v234, v81 row_ror:1 row_mask:0xf bank_mask:0xf
	v_mov_b32_dpp v239, v68 row_ror:15 row_mask:0xf bank_mask:0xf
	v_mov_b32_dpp v238, v68 row_ror:1 row_mask:0xf bank_mask:0xf
	v_mov_b32_e32 v243, v171
	v_mov_b32_e32 v242, v171
	s_waitcnt vmcnt(6)
	v_fma_f32 v222, v146, v202, v150
	s_waitcnt vmcnt(5)
	v_mov_b32_e32 v193, v158
	s_waitcnt vmcnt(4)
	v_mov_b32_e32 v200, v154
	v_mov_b32_e32 v195, v158
	v_mov_b32_e32 v202, v154
	v_fma_f32 v170, v146, v170, v150
	v_mov_b32_e32 v197, v158
	v_mov_b32_e32 v204, v154
	v_mov_b32_e32 v198, v158
	v_mov_b32_e32 v207, v154
	v_pk_mul_f32 v[192:193], v[192:193], v[200:201]
	v_pk_mul_f32 v[194:195], v[194:195], v[202:203]
	v_fma_f32 v177, v146, v177, v150
	v_fma_f32 v179, v146, v179, v150
	v_pk_mul_f32 v[196:197], v[196:197], v[204:205]
	v_pk_mul_f32 v[198:199], v[198:199], v[206:207]
	v_add_f32_e32 v192, v192, v222
	v_add_f32_e32 v170, v194, v170
	v_add_f32_e32 v177, v196, v177
	v_add_f32_e32 v179, v199, v179
	v_add_f32_e32 v192, v192, v193
	v_add_f32_e32 v170, v170, v195
	v_add_f32_e32 v177, v177, v197
	v_add_f32_e32 v193, v198, v179
	v_mul_f32_e32 v179, 0xbfb8aa3b, v192
	v_mul_f32_e32 v194, 0xbfb8aa3b, v170
	v_mul_f32_e32 v195, 0xbfb8aa3b, v177
	v_mul_f32_e32 v196, 0xbfb8aa3b, v193
	v_exp_f32_e32 v179, v179
	v_exp_f32_e32 v194, v194
	v_exp_f32_e32 v195, v195
	v_exp_f32_e32 v196, v196
	v_add_f32_e32 v179, 1.0, v179
	v_add_f32_e32 v194, 1.0, v194
	v_add_f32_e32 v195, 1.0, v195
	v_add_f32_e32 v196, 1.0, v196
	v_rcp_f32_e32 v179, v179
	v_rcp_f32_e32 v194, v194
	v_rcp_f32_e32 v195, v195
	v_rcp_f32_e32 v196, v196
	v_mul_f32_e32 v192, v192, v179
	v_mul_f32_e32 v179, v170, v194
	v_cndmask_b32_e64 v194, v208, 0, s[14:15]
	v_mul_f32_e32 v177, v177, v195
	v_mul_f32_e32 v170, v193, v196
	v_cndmask_b32_e64 v195, v209, v219, s[12:13]
	v_fma_f32 v199, v147, v194, v151
	v_mov_b32_e32 v196, v127
	v_mov_b32_e32 v197, v159
	v_mov_b32_e32 v194, v155
	v_pk_mul_f32 v[194:195], v[196:197], v[194:195]
	v_mov_b32_e32 v196, v119
	v_add_f32_e32 v194, v194, v199
	v_add_f32_e32 v199, v194, v195
	v_mul_f32_e32 v194, 0xbfb8aa3b, v199
	v_exp_f32_e32 v200, v194
	v_cndmask_b32_e64 v194, v218, v208, s[14:15]
	v_cndmask_b32_e64 v195, v219, v221, s[12:13]
	v_fma_f32 v201, v147, v194, v151
	v_mov_b32_e32 v194, v155
	v_pk_mul_f32 v[194:195], v[196:197], v[194:195]
	v_mov_b32_e32 v198, v171
	v_add_f32_e32 v194, v194, v201
; __device__ __forceinline__ float siluf(float x) { return x * __builtin_amdgcn_rcpf(1.f + __expf(-x)); }
; __device__ __forceinline__ float dpp_ror1(float v) { return __builtin_bit_cast(float, __builtin_amdgcn_update_dpp(0, __builtin_bit_cast(int, v), 0x121, 0xf, 0xf, false)); }
; __device__ __forceinline__ float dpp_ror15(float v) { return __builtin_bit_cast(float, __builtin_amdgcn_update_dpp(0, __builtin_bit_cast(int, v), 0x12F, 0xf, 0xf, false)); }
;     __device__ __forceinline__ void operator()(const f32x4 (&acc)[2][2][4][2], const pg8::Unit& u, int wr, int wc, int fr, int fq_in) const {
;     ...
;                     for (int ai = 0; ai < 2; ++ai) {
;                         f32x4 o[4][2];
; #pragma unroll
;                         for (int n = 0; n < 2; ++n)
; #pragma unroll
;                             for (int q = 0; q < 4; ++q) { float A[4], B[4];
; #pragma unroll
;                                 for (int m = 0; m < 4; ++m) { A[m] = dpp_ror1(acc[ai][bj][m][n][q]); B[m] = dpp_ror15(acc[ai][bj][m][n][q]); }
; #pragma unroll
;                                 for (int m = 0; m < 4; ++m) { const float pv = fr > 0 ? A[m] : (m > 0 ? A[m > 0 ? m - 1 : 0] : 0.f), nv = fr < 15 ? B[m] : (m < 3 ? B[m < 3 ? m + 1 : 3] : 0.f);
;                                     o[m][n][q] = siluf(bb[n][q] + w0[n][q] * pv + w1[n][q] * acc[ai][bj][m][n][q] + w2[n][q] * nv); } }
	v_add_f32_e32 v201, v194, v195
	v_mul_f32_e32 v194, 0xbfb8aa3b, v201
	v_exp_f32_e32 v194, v194
	v_mov_b32_dpp v198, v87 row_ror:15 row_mask:0xf bank_mask:0xf
	v_add_f32_e32 v195, 1.0, v200
	v_rcp_f32_e32 v200, v195
	v_add_f32_e32 v202, 1.0, v194
	v_cndmask_b32_e64 v194, v220, v218, s[14:15]
	v_cndmask_b32_e64 v195, v221, v198, s[12:13]
	v_fma_f32 v203, v147, v194, v151
	v_mov_b32_e32 v196, v103
	v_mov_b32_e32 v194, v155
	v_pk_mul_f32 v[194:195], v[196:197], v[194:195]
	v_mov_b32_e32 v193, v171
	v_add_f32_e32 v194, v194, v203
	v_add_f32_e32 v203, v194, v195
	v_mov_b32_dpp v193, v87 row_ror:1 row_mask:0xf bank_mask:0xf
	v_mul_f32_e32 v194, 0xbfb8aa3b, v203
	v_exp_f32_e32 v204, v194
	v_cndmask_b32_e64 v193, v193, v220, s[14:15]
	v_cndmask_b32_e64 v194, v198, 0, s[12:13]
	v_mov_b32_e32 v196, v159
	v_mov_b32_e32 v197, v87
	v_mov_b32_e32 v195, v155
	v_fma_f32 v193, v147, v193, v151
	v_pk_mul_f32 v[194:195], v[196:197], v[194:195]
	v_add_f32_e32 v196, 1.0, v204
	v_add_f32_e32 v193, v195, v193
	v_add_f32_e32 v195, v194, v193
	v_mul_f32_e32 v193, 0xbfb8aa3b, v195
	v_exp_f32_e32 v193, v193
	v_rcp_f32_e32 v194, v202
	v_rcp_f32_e32 v196, v196
	v_mov_b32_e32 v204, v171
	v_add_f32_e32 v193, 1.0, v193
	v_rcp_f32_e32 v197, v193
	v_mul_f32_e32 v193, v199, v200
	v_mov_b32_dpp v204, v120 row_ror:15 row_mask:0xf bank_mask:0xf
	v_mul_f32_e32 v194, v201, v194
	v_mul_f32_e32 v198, v195, v197
	v_mov_b32_e32 v195, v171
	v_mov_b32_e32 v197, v171
	v_mul_f32_e32 v196, v203, v196
	v_mov_b32_dpp v195, v128 row_ror:1 row_mask:0xf bank_mask:0xf
	v_mov_b32_dpp v197, v128 row_ror:15 row_mask:0xf bank_mask:0xf
	v_cndmask_b32_e64 v200, v195, 0, s[14:15]
	v_cndmask_b32_e64 v201, v197, v204, s[12:13]
	v_fma_f32 v197, v148, v200, v152
	v_mov_b32_e32 v202, v128
	v_mov_b32_e32 v203, v160
	v_mov_b32_e32 v200, v156
	v_pk_mul_f32 v[200:201], v[202:203], v[200:201]
	v_mov_b32_e32 v199, v171
	v_add_f32_e32 v197, v200, v197
	v_mov_b32_e32 v206, v171
	v_add_f32_e32 v197, v197, v201
	v_mov_b32_dpp v199, v120 row_ror:1 row_mask:0xf bank_mask:0xf
	v_mov_b32_dpp v206, v104 row_ror:15 row_mask:0xf bank_mask:0xf
	v_mul_f32_e32 v200, 0xbfb8aa3b, v197
	v_exp_f32_e32 v209, v200
	v_cndmask_b32_e64 v195, v199, v195, s[14:15]
	v_cndmask_b32_e64 v201, v204, v206, s[12:13]
	v_mov_b32_e32 v202, v120
	v_mov_b32_e32 v200, v156
	v_fma_f32 v195, v148, v195, v152
	v_pk_mul_f32 v[200:201], v[202:203], v[200:201]
	v_mov_b32_e32 v205, v171
	v_add_f32_e32 v195, v200, v195
	v_add_f32_e32 v195, v195, v201
	v_mul_f32_e32 v200, 0xbfb8aa3b, v195
	v_exp_f32_e32 v200, v200
	v_mov_b32_e32 v208, v171
	v_mov_b32_dpp v205, v104 row_ror:1 row_mask:0xf bank_mask:0xf
	v_add_f32_e32 v201, 1.0, v209
	v_mov_b32_dpp v208, v88 row_ror:15 row_mask:0xf bank_mask:0xf
	v_rcp_f32_e32 v204, v201
	v_add_f32_e32 v209, 1.0, v200
	v_cndmask_b32_e64 v199, v205, v199, s[14:15]
	v_cndmask_b32_e64 v201, v206, v208, s[12:13]
	v_mov_b32_e32 v202, v104
	v_mov_b32_e32 v200, v156
	v_fma_f32 v199, v148, v199, v152
	v_pk_mul_f32 v[200:201], v[202:203], v[200:201]
	v_mov_b32_e32 v207, v171
	v_add_f32_e32 v199, v200, v199
	v_add_f32_e32 v199, v199, v201
	v_mov_b32_dpp v207, v88 row_ror:1 row_mask:0xf bank_mask:0xf
	v_mul_f32_e32 v200, 0xbfb8aa3b, v199
	v_cndmask_b32_e64 v201, v207, v205, s[14:15]
	v_exp_f32_e32 v206, v200
	v_cndmask_b32_e64 v200, v208, 0, s[12:13]
	v_fma_f32 v205, v148, v201, v152
	v_mov_b32_e32 v202, v160
	v_mov_b32_e32 v203, v88
	v_mov_b32_e32 v201, v156
	v_pk_mul_f32 v[200:201], v[202:203], v[200:201]
	v_rcp_f32_e32 v202, v209
	v_add_f32_e32 v201, v201, v205
	v_add_f32_e32 v200, v200, v201
	v_mul_f32_e32 v201, 0xbfb8aa3b, v200
	v_exp_f32_e32 v201, v201
	v_add_f32_e32 v203, 1.0, v206
	v_rcp_f32_e32 v203, v203
	v_mov_b32_e32 v205, v171
	v_add_f32_e32 v201, 1.0, v201
	v_rcp_f32_e32 v201, v201
	v_mul_f32_e32 v197, v197, v204
	v_mov_b32_dpp v205, v129 row_ror:1 row_mask:0xf bank_mask:0xf
	v_mov_b32_e32 v207, v171
	v_mul_f32_e32 v204, v200, v201
	v_mov_b32_e32 v200, v171
	v_mul_f32_e32 v195, v195, v202
	v_mov_b32_dpp v207, v121 row_ror:15 row_mask:0xf bank_mask:0xf
	v_mov_b32_dpp v200, v129 row_ror:15 row_mask:0xf bank_mask:0xf
	v_cndmask_b32_e64 v202, v205, 0, s[14:15]
	v_mul_f32_e32 v199, v199, v203
	v_cndmask_b32_e64 v201, v200, v207, s[12:13]
	v_fma_f32 v220, v149, v202, v153
	v_mov_b32_e32 v202, v129
	v_mov_b32_e32 v203, v161
	v_mov_b32_e32 v200, v157
	v_pk_mul_f32 v[200:201], v[202:203], v[200:201]
	v_mov_b32_e32 v206, v171
	v_add_f32_e32 v200, v200, v220
	v_add_f32_e32 v220, v200, v201
	v_mov_b32_dpp v206, v121 row_ror:1 row_mask:0xf bank_mask:0xf
	v_mov_b32_e32 v209, v171
	v_mul_f32_e32 v200, 0xbfb8aa3b, v220
	v_exp_f32_e32 v221, v200
	v_mov_b32_dpp v209, v105 row_ror:15 row_mask:0xf bank_mask:0xf
	v_cndmask_b32_e64 v200, v206, v205, s[14:15]
	v_cndmask_b32_e64 v201, v207, v209, s[12:13]
	v_fma_f32 v205, v149, v200, v153
	v_mov_b32_e32 v202, v121
	v_mov_b32_e32 v200, v157
	v_pk_mul_f32 v[200:201], v[202:203], v[200:201]
	v_mov_b32_e32 v208, v171
	v_add_f32_e32 v200, v200, v205
	v_add_f32_e32 v205, v200, v201
	v_mul_f32_e32 v200, 0xbfb8aa3b, v205
	v_exp_f32_e32 v200, v200
	v_mov_b32_dpp v208, v105 row_ror:1 row_mask:0xf bank_mask:0xf
	v_mov_b32_e32 v219, v171
	v_add_f32_e32 v201, 1.0, v221
	v_add_f32_e32 v221, 1.0, v200
	v_mov_b32_dpp v219, v89 row_ror:15 row_mask:0xf bank_mask:0xf
	v_cndmask_b32_e64 v200, v208, v206, s[14:15]
	v_rcp_f32_e32 v207, v201
	v_cndmask_b32_e64 v201, v209, v219, s[12:13]
	v_fma_f32 v206, v149, v200, v153
	v_mov_b32_e32 v202, v105
	v_mov_b32_e32 v200, v157
	v_pk_mul_f32 v[200:201], v[202:203], v[200:201]
	v_mov_b32_e32 v218, v171
	v_add_f32_e32 v200, v200, v206
	v_add_f32_e32 v206, v200, v201
	v_mov_b32_dpp v218, v89 row_ror:1 row_mask:0xf bank_mask:0xf
	v_mul_f32_e32 v200, 0xbfb8aa3b, v206
	v_cndmask_b32_e64 v201, v218, v208, s[14:15]
	v_exp_f32_e32 v209, v200
	v_cndmask_b32_e64 v200, v219, 0, s[12:13]
	v_fma_f32 v208, v149, v201, v153
	v_mov_b32_e32 v202, v161
	v_mov_b32_e32 v203, v89
	v_mov_b32_e32 v201, v157
	v_pk_mul_f32 v[200:201], v[202:203], v[200:201]
	v_add_f32_e32 v203, 1.0, v209
	v_add_f32_e32 v201, v201, v208
	v_add_f32_e32 v200, v200, v201
	v_mul_f32_e32 v201, 0xbfb8aa3b, v200
	v_exp_f32_e32 v201, v201
	v_rcp_f32_e32 v203, v203
	v_rcp_f32_e32 v202, v221
	v_mov_b32_e32 v209, v171
	v_add_f32_e32 v201, 1.0, v201
	v_rcp_f32_e32 v201, v201
	v_mul_f32_e32 v218, v206, v203
	v_mov_b32_e32 v206, v171
	v_mul_f32_e32 v205, v205, v202
	v_mul_f32_e32 v219, v200, v201
	v_mov_b32_dpp v206, v122 row_ror:1 row_mask:0xf bank_mask:0xf
	v_mov_b32_e32 v200, v171
	v_mov_b32_dpp v209, v110 row_ror:15 row_mask:0xf bank_mask:0xf
	v_cndmask_b32_e64 v202, v206, 0, s[14:15]
	v_mov_b32_dpp v200, v122 row_ror:15 row_mask:0xf bank_mask:0xf
	v_cndmask_b32_e64 v201, v200, v209, s[12:13]
	s_waitcnt vmcnt(0)
; __device__ __forceinline__ float siluf(float x) { return x * __builtin_amdgcn_rcpf(1.f + __expf(-x)); }
; __device__ __forceinline__ float dpp_ror1(float v) { return __builtin_bit_cast(float, __builtin_amdgcn_update_dpp(0, __builtin_bit_cast(int, v), 0x121, 0xf, 0xf, false)); }
; __device__ __forceinline__ float dpp_ror15(float v) { return __builtin_bit_cast(float, __builtin_amdgcn_update_dpp(0, __builtin_bit_cast(int, v), 0x12F, 0xf, 0xf, false)); }
;     __device__ __forceinline__ void operator()(const f32x4 (&acc)[2][2][4][2], const pg8::Unit& u, int wr, int wc, int fr, int fq_in) const {
;     ...
;                     for (int ai = 0; ai < 2; ++ai) {
;                         f32x4 o[4][2];
; #pragma unroll
;                         for (int n = 0; n < 2; ++n)
; #pragma unroll
;                             for (int q = 0; q < 4; ++q) { float A[4], B[4];
; #pragma unroll
;                                 for (int m = 0; m < 4; ++m) { A[m] = dpp_ror1(acc[ai][bj][m][n][q]); B[m] = dpp_ror15(acc[ai][bj][m][n][q]); }
; #pragma unroll
;                                 for (int m = 0; m < 4; ++m) { const float pv = fr > 0 ? A[m] : (m > 0 ? A[m > 0 ? m - 1 : 0] : 0.f), nv = fr < 15 ? B[m] : (m < 3 ? B[m < 3 ? m + 1 : 3] : 0.f);
;                                     o[m][n][q] = siluf(bb[n][q] + w0[n][q] * pv + w1[n][q] * acc[ai][bj][m][n][q] + w2[n][q] * nv); } }
	v_fma_f32 v224, v138, v202, v134
	v_mov_b32_e32 v202, v122
	v_mov_b32_e32 v203, v142
	v_mov_b32_e32 v200, v130
	v_pk_mul_f32 v[200:201], v[202:203], v[200:201]
	v_mov_b32_e32 v208, v171
	v_add_f32_e32 v200, v200, v224
	v_add_f32_e32 v224, v200, v201
	v_mov_b32_dpp v208, v110 row_ror:1 row_mask:0xf bank_mask:0xf
	v_mov_b32_e32 v221, v171
	v_mul_f32_e32 v200, 0xbfb8aa3b, v224
	v_exp_f32_e32 v225, v200
	v_mov_b32_dpp v221, v94 row_ror:15 row_mask:0xf bank_mask:0xf
	v_cndmask_b32_e64 v200, v208, v206, s[14:15]
	v_cndmask_b32_e64 v201, v209, v221, s[12:13]
	v_fma_f32 v206, v138, v200, v134
	v_mov_b32_e32 v202, v110
	v_mov_b32_e32 v200, v130
	v_pk_mul_f32 v[200:201], v[202:203], v[200:201]
	v_mul_f32_e32 v207, v220, v207
	v_add_f32_e32 v200, v200, v206
	v_add_f32_e32 v206, v200, v201
	v_mul_f32_e32 v200, 0xbfb8aa3b, v206
	v_exp_f32_e32 v200, v200
	v_mov_b32_e32 v220, v171
	v_add_f32_e32 v201, 1.0, v225
	v_rcp_f32_e32 v209, v201
	v_mov_b32_dpp v220, v94 row_ror:1 row_mask:0xf bank_mask:0xf
	v_add_f32_e32 v225, 1.0, v200
	v_cndmask_b32_e64 v200, v220, v208, s[14:15]
	v_cndmask_b32_e64 v201, v221, v223, s[12:13]
	v_fma_f32 v208, v138, v200, v134
	v_mov_b32_e32 v202, v94
	v_mov_b32_e32 v200, v130
	v_pk_mul_f32 v[200:201], v[202:203], v[200:201]
	v_mov_b32_e32 v222, v171
	v_add_f32_e32 v200, v200, v208
	v_add_f32_e32 v208, v200, v201
	v_mov_b32_dpp v222, v78 row_ror:1 row_mask:0xf bank_mask:0xf
	v_mul_f32_e32 v200, 0xbfb8aa3b, v208
	v_cndmask_b32_e64 v201, v222, v220, s[14:15]
	v_exp_f32_e32 v221, v200
	v_cndmask_b32_e64 v200, v223, 0, s[12:13]
	v_fma_f32 v220, v138, v201, v134
	v_mov_b32_e32 v202, v142
	v_mov_b32_e32 v203, v78
	v_mov_b32_e32 v201, v130
	v_pk_mul_f32 v[200:201], v[202:203], v[200:201]
	v_rcp_f32_e32 v202, v225
	v_add_f32_e32 v201, v201, v220
	v_add_f32_e32 v200, v200, v201
	v_mul_f32_e32 v201, 0xbfb8aa3b, v200
	v_exp_f32_e32 v201, v201
	v_add_f32_e32 v203, 1.0, v221
	v_rcp_f32_e32 v203, v203
	v_mul_f32_e32 v220, v206, v202
	v_add_f32_e32 v201, 1.0, v201
	v_rcp_f32_e32 v201, v201
	v_mov_b32_e32 v206, v171
	v_mov_b32_e32 v223, v171
	v_mul_f32_e32 v221, v208, v203
	v_mul_f32_e32 v222, v200, v201
	v_mov_b32_dpp v206, v123 row_ror:1 row_mask:0xf bank_mask:0xf
	v_mov_b32_e32 v200, v171
	v_mov_b32_dpp v223, v111 row_ror:15 row_mask:0xf bank_mask:0xf
	v_cndmask_b32_e64 v202, v206, 0, s[14:15]
	v_mov_b32_dpp v200, v123 row_ror:15 row_mask:0xf bank_mask:0xf
	v_cndmask_b32_e64 v201, v200, v223, s[12:13]
	v_fma_f32 v228, v139, v202, v135
	v_mov_b32_e32 v202, v123
	v_mov_b32_e32 v203, v143
	v_mov_b32_e32 v200, v131
	v_pk_mul_f32 v[200:201], v[202:203], v[200:201]
	v_mov_b32_e32 v208, v171
	v_add_f32_e32 v200, v200, v228
	v_add_f32_e32 v228, v200, v201
	v_mov_b32_dpp v208, v111 row_ror:1 row_mask:0xf bank_mask:0xf
	v_mov_b32_e32 v225, v171
	v_mul_f32_e32 v200, 0xbfb8aa3b, v228
	v_exp_f32_e32 v229, v200
	v_mov_b32_dpp v225, v95 row_ror:15 row_mask:0xf bank_mask:0xf
	v_cndmask_b32_e64 v200, v208, v206, s[14:15]
	v_cndmask_b32_e64 v201, v223, v225, s[12:13]
	v_fma_f32 v206, v139, v200, v135
	v_mov_b32_e32 v202, v111
	v_mov_b32_e32 v200, v131
	v_pk_mul_f32 v[200:201], v[202:203], v[200:201]
	v_mul_f32_e32 v209, v224, v209
	v_add_f32_e32 v200, v200, v206
	v_add_f32_e32 v206, v200, v201
	v_mul_f32_e32 v200, 0xbfb8aa3b, v206
	v_exp_f32_e32 v200, v200
	v_mov_b32_e32 v224, v171
	v_add_f32_e32 v201, 1.0, v229
	v_rcp_f32_e32 v223, v201
	v_mov_b32_dpp v224, v95 row_ror:1 row_mask:0xf bank_mask:0xf
	v_add_f32_e32 v229, 1.0, v200
	v_cndmask_b32_e64 v200, v224, v208, s[14:15]
	v_cndmask_b32_e64 v201, v225, v227, s[12:13]
	v_fma_f32 v208, v139, v200, v135
	v_mov_b32_e32 v202, v95
	v_mov_b32_e32 v200, v131
	v_pk_mul_f32 v[200:201], v[202:203], v[200:201]
	v_mov_b32_e32 v202, v143
	v_add_f32_e32 v200, v200, v208
	v_add_f32_e32 v208, v200, v201
	v_mul_f32_e32 v200, 0xbfb8aa3b, v208
	v_cndmask_b32_e64 v201, v226, v224, s[14:15]
	v_exp_f32_e32 v225, v200
	v_cndmask_b32_e64 v200, v227, 0, s[12:13]
	v_fma_f32 v224, v139, v201, v135
	v_mov_b32_e32 v203, v79
	v_mov_b32_e32 v201, v131
	v_pk_mul_f32 v[200:201], v[202:203], v[200:201]
	v_rcp_f32_e32 v202, v229
	v_add_f32_e32 v201, v201, v224
	v_add_f32_e32 v200, v200, v201
	v_mul_f32_e32 v201, 0xbfb8aa3b, v200
	v_exp_f32_e32 v201, v201
	v_add_f32_e32 v203, 1.0, v225
	v_rcp_f32_e32 v203, v203
	v_mul_f32_e32 v224, v206, v202
	v_add_f32_e32 v201, 1.0, v201
	v_rcp_f32_e32 v201, v201
	v_mov_b32_e32 v206, v171
	v_mov_b32_e32 v227, v171
	v_mul_f32_e32 v225, v208, v203
	v_mul_f32_e32 v226, v200, v201
	v_mov_b32_dpp v206, v124 row_ror:1 row_mask:0xf bank_mask:0xf
	v_mov_b32_e32 v200, v171
	v_mov_b32_dpp v227, v112 row_ror:15 row_mask:0xf bank_mask:0xf
	v_cndmask_b32_e64 v202, v206, 0, s[14:15]
	v_mov_b32_dpp v200, v124 row_ror:15 row_mask:0xf bank_mask:0xf
	v_cndmask_b32_e64 v201, v200, v227, s[12:13]
	v_fma_f32 v232, v140, v202, v136
	v_mov_b32_e32 v202, v124
	v_mov_b32_e32 v203, v144
	v_mov_b32_e32 v200, v132
	v_pk_mul_f32 v[200:201], v[202:203], v[200:201]
	v_mov_b32_e32 v208, v171
	v_add_f32_e32 v200, v200, v232
	v_add_f32_e32 v232, v200, v201
	v_mov_b32_dpp v208, v112 row_ror:1 row_mask:0xf bank_mask:0xf
	v_mov_b32_e32 v229, v171
	v_mul_f32_e32 v200, 0xbfb8aa3b, v232
	v_exp_f32_e32 v233, v200
	v_mov_b32_dpp v229, v96 row_ror:15 row_mask:0xf bank_mask:0xf
	v_cndmask_b32_e64 v200, v208, v206, s[14:15]
	v_cndmask_b32_e64 v201, v227, v229, s[12:13]
	v_fma_f32 v206, v140, v200, v136
	v_mov_b32_e32 v202, v112
	v_mov_b32_e32 v200, v132
	v_pk_mul_f32 v[200:201], v[202:203], v[200:201]
	v_mul_f32_e32 v223, v228, v223
	v_add_f32_e32 v200, v200, v206
	v_add_f32_e32 v206, v200, v201
	v_mul_f32_e32 v200, 0xbfb8aa3b, v206
	v_exp_f32_e32 v200, v200
; __device__ __forceinline__ unsigned cvt_pk_bf16(float lo, float hi) { unsigned r; asm volatile("v_cvt_pk_bf16_f32 %0, %1, %2" : "=v"(r) : "v"(lo), "v"(hi)); return r; }
; __device__ __forceinline__ float siluf(float x) { return x * __builtin_amdgcn_rcpf(1.f + __expf(-x)); }
; __device__ __forceinline__ float dpp_ror1(float v) { return __builtin_bit_cast(float, __builtin_amdgcn_update_dpp(0, __builtin_bit_cast(int, v), 0x121, 0xf, 0xf, false)); }
; __device__ __forceinline__ float dpp_ror15(float v) { return __builtin_bit_cast(float, __builtin_amdgcn_update_dpp(0, __builtin_bit_cast(int, v), 0x12F, 0xf, 0xf, false)); }
;     __device__ __forceinline__ void operator()(const f32x4 (&acc)[2][2][4][2], const pg8::Unit& u, int wr, int wc, int fr, int fq_in) const {
;     ...
;                     for (int ai = 0; ai < 2; ++ai) {
;                         f32x4 o[4][2];
; #pragma unroll
;                         for (int n = 0; n < 2; ++n)
; #pragma unroll
;                             for (int q = 0; q < 4; ++q) { float A[4], B[4];
; #pragma unroll
;                                 for (int m = 0; m < 4; ++m) { A[m] = dpp_ror1(acc[ai][bj][m][n][q]); B[m] = dpp_ror15(acc[ai][bj][m][n][q]); }
; #pragma unroll
;                                 for (int m = 0; m < 4; ++m) { const float pv = fr > 0 ? A[m] : (m > 0 ? A[m > 0 ? m - 1 : 0] : 0.f), nv = fr < 15 ? B[m] : (m < 3 ? B[m < 3 ? m + 1 : 3] : 0.f);
;                                     o[m][n][q] = siluf(bb[n][q] + w0[n][q] * pv + w1[n][q] * acc[ai][bj][m][n][q] + w2[n][q] * nv); } }
; #pragma unroll
;                         for (int m = 0; m < 4; ++m) { u32x4 w; w.x = pg8::cvt_pk_bf16(o[m][0][0], o[m][0][1]); w.y = pg8::cvt_pk_bf16(o[m][0][2], o[m][0][3]); w.z = pg8::cvt_pk_bf16(o[m][1][0], o[m][1][1]); w.w = pg8::cvt_pk_bf16(o[m][1][2], o[m][1][3]);
;                             *(u32x4*)(XBC + (size_t)(row0 + ai * 128 + m * 16) * XBCW + col) = w; }
	v_mov_b32_e32 v228, v171
	v_add_f32_e32 v201, 1.0, v233
	v_rcp_f32_e32 v227, v201
	v_mov_b32_dpp v228, v96 row_ror:1 row_mask:0xf bank_mask:0xf
	v_add_f32_e32 v233, 1.0, v200
	v_cndmask_b32_e64 v200, v228, v208, s[14:15]
	v_cndmask_b32_e64 v201, v229, v231, s[12:13]
	v_fma_f32 v208, v140, v200, v136
	v_mov_b32_e32 v202, v96
	v_mov_b32_e32 v200, v132
	v_pk_mul_f32 v[200:201], v[202:203], v[200:201]
	v_mov_b32_e32 v202, v144
	v_add_f32_e32 v200, v200, v208
	v_add_f32_e32 v208, v200, v201
	v_mul_f32_e32 v200, 0xbfb8aa3b, v208
	v_cndmask_b32_e64 v201, v230, v228, s[14:15]
	v_exp_f32_e32 v229, v200
	v_cndmask_b32_e64 v200, v231, 0, s[12:13]
	v_fma_f32 v228, v140, v201, v136
	v_mov_b32_e32 v203, v80
	v_mov_b32_e32 v201, v132
	v_pk_mul_f32 v[200:201], v[202:203], v[200:201]
	v_rcp_f32_e32 v202, v233
	v_add_f32_e32 v201, v201, v228
	v_add_f32_e32 v200, v200, v201
	v_mul_f32_e32 v201, 0xbfb8aa3b, v200
	v_exp_f32_e32 v201, v201
	v_add_f32_e32 v203, 1.0, v229
	v_rcp_f32_e32 v203, v203
	v_mul_f32_e32 v228, v206, v202
	v_add_f32_e32 v201, 1.0, v201
	v_rcp_f32_e32 v201, v201
	v_mov_b32_e32 v206, v171
	v_mov_b32_e32 v231, v171
	v_mul_f32_e32 v229, v208, v203
	v_mul_f32_e32 v230, v200, v201
	v_mov_b32_dpp v206, v125 row_ror:1 row_mask:0xf bank_mask:0xf
	v_mov_b32_e32 v200, v171
	v_mov_b32_dpp v231, v113 row_ror:15 row_mask:0xf bank_mask:0xf
	v_cndmask_b32_e64 v202, v206, 0, s[14:15]
	v_mov_b32_dpp v200, v125 row_ror:15 row_mask:0xf bank_mask:0xf
	v_cndmask_b32_e64 v201, v200, v231, s[12:13]
	v_fma_f32 v236, v141, v202, v137
	v_mov_b32_e32 v202, v125
	v_mov_b32_e32 v203, v145
	v_mov_b32_e32 v200, v133
	v_pk_mul_f32 v[200:201], v[202:203], v[200:201]
	v_mov_b32_e32 v208, v171
	v_add_f32_e32 v200, v200, v236
	v_add_f32_e32 v236, v200, v201
	v_mov_b32_dpp v208, v113 row_ror:1 row_mask:0xf bank_mask:0xf
	v_mov_b32_e32 v233, v171
	v_mul_f32_e32 v200, 0xbfb8aa3b, v236
	v_exp_f32_e32 v237, v200
	v_mov_b32_dpp v233, v97 row_ror:15 row_mask:0xf bank_mask:0xf
	v_cndmask_b32_e64 v200, v208, v206, s[14:15]
	v_cndmask_b32_e64 v201, v231, v233, s[12:13]
	v_fma_f32 v206, v141, v200, v137
	v_mov_b32_e32 v202, v113
	v_mov_b32_e32 v200, v133
	v_pk_mul_f32 v[200:201], v[202:203], v[200:201]
	v_mul_f32_e32 v227, v232, v227
	v_add_f32_e32 v200, v200, v206
	v_add_f32_e32 v206, v200, v201
	v_mul_f32_e32 v200, 0xbfb8aa3b, v206
	v_exp_f32_e32 v200, v200
	v_mov_b32_e32 v232, v171
	v_add_f32_e32 v201, 1.0, v237
	v_rcp_f32_e32 v231, v201
	v_mov_b32_dpp v232, v97 row_ror:1 row_mask:0xf bank_mask:0xf
	v_add_f32_e32 v237, 1.0, v200
	v_cndmask_b32_e64 v200, v232, v208, s[14:15]
	v_cndmask_b32_e64 v201, v233, v235, s[12:13]
	v_fma_f32 v208, v141, v200, v137
	v_mov_b32_e32 v202, v97
	v_mov_b32_e32 v200, v133
	v_pk_mul_f32 v[200:201], v[202:203], v[200:201]
	v_mov_b32_e32 v202, v145
	v_add_f32_e32 v200, v200, v208
	v_add_f32_e32 v208, v200, v201
	v_mul_f32_e32 v200, 0xbfb8aa3b, v208
	v_cndmask_b32_e64 v201, v234, v232, s[14:15]
	v_exp_f32_e32 v233, v200
	v_cndmask_b32_e64 v200, v235, 0, s[12:13]
	v_fma_f32 v232, v141, v201, v137
	v_mov_b32_e32 v203, v81
	v_mov_b32_e32 v201, v133
	v_pk_mul_f32 v[200:201], v[202:203], v[200:201]
	v_rcp_f32_e32 v202, v237
	v_add_f32_e32 v201, v201, v232
	v_add_f32_e32 v200, v200, v201
	v_mul_f32_e32 v201, 0xbfb8aa3b, v200
	v_exp_f32_e32 v201, v201
	v_add_f32_e32 v203, 1.0, v233
	v_rcp_f32_e32 v203, v203
	v_mul_f32_e32 v232, v206, v202
	v_add_f32_e32 v201, 1.0, v201
	v_rcp_f32_e32 v201, v201
	v_mul_f32_e32 v233, v208, v203
	v_mul_f32_e32 v231, v236, v231
	v_mov_b32_e32 v235, v171
	v_mul_f32_e32 v234, v200, v201
	v_cvt_pk_bf16_f32 v200, v192, v193
	v_cvt_pk_bf16_f32 v201, v197, v207
	v_mov_b64_e32 v[206:207], s[28:29]
	v_cvt_pk_bf16_f32 v202, v209, v223
	v_mad_i64_i32 v[192:193], s[0:1], v178, s93, v[206:207]
	v_lshlrev_b64 v[208:209], 1, v[180:181]
	v_lshl_add_u64 v[192:193], v[192:193], 0, v[208:209]
	v_cvt_pk_bf16_f32 v203, v227, v231
	global_store_dwordx4 v[192:193], v[200:203], off nt
	v_mov_b32_e32 v223, v171
	v_mov_b32_e32 v227, v171
	v_cvt_pk_bf16_f32 v200, v179, v194
	v_or_b32_e32 v179, 16, v178
	v_cvt_pk_bf16_f32 v201, v195, v205
	v_mad_i64_i32 v[194:195], s[0:1], v179, s93, v[206:207]
	v_lshl_add_u64 v[194:195], v[194:195], 0, v[208:209]
	v_cvt_pk_bf16_f32 v202, v220, v224
	v_cvt_pk_bf16_f32 v203, v228, v232
	global_store_dwordx4 v[194:195], v[200:203], off nt
	v_mov_b32_e32 v179, v171
	v_mov_b32_e32 v205, v171
	v_cvt_pk_bf16_f32 v200, v177, v196
	v_or_b32_e32 v177, 32, v178
	v_mad_i64_i32 v[196:197], s[0:1], v177, s93, v[206:207]
	v_lshl_add_u64 v[196:197], v[196:197], 0, v[208:209]
	v_cvt_pk_bf16_f32 v201, v199, v218
	v_cvt_pk_bf16_f32 v202, v221, v225
	v_cvt_pk_bf16_f32 v203, v229, v233
	global_store_dwordx4 v[196:197], v[200:203], off nt
	v_mov_b32_e32 v177, v171
	v_mov_b32_e32 v218, v171
	v_cvt_pk_bf16_f32 v200, v170, v198
	v_or_b32_e32 v170, 48, v178
	v_mad_i64_i32 v[198:199], s[0:1], v170, s93, v[206:207]
	v_mov_b32_e32 v170, v171
	v_cvt_pk_bf16_f32 v201, v204, v219
	v_lshl_add_u64 v[198:199], v[198:199], 0, v[208:209]
	v_mov_b32_e32 v204, v171
	v_mov_b32_dpp v170, v62 row_ror:1 row_mask:0xf bank_mask:0xf
	v_cvt_pk_bf16_f32 v202, v222, v226
	v_cvt_pk_bf16_f32 v203, v230, v234
	global_store_dwordx4 v[198:199], v[200:203], off nt
	v_mov_b32_dpp v177, v62 row_ror:15 row_mask:0xf bank_mask:0xf
	v_mov_b32_dpp v204, v54 row_ror:15 row_mask:0xf bank_mask:0xf
	v_cndmask_b32_e64 v200, v170, 0, s[14:15]
	v_cndmask_b32_e64 v201, v177, v204, s[12:13]
	v_fma_f32 v177, v146, v200, v150
	v_mov_b32_e32 v202, v62
	v_mov_b32_e32 v203, v158
	v_mov_b32_e32 v200, v154
	v_pk_mul_f32 v[200:201], v[202:203], v[200:201]
	v_mov_b32_dpp v179, v54 row_ror:1 row_mask:0xf bank_mask:0xf
; __device__ __forceinline__ float siluf(float x) { return x * __builtin_amdgcn_rcpf(1.f + __expf(-x)); }
; __device__ __forceinline__ float dpp_ror1(float v) { return __builtin_bit_cast(float, __builtin_amdgcn_update_dpp(0, __builtin_bit_cast(int, v), 0x121, 0xf, 0xf, false)); }
; __device__ __forceinline__ float dpp_ror15(float v) { return __builtin_bit_cast(float, __builtin_amdgcn_update_dpp(0, __builtin_bit_cast(int, v), 0x12F, 0xf, 0xf, false)); }
;     __device__ __forceinline__ void operator()(const f32x4 (&acc)[2][2][4][2], const pg8::Unit& u, int wr, int wc, int fr, int fq_in) const {
;     ...
;                     for (int ai = 0; ai < 2; ++ai) {
;                         f32x4 o[4][2];
; #pragma unroll
;                         for (int n = 0; n < 2; ++n)
; #pragma unroll
;                             for (int q = 0; q < 4; ++q) { float A[4], B[4];
; #pragma unroll
;                                 for (int m = 0; m < 4; ++m) { A[m] = dpp_ror1(acc[ai][bj][m][n][q]); B[m] = dpp_ror15(acc[ai][bj][m][n][q]); }
; #pragma unroll
;                                 for (int m = 0; m < 4; ++m) { const float pv = fr > 0 ? A[m] : (m > 0 ? A[m > 0 ? m - 1 : 0] : 0.f), nv = fr < 15 ? B[m] : (m < 3 ? B[m < 3 ? m + 1 : 3] : 0.f);
;                                     o[m][n][q] = siluf(bb[n][q] + w0[n][q] * pv + w1[n][q] * acc[ai][bj][m][n][q] + w2[n][q] * nv); } }
	v_add_f32_e32 v177, v200, v177
	v_add_f32_e32 v177, v177, v201
	v_mov_b32_dpp v218, v38 row_ror:15 row_mask:0xf bank_mask:0xf
	v_mul_f32_e32 v200, 0xbfb8aa3b, v177
	v_exp_f32_e32 v221, v200
	v_cndmask_b32_e64 v170, v179, v170, s[14:15]
	v_cndmask_b32_e64 v201, v204, v218, s[12:13]
	v_mov_b32_e32 v202, v54
	v_mov_b32_e32 v200, v154
	v_fma_f32 v170, v146, v170, v150
	v_pk_mul_f32 v[200:201], v[202:203], v[200:201]
	v_mov_b32_e32 v220, v171
	v_add_f32_e32 v170, v200, v170
	v_add_f32_e32 v170, v170, v201
	v_mul_f32_e32 v200, 0xbfb8aa3b, v170
	v_exp_f32_e32 v200, v200
	v_mov_b32_dpp v205, v38 row_ror:1 row_mask:0xf bank_mask:0xf
	v_mov_b32_dpp v220, v22 row_ror:15 row_mask:0xf bank_mask:0xf
	v_add_f32_e32 v201, 1.0, v221
	v_rcp_f32_e32 v204, v201
	v_add_f32_e32 v221, 1.0, v200
	v_cndmask_b32_e64 v179, v205, v179, s[14:15]
	v_cndmask_b32_e64 v201, v218, v220, s[12:13]
	v_mov_b32_e32 v202, v38
	v_mov_b32_e32 v200, v154
	v_fma_f32 v179, v146, v179, v150
	v_pk_mul_f32 v[200:201], v[202:203], v[200:201]
	v_mov_b32_e32 v219, v171
	v_add_f32_e32 v179, v200, v179
	v_add_f32_e32 v179, v179, v201
	v_mov_b32_dpp v219, v22 row_ror:1 row_mask:0xf bank_mask:0xf
	v_mul_f32_e32 v200, 0xbfb8aa3b, v179
	v_cndmask_b32_e64 v201, v219, v205, s[14:15]
	v_exp_f32_e32 v218, v200
	v_cndmask_b32_e64 v200, v220, 0, s[12:13]
	v_fma_f32 v146, v146, v201, v150
	v_mov_b32_e32 v202, v158
	v_mov_b32_e32 v203, v22
	v_mov_b32_e32 v201, v154
	v_pk_mul_f32 v[200:201], v[202:203], v[200:201]
	v_rcp_f32_e32 v154, v221
	v_add_f32_e32 v146, v201, v146
	v_add_f32_e32 v146, v200, v146
	v_mul_f32_e32 v150, 0xbfb8aa3b, v146
	v_exp_f32_e32 v150, v150
	v_add_f32_e32 v158, 1.0, v218
	v_rcp_f32_e32 v158, v158
	v_mul_f32_e32 v170, v170, v154
	v_add_f32_e32 v150, 1.0, v150
	v_rcp_f32_e32 v200, v150
	v_mov_b32_e32 v154, v171
	v_mul_f32_e32 v150, v179, v158
	v_mov_b32_e32 v158, v171
	v_mov_b32_dpp v154, v63 row_ror:1 row_mask:0xf bank_mask:0xf
	v_mov_b32_e32 v202, v171
	v_mul_f32_e32 v146, v146, v200
	v_mov_b32_dpp v158, v63 row_ror:15 row_mask:0xf bank_mask:0xf
	v_mov_b32_dpp v202, v55 row_ror:15 row_mask:0xf bank_mask:0xf
	v_cndmask_b32_e64 v200, v154, 0, s[14:15]
	v_cndmask_b32_e64 v201, v158, v202, s[12:13]
	v_fma_f32 v219, v147, v200, v151
	v_mov_b32_e32 v158, v63
	v_mov_b32_e32 v200, v155
	v_pk_mul_f32 v[200:201], v[158:159], v[200:201]
	v_mul_f32_e32 v177, v177, v204
	v_add_f32_e32 v158, v200, v219
	v_mov_b32_e32 v179, v171
	v_mov_b32_e32 v204, v171
	v_add_f32_e32 v219, v158, v201
	v_mov_b32_dpp v179, v55 row_ror:1 row_mask:0xf bank_mask:0xf
	v_mov_b32_dpp v204, v39 row_ror:15 row_mask:0xf bank_mask:0xf
	v_mul_f32_e32 v158, 0xbfb8aa3b, v219
	v_exp_f32_e32 v220, v158
	v_cndmask_b32_e64 v154, v179, v154, s[14:15]
	v_cndmask_b32_e64 v201, v202, v204, s[12:13]
	v_mov_b32_e32 v158, v55
	v_mov_b32_e32 v200, v155
	v_fma_f32 v154, v147, v154, v151
	v_pk_mul_f32 v[200:201], v[158:159], v[200:201]
	v_mov_b32_e32 v203, v171
	v_add_f32_e32 v154, v200, v154
	v_add_f32_e32 v202, v154, v201
	v_mul_f32_e32 v154, 0xbfb8aa3b, v202
	v_exp_f32_e32 v154, v154
	v_mov_b32_e32 v218, v171
	v_mov_b32_dpp v203, v39 row_ror:1 row_mask:0xf bank_mask:0xf
	v_add_f32_e32 v158, 1.0, v220
	v_mov_b32_dpp v218, v23 row_ror:15 row_mask:0xf bank_mask:0xf
	v_rcp_f32_e32 v220, v158
	v_add_f32_e32 v221, 1.0, v154
	v_cndmask_b32_e64 v154, v203, v179, s[14:15]
	v_cndmask_b32_e64 v201, v204, v218, s[12:13]
	v_mov_b32_e32 v158, v39
	v_mov_b32_e32 v200, v155
	v_fma_f32 v154, v147, v154, v151
	v_pk_mul_f32 v[200:201], v[158:159], v[200:201]
	v_mov_b32_e32 v205, v171
	v_add_f32_e32 v154, v200, v154
	v_add_f32_e32 v179, v154, v201
	v_mov_b32_dpp v205, v23 row_ror:1 row_mask:0xf bank_mask:0xf
	v_mul_f32_e32 v154, 0xbfb8aa3b, v179
	v_cndmask_b32_e64 v158, v205, v203, s[14:15]
	v_exp_f32_e32 v200, v154
	v_cndmask_b32_e64 v154, v218, 0, s[12:13]
	v_fma_f32 v147, v147, v158, v151
	v_mov_b32_e32 v158, v159
	v_mov_b32_e32 v159, v23
	v_pk_mul_f32 v[154:155], v[158:159], v[154:155]
	v_mov_b32_e32 v203, v171
	v_add_f32_e32 v147, v155, v147
	v_add_f32_e32 v147, v154, v147
	v_mul_f32_e32 v151, 0xbfb8aa3b, v147
	v_exp_f32_e32 v151, v151
	v_add_f32_e32 v155, 1.0, v200
	v_rcp_f32_e32 v158, v155
	v_rcp_f32_e32 v154, v221
	v_add_f32_e32 v151, 1.0, v151
	v_rcp_f32_e32 v159, v151
	v_mul_f32_e32 v151, v179, v158
	v_mov_b32_e32 v179, v171
	v_mov_b32_e32 v158, v171
	v_mov_b32_dpp v203, v56 row_ror:15 row_mask:0xf bank_mask:0xf
	v_mov_b32_dpp v179, v64 row_ror:1 row_mask:0xf bank_mask:0xf
	v_mov_b32_dpp v158, v64 row_ror:15 row_mask:0xf bank_mask:0xf
	v_cndmask_b32_e64 v200, v179, 0, s[14:15]
	v_mul_f32_e32 v155, v219, v220
	v_mul_f32_e32 v147, v147, v159
	v_cndmask_b32_e64 v159, v158, v203, s[12:13]
	v_fma_f32 v220, v148, v200, v152
	v_mov_b32_e32 v200, v64
	v_mov_b32_e32 v201, v160
	v_mov_b32_e32 v158, v156
	v_pk_mul_f32 v[158:159], v[200:201], v[158:159]
	v_mul_f32_e32 v154, v202, v154
	v_add_f32_e32 v158, v158, v220
	v_mov_b32_e32 v202, v171
	v_add_f32_e32 v220, v158, v159
	v_mov_b32_e32 v205, v171
	v_mov_b32_dpp v202, v56 row_ror:1 row_mask:0xf bank_mask:0xf
	v_mul_f32_e32 v158, 0xbfb8aa3b, v220
	v_mov_b32_dpp v205, v40 row_ror:15 row_mask:0xf bank_mask:0xf
	v_exp_f32_e32 v221, v158
	v_cndmask_b32_e64 v158, v202, v179, s[14:15]
	v_cndmask_b32_e64 v159, v203, v205, s[12:13]
	v_fma_f32 v179, v148, v158, v152
	v_mov_b32_e32 v200, v56
	v_mov_b32_e32 v158, v156
	v_pk_mul_f32 v[158:159], v[200:201], v[158:159]
	v_mov_b32_e32 v204, v171
	v_add_f32_e32 v158, v158, v179
	v_add_f32_e32 v179, v158, v159
	v_mul_f32_e32 v158, 0xbfb8aa3b, v179
	v_exp_f32_e32 v158, v158
	v_mov_b32_dpp v204, v40 row_ror:1 row_mask:0xf bank_mask:0xf
	v_mov_b32_e32 v219, v171
; __device__ __forceinline__ float siluf(float x) { return x * __builtin_amdgcn_rcpf(1.f + __expf(-x)); }
; __device__ __forceinline__ float dpp_ror1(float v) { return __builtin_bit_cast(float, __builtin_amdgcn_update_dpp(0, __builtin_bit_cast(int, v), 0x121, 0xf, 0xf, false)); }
; __device__ __forceinline__ float dpp_ror15(float v) { return __builtin_bit_cast(float, __builtin_amdgcn_update_dpp(0, __builtin_bit_cast(int, v), 0x12F, 0xf, 0xf, false)); }
;     __device__ __forceinline__ void operator()(const f32x4 (&acc)[2][2][4][2], const pg8::Unit& u, int wr, int wc, int fr, int fq_in) const {
;     ...
;                     for (int ai = 0; ai < 2; ++ai) {
;                         f32x4 o[4][2];
; #pragma unroll
;                         for (int n = 0; n < 2; ++n)
; #pragma unroll
;                             for (int q = 0; q < 4; ++q) { float A[4], B[4];
; #pragma unroll
;                                 for (int m = 0; m < 4; ++m) { A[m] = dpp_ror1(acc[ai][bj][m][n][q]); B[m] = dpp_ror15(acc[ai][bj][m][n][q]); }
; #pragma unroll
;                                 for (int m = 0; m < 4; ++m) { const float pv = fr > 0 ? A[m] : (m > 0 ? A[m > 0 ? m - 1 : 0] : 0.f), nv = fr < 15 ? B[m] : (m < 3 ? B[m < 3 ? m + 1 : 3] : 0.f);
;                                     o[m][n][q] = siluf(bb[n][q] + w0[n][q] * pv + w1[n][q] * acc[ai][bj][m][n][q] + w2[n][q] * nv); } }
	v_add_f32_e32 v159, 1.0, v221
	v_add_f32_e32 v221, 1.0, v158
	v_mov_b32_dpp v219, v24 row_ror:15 row_mask:0xf bank_mask:0xf
	v_cndmask_b32_e64 v158, v204, v202, s[14:15]
	v_rcp_f32_e32 v203, v159
	v_cndmask_b32_e64 v159, v205, v219, s[12:13]
	v_fma_f32 v202, v148, v158, v152
	v_mov_b32_e32 v200, v40
	v_mov_b32_e32 v158, v156
	v_pk_mul_f32 v[158:159], v[200:201], v[158:159]
	v_mov_b32_e32 v218, v171
	v_add_f32_e32 v158, v158, v202
	v_add_f32_e32 v202, v158, v159
	v_mov_b32_dpp v218, v24 row_ror:1 row_mask:0xf bank_mask:0xf
	v_mul_f32_e32 v158, 0xbfb8aa3b, v202
	v_cndmask_b32_e64 v159, v218, v204, s[14:15]
	v_exp_f32_e32 v205, v158
	v_cndmask_b32_e64 v158, v219, 0, s[12:13]
	v_fma_f32 v148, v148, v159, v152
	v_mov_b32_e32 v200, v160
	v_mov_b32_e32 v201, v24
	v_mov_b32_e32 v159, v156
	v_pk_mul_f32 v[158:159], v[200:201], v[158:159]
	v_mov_b32_e32 v201, v171
	v_add_f32_e32 v148, v159, v148
	v_add_f32_e32 v148, v158, v148
	v_mul_f32_e32 v152, 0xbfb8aa3b, v148
	v_exp_f32_e32 v152, v152
	v_add_f32_e32 v158, 1.0, v205
	v_rcp_f32_e32 v158, v158
	v_rcp_f32_e32 v156, v221
	v_add_f32_e32 v152, 1.0, v152
	v_rcp_f32_e32 v152, v152
	v_mul_f32_e32 v204, v202, v158
	v_mov_b32_dpp v201, v57 row_ror:15 row_mask:0xf bank_mask:0xf
	v_mov_b32_e32 v160, v65
	v_mul_f32_e32 v218, v148, v152
	v_mov_b32_e32 v148, v171
	v_mov_b32_e32 v152, v171
	v_mul_f32_e32 v200, v220, v203
	v_mov_b32_dpp v148, v65 row_ror:1 row_mask:0xf bank_mask:0xf
	v_mov_b32_dpp v152, v65 row_ror:15 row_mask:0xf bank_mask:0xf
	v_cndmask_b32_e64 v158, v148, 0, s[14:15]
	v_cndmask_b32_e64 v159, v152, v201, s[12:13]
	v_fma_f32 v152, v149, v158, v153
	v_mov_b32_e32 v158, v157
	v_pk_mul_f32 v[158:159], v[160:161], v[158:159]
	v_mul_f32_e32 v179, v179, v156
	v_add_f32_e32 v152, v158, v152
	v_mov_b32_e32 v156, v171
	v_mov_b32_e32 v203, v171
	v_add_f32_e32 v152, v152, v159
	v_mov_b32_dpp v156, v57 row_ror:1 row_mask:0xf bank_mask:0xf
	v_mov_b32_dpp v203, v41 row_ror:15 row_mask:0xf bank_mask:0xf
	v_mul_f32_e32 v158, 0xbfb8aa3b, v152
	v_exp_f32_e32 v220, v158
	v_cndmask_b32_e64 v148, v156, v148, s[14:15]
	v_cndmask_b32_e64 v159, v201, v203, s[12:13]
	v_mov_b32_e32 v160, v57
	v_mov_b32_e32 v158, v157
	v_fma_f32 v148, v149, v148, v153
	v_pk_mul_f32 v[158:159], v[160:161], v[158:159]
	v_mov_b32_e32 v202, v171
	v_add_f32_e32 v148, v158, v148
	v_add_f32_e32 v201, v148, v159
	v_mul_f32_e32 v148, 0xbfb8aa3b, v201
	v_exp_f32_e32 v148, v148
	v_mov_b32_e32 v219, v171
	v_mov_b32_dpp v202, v41 row_ror:1 row_mask:0xf bank_mask:0xf
	v_add_f32_e32 v158, 1.0, v220
	v_mov_b32_dpp v219, v25 row_ror:15 row_mask:0xf bank_mask:0xf
	v_rcp_f32_e32 v220, v158
	v_add_f32_e32 v221, 1.0, v148
	v_cndmask_b32_e64 v148, v202, v156, s[14:15]
	v_cndmask_b32_e64 v159, v203, v219, s[12:13]
	v_mov_b32_e32 v160, v41
	v_mov_b32_e32 v158, v157
	v_fma_f32 v148, v149, v148, v153
	v_pk_mul_f32 v[158:159], v[160:161], v[158:159]
	v_mov_b32_e32 v205, v171
	v_add_f32_e32 v148, v158, v148
	v_add_f32_e32 v158, v148, v159
	v_mov_b32_dpp v205, v25 row_ror:1 row_mask:0xf bank_mask:0xf
	v_mul_f32_e32 v148, 0xbfb8aa3b, v158
	v_exp_f32_e32 v159, v148
	v_cndmask_b32_e64 v148, v205, v202, s[14:15]
	v_cndmask_b32_e64 v156, v219, 0, s[12:13]
	v_fmac_f32_e32 v153, v149, v148
	v_mov_b32_e32 v148, v161
	v_mov_b32_e32 v149, v25
	v_pk_mul_f32 v[148:149], v[148:149], v[156:157]
	v_add_f32_e32 v156, 1.0, v159
	v_add_f32_e32 v149, v149, v153
	v_add_f32_e32 v148, v148, v149
	v_mul_f32_e32 v149, 0xbfb8aa3b, v148
	v_exp_f32_e32 v149, v149
	v_rcp_f32_e32 v153, v221
	v_rcp_f32_e32 v156, v156
	v_mov_b32_e32 v160, v171
	v_add_f32_e32 v149, 1.0, v149
	v_rcp_f32_e32 v149, v149
	v_mul_f32_e32 v159, v201, v153
	v_mul_f32_e32 v156, v158, v156
	v_mov_b32_dpp v160, v58 row_ror:1 row_mask:0xf bank_mask:0xf
	v_mul_f32_e32 v158, v148, v149
	v_mov_b32_e32 v148, v171
	v_mov_b32_e32 v201, v171
	v_mul_f32_e32 v157, v152, v220
	v_mov_b32_dpp v148, v58 row_ror:15 row_mask:0xf bank_mask:0xf
	v_mov_b32_dpp v201, v46 row_ror:15 row_mask:0xf bank_mask:0xf
	v_cndmask_b32_e64 v152, v160, 0, s[14:15]
	v_cndmask_b32_e64 v149, v148, v201, s[12:13]
	v_fma_f32 v220, v138, v152, v134
	v_mov_b32_e32 v152, v58
	v_mov_b32_e32 v153, v142
	v_mov_b32_e32 v148, v130
	v_pk_mul_f32 v[148:149], v[152:153], v[148:149]
	v_mov_b32_e32 v161, v171
	v_add_f32_e32 v148, v148, v220
	v_add_f32_e32 v220, v148, v149
	v_mov_b32_dpp v161, v46 row_ror:1 row_mask:0xf bank_mask:0xf
	v_mov_b32_e32 v203, v171
	v_mul_f32_e32 v148, 0xbfb8aa3b, v220
	v_exp_f32_e32 v221, v148
	v_mov_b32_dpp v203, v30 row_ror:15 row_mask:0xf bank_mask:0xf
	v_cndmask_b32_e64 v148, v161, v160, s[14:15]
	v_cndmask_b32_e64 v149, v201, v203, s[12:13]
	v_fma_f32 v160, v138, v148, v134
	v_mov_b32_e32 v152, v46
	v_mov_b32_e32 v148, v130
	v_pk_mul_f32 v[148:149], v[152:153], v[148:149]
	v_mov_b32_e32 v202, v171
	v_add_f32_e32 v148, v148, v160
	v_add_f32_e32 v160, v148, v149
	v_mul_f32_e32 v148, 0xbfb8aa3b, v160
	v_exp_f32_e32 v148, v148
	v_mov_b32_dpp v202, v30 row_ror:1 row_mask:0xf bank_mask:0xf
	v_mov_b32_e32 v219, v171
	v_add_f32_e32 v149, 1.0, v221
	v_add_f32_e32 v221, 1.0, v148
	v_mov_b32_dpp v219, v14 row_ror:15 row_mask:0xf bank_mask:0xf
	v_cndmask_b32_e64 v148, v202, v161, s[14:15]
	v_rcp_f32_e32 v201, v149
	v_cndmask_b32_e64 v149, v203, v219, s[12:13]
	v_fma_f32 v161, v138, v148, v134
	v_mov_b32_e32 v152, v30
	v_mov_b32_e32 v148, v130
	v_pk_mul_f32 v[148:149], v[152:153], v[148:149]
	v_mov_b32_e32 v205, v171
	v_add_f32_e32 v148, v148, v161
	v_add_f32_e32 v161, v148, v149
	v_mov_b32_dpp v205, v14 row_ror:1 row_mask:0xf bank_mask:0xf
	v_mul_f32_e32 v148, 0xbfb8aa3b, v161
	v_cndmask_b32_e64 v149, v205, v202, s[14:15]
	v_exp_f32_e32 v203, v148
; __device__ __forceinline__ float siluf(float x) { return x * __builtin_amdgcn_rcpf(1.f + __expf(-x)); }
; __device__ __forceinline__ float dpp_ror1(float v) { return __builtin_bit_cast(float, __builtin_amdgcn_update_dpp(0, __builtin_bit_cast(int, v), 0x121, 0xf, 0xf, false)); }
; __device__ __forceinline__ float dpp_ror15(float v) { return __builtin_bit_cast(float, __builtin_amdgcn_update_dpp(0, __builtin_bit_cast(int, v), 0x12F, 0xf, 0xf, false)); }
;     __device__ __forceinline__ void operator()(const f32x4 (&acc)[2][2][4][2], const pg8::Unit& u, int wr, int wc, int fr, int fq_in) const {
;     ...
;                     for (int ai = 0; ai < 2; ++ai) {
;                         f32x4 o[4][2];
; #pragma unroll
;                         for (int n = 0; n < 2; ++n)
; #pragma unroll
;                             for (int q = 0; q < 4; ++q) { float A[4], B[4];
; #pragma unroll
;                                 for (int m = 0; m < 4; ++m) { A[m] = dpp_ror1(acc[ai][bj][m][n][q]); B[m] = dpp_ror15(acc[ai][bj][m][n][q]); }
; #pragma unroll
;                                 for (int m = 0; m < 4; ++m) { const float pv = fr > 0 ? A[m] : (m > 0 ? A[m > 0 ? m - 1 : 0] : 0.f), nv = fr < 15 ? B[m] : (m < 3 ? B[m < 3 ? m + 1 : 3] : 0.f);
;                                     o[m][n][q] = siluf(bb[n][q] + w0[n][q] * pv + w1[n][q] * acc[ai][bj][m][n][q] + w2[n][q] * nv); } }
	v_cndmask_b32_e64 v148, v219, 0, s[12:13]
	v_fma_f32 v134, v138, v149, v134
	v_mov_b32_e32 v152, v142
	v_mov_b32_e32 v153, v14
	v_mov_b32_e32 v149, v130
	v_pk_mul_f32 v[148:149], v[152:153], v[148:149]
	v_rcp_f32_e32 v138, v221
	v_add_f32_e32 v130, v149, v134
	v_add_f32_e32 v130, v148, v130
	v_mul_f32_e32 v134, 0xbfb8aa3b, v130
	v_exp_f32_e32 v134, v134
	v_add_f32_e32 v142, 1.0, v203
	v_rcp_f32_e32 v142, v142
	v_mul_f32_e32 v138, v160, v138
	v_add_f32_e32 v134, 1.0, v134
	v_rcp_f32_e32 v134, v134
	v_mul_f32_e32 v152, v220, v201
	v_mov_b32_e32 v201, v171
	v_mul_f32_e32 v153, v161, v142
	v_mul_f32_e32 v160, v130, v134
	v_mov_b32_e32 v130, v171
	v_mov_b32_e32 v134, v171
	v_mov_b32_dpp v201, v47 row_ror:15 row_mask:0xf bank_mask:0xf
	v_mov_b32_dpp v130, v59 row_ror:1 row_mask:0xf bank_mask:0xf
	v_mov_b32_dpp v134, v59 row_ror:15 row_mask:0xf bank_mask:0xf
	v_cndmask_b32_e64 v142, v130, 0, s[14:15]
	v_cndmask_b32_e64 v149, v134, v201, s[12:13]
	v_fma_f32 v134, v139, v142, v135
	v_mov_b32_e32 v142, v59
	v_mov_b32_e32 v148, v131
	v_mov_b32_e32 v161, v171
	v_mov_b32_e32 v203, v171
	v_pk_mul_f32 v[148:149], v[142:143], v[148:149]
	v_mov_b32_dpp v161, v47 row_ror:1 row_mask:0xf bank_mask:0xf
	v_mov_b32_dpp v203, v31 row_ror:15 row_mask:0xf bank_mask:0xf
	v_add_f32_e32 v134, v148, v134
	v_add_f32_e32 v220, v134, v149
	v_cndmask_b32_e64 v130, v161, v130, s[14:15]
	v_cndmask_b32_e64 v149, v201, v203, s[12:13]
	v_mov_b32_e32 v142, v47
	v_mov_b32_e32 v148, v131
	v_fma_f32 v130, v139, v130, v135
	v_pk_mul_f32 v[148:149], v[142:143], v[148:149]
	v_mov_b32_e32 v202, v171
	v_add_f32_e32 v130, v148, v130
	v_add_f32_e32 v201, v130, v149
	v_mul_f32_e32 v130, 0xbfb8aa3b, v201
	v_exp_f32_e32 v130, v130
	v_mov_b32_e32 v219, v171
	v_mul_f32_e32 v134, 0xbfb8aa3b, v220
	v_mov_b32_dpp v202, v31 row_ror:1 row_mask:0xf bank_mask:0xf
	v_exp_f32_e32 v134, v134
	v_mov_b32_dpp v219, v15 row_ror:15 row_mask:0xf bank_mask:0xf
	v_add_f32_e32 v222, 1.0, v130
	v_cndmask_b32_e64 v130, v202, v161, s[14:15]
	v_cndmask_b32_e64 v149, v203, v219, s[12:13]
	v_mov_b32_e32 v142, v31
	v_mov_b32_e32 v148, v131
	v_fma_f32 v130, v139, v130, v135
	v_pk_mul_f32 v[148:149], v[142:143], v[148:149]
	v_mov_b32_e32 v205, v171
	v_add_f32_e32 v130, v148, v130
	v_add_f32_e32 v134, 1.0, v134
	v_mov_b32_dpp v205, v15 row_ror:1 row_mask:0xf bank_mask:0xf
	v_add_f32_e32 v142, v130, v149
	v_rcp_f32_e32 v221, v134
	v_mul_f32_e32 v130, 0xbfb8aa3b, v142
	v_cndmask_b32_e64 v134, v205, v202, s[14:15]
	v_exp_f32_e32 v148, v130
	v_cndmask_b32_e64 v130, v219, 0, s[12:13]
	v_fma_f32 v139, v139, v134, v135
	v_mov_b32_e32 v134, v143
	v_mov_b32_e32 v135, v15
	v_pk_mul_f32 v[130:131], v[134:135], v[130:131]
	v_rcp_f32_e32 v134, v222
	v_add_f32_e32 v131, v131, v139
	v_add_f32_e32 v130, v130, v131
	v_mul_f32_e32 v131, 0xbfb8aa3b, v130
	v_exp_f32_e32 v131, v131
	v_add_f32_e32 v135, 1.0, v148
	v_rcp_f32_e32 v135, v135
	v_mov_b32_e32 v149, v171
	v_add_f32_e32 v131, 1.0, v131
	v_rcp_f32_e32 v131, v131
	v_mul_f32_e32 v143, v201, v134
	v_mov_b32_dpp v149, v60 row_ror:1 row_mask:0xf bank_mask:0xf
	v_mov_b32_e32 v201, v171
	v_mul_f32_e32 v148, v130, v131
	v_mov_b32_e32 v130, v171
	v_mov_b32_dpp v201, v48 row_ror:15 row_mask:0xf bank_mask:0xf
	v_cndmask_b32_e64 v134, v149, 0, s[14:15]
	v_mov_b32_dpp v130, v60 row_ror:15 row_mask:0xf bank_mask:0xf
	v_mul_f32_e32 v139, v220, v221
	v_mul_f32_e32 v142, v142, v135
	v_cndmask_b32_e64 v131, v130, v201, s[12:13]
	v_fma_f32 v220, v140, v134, v136
	v_mov_b32_e32 v134, v60
	v_mov_b32_e32 v135, v144
	v_mov_b32_e32 v130, v132
	v_pk_mul_f32 v[130:131], v[134:135], v[130:131]
	v_mov_b32_e32 v161, v171
	v_add_f32_e32 v130, v130, v220
	v_add_f32_e32 v220, v130, v131
	v_mov_b32_dpp v161, v48 row_ror:1 row_mask:0xf bank_mask:0xf
	v_mov_b32_e32 v203, v171
	v_mul_f32_e32 v130, 0xbfb8aa3b, v220
	v_exp_f32_e32 v221, v130
	v_mov_b32_dpp v203, v32 row_ror:15 row_mask:0xf bank_mask:0xf
	v_cndmask_b32_e64 v130, v161, v149, s[14:15]
	v_cndmask_b32_e64 v131, v201, v203, s[12:13]
	v_fma_f32 v149, v140, v130, v136
	v_mov_b32_e32 v134, v48
	v_mov_b32_e32 v130, v132
	v_pk_mul_f32 v[130:131], v[134:135], v[130:131]
	v_mov_b32_e32 v202, v171
	v_add_f32_e32 v130, v130, v149
	v_add_f32_e32 v149, v130, v131
	v_mul_f32_e32 v130, 0xbfb8aa3b, v149
	v_exp_f32_e32 v130, v130
	v_mov_b32_dpp v202, v32 row_ror:1 row_mask:0xf bank_mask:0xf
	v_mov_b32_e32 v219, v171
	v_add_f32_e32 v131, 1.0, v221
	v_add_f32_e32 v221, 1.0, v130
	v_mov_b32_dpp v219, v16 row_ror:15 row_mask:0xf bank_mask:0xf
	v_cndmask_b32_e64 v130, v202, v161, s[14:15]
	v_rcp_f32_e32 v201, v131
	v_cndmask_b32_e64 v131, v203, v219, s[12:13]
	v_fma_f32 v161, v140, v130, v136
	v_mov_b32_e32 v134, v32
	v_mov_b32_e32 v130, v132
	v_pk_mul_f32 v[130:131], v[134:135], v[130:131]
	v_mov_b32_e32 v205, v171
	v_add_f32_e32 v130, v130, v161
	v_add_f32_e32 v161, v130, v131
	v_mov_b32_dpp v205, v16 row_ror:1 row_mask:0xf bank_mask:0xf
	v_mul_f32_e32 v130, 0xbfb8aa3b, v161
	v_cndmask_b32_e64 v131, v205, v202, s[14:15]
	v_exp_f32_e32 v203, v130
	v_cndmask_b32_e64 v130, v219, 0, s[12:13]
	v_fma_f32 v136, v140, v131, v136
	v_mov_b32_e32 v134, v144
	v_mov_b32_e32 v135, v16
	v_mov_b32_e32 v131, v132
	v_pk_mul_f32 v[130:131], v[134:135], v[130:131]
	v_rcp_f32_e32 v132, v221
	v_add_f32_e32 v131, v131, v136
	v_add_f32_e32 v130, v130, v131
	v_mul_f32_e32 v131, 0xbfb8aa3b, v130
	v_exp_f32_e32 v131, v131
	v_add_f32_e32 v134, 1.0, v203
	v_rcp_f32_e32 v134, v134
	v_mul_f32_e32 v136, v149, v132
	v_add_f32_e32 v131, 1.0, v131
	v_rcp_f32_e32 v131, v131
	v_mov_b32_e32 v132, v171
	v_mul_f32_e32 v140, v161, v134
	v_mov_b32_e32 v161, v171
	v_mul_f32_e32 v149, v130, v131
; __device__ __forceinline__ unsigned cvt_pk_bf16(float lo, float hi) { unsigned r; asm volatile("v_cvt_pk_bf16_f32 %0, %1, %2" : "=v"(r) : "v"(lo), "v"(hi)); return r; }
; __device__ __forceinline__ float siluf(float x) { return x * __builtin_amdgcn_rcpf(1.f + __expf(-x)); }
; __device__ __forceinline__ float dpp_ror1(float v) { return __builtin_bit_cast(float, __builtin_amdgcn_update_dpp(0, __builtin_bit_cast(int, v), 0x121, 0xf, 0xf, false)); }
; __device__ __forceinline__ float dpp_ror15(float v) { return __builtin_bit_cast(float, __builtin_amdgcn_update_dpp(0, __builtin_bit_cast(int, v), 0x12F, 0xf, 0xf, false)); }
;     __device__ __forceinline__ void operator()(const f32x4 (&acc)[2][2][4][2], const pg8::Unit& u, int wr, int wc, int fr, int fq_in) const {
;     ...
;                 for (int bj = 0; bj < 2; ++bj) {
;                     const int col = col0 + bj * 128;
;                     f32x4 w0[2], w1[2], w2[2], bb[2];
; #pragma unroll
;                     for (int n = 0; n < 2; ++n) { w0[n] = *(const f32x4*)(cw + col + 4 * n); w1[n] = *(const f32x4*)(cw + XBCW + col + 4 * n); w2[n] = *(const f32x4*)(cw + 2 * XBCW + col + 4 * n); bb[n] = *(const f32x4*)(cb + col + 4 * n); }
; #pragma unroll
;                     for (int ai = 0; ai < 2; ++ai) {
;                         f32x4 o[4][2];
; #pragma unroll
;                         for (int n = 0; n < 2; ++n)
; #pragma unroll
;                             for (int q = 0; q < 4; ++q) { float A[4], B[4];
; #pragma unroll
;                                 for (int m = 0; m < 4; ++m) { A[m] = dpp_ror1(acc[ai][bj][m][n][q]); B[m] = dpp_ror15(acc[ai][bj][m][n][q]); }
; #pragma unroll
;                                 for (int m = 0; m < 4; ++m) { const float pv = fr > 0 ? A[m] : (m > 0 ? A[m > 0 ? m - 1 : 0] : 0.f), nv = fr < 15 ? B[m] : (m < 3 ? B[m < 3 ? m + 1 : 3] : 0.f);
;                                     o[m][n][q] = siluf(bb[n][q] + w0[n][q] * pv + w1[n][q] * acc[ai][bj][m][n][q] + w2[n][q] * nv); } }
; #pragma unroll
;                         for (int m = 0; m < 4; ++m) { u32x4 w; w.x = pg8::cvt_pk_bf16(o[m][0][0], o[m][0][1]); w.y = pg8::cvt_pk_bf16(o[m][0][2], o[m][0][3]); w.z = pg8::cvt_pk_bf16(o[m][1][0], o[m][1][1]); w.w = pg8::cvt_pk_bf16(o[m][1][2], o[m][1][3]);
;                             *(u32x4*)(XBC + (size_t)(row0 + ai * 128 + m * 16) * XBCW + col) = w; }
	v_mov_b32_dpp v132, v61 row_ror:1 row_mask:0xf bank_mask:0xf
	v_mov_b32_e32 v130, v171
	v_mov_b32_dpp v161, v49 row_ror:15 row_mask:0xf bank_mask:0xf
	v_cndmask_b32_e64 v144, v132, 0, s[14:15]
	v_mov_b32_dpp v130, v61 row_ror:15 row_mask:0xf bank_mask:0xf
	v_cndmask_b32_e64 v131, v130, v161, s[12:13]
	v_fma_f32 v219, v141, v144, v137
	v_mov_b32_e32 v144, v61
	v_mov_b32_e32 v130, v133
	v_pk_mul_f32 v[130:131], v[144:145], v[130:131]
	v_mov_b32_e32 v134, v171
	v_add_f32_e32 v130, v130, v219
	v_add_f32_e32 v219, v130, v131
	v_mov_b32_dpp v134, v49 row_ror:1 row_mask:0xf bank_mask:0xf
	v_mov_b32_e32 v202, v171
	v_mul_f32_e32 v130, 0xbfb8aa3b, v219
	v_mul_f32_e32 v135, v220, v201
	v_mov_b32_dpp v202, v33 row_ror:15 row_mask:0xf bank_mask:0xf
	v_exp_f32_e32 v220, v130
	v_cndmask_b32_e64 v130, v134, v132, s[14:15]
	v_cndmask_b32_e64 v131, v161, v202, s[12:13]
	v_fma_f32 v132, v141, v130, v137
	v_mov_b32_e32 v144, v49
	v_mov_b32_e32 v130, v133
	v_pk_mul_f32 v[130:131], v[144:145], v[130:131]
	v_mov_b32_e32 v201, v171
	v_add_f32_e32 v130, v130, v132
	v_add_f32_e32 v161, v130, v131
	v_mul_f32_e32 v130, 0xbfb8aa3b, v161
	v_exp_f32_e32 v130, v130
	v_mov_b32_dpp v201, v33 row_ror:1 row_mask:0xf bank_mask:0xf
	v_mov_b32_e32 v205, v171
	v_add_f32_e32 v131, 1.0, v220
	v_add_f32_e32 v221, 1.0, v130
	v_mov_b32_dpp v205, v17 row_ror:15 row_mask:0xf bank_mask:0xf
	v_cndmask_b32_e64 v130, v201, v134, s[14:15]
	v_rcp_f32_e32 v220, v131
	v_cndmask_b32_e64 v131, v202, v205, s[12:13]
	v_fma_f32 v132, v141, v130, v137
	v_mov_b32_e32 v144, v33
	v_mov_b32_e32 v130, v133
	v_pk_mul_f32 v[130:131], v[144:145], v[130:131]
	v_mov_b32_e32 v203, v171
	v_add_f32_e32 v130, v130, v132
	v_add_f32_e32 v134, v130, v131
	v_mov_b32_dpp v203, v17 row_ror:1 row_mask:0xf bank_mask:0xf
	v_mul_f32_e32 v130, 0xbfb8aa3b, v134
	v_exp_f32_e32 v144, v130
	v_cndmask_b32_e64 v130, v203, v201, s[14:15]
	v_cndmask_b32_e64 v132, v205, 0, s[12:13]
	v_fmac_f32_e32 v137, v141, v130
	v_mov_b32_e32 v130, v145
	v_mov_b32_e32 v131, v17
	v_pk_mul_f32 v[130:131], v[130:131], v[132:133]
	v_add_f32_e32 v133, 1.0, v144
	v_add_f32_e32 v131, v131, v137
	v_add_f32_e32 v130, v130, v131
	v_mul_f32_e32 v131, 0xbfb8aa3b, v130
	v_exp_f32_e32 v131, v131
	v_rcp_f32_e32 v133, v133
	v_rcp_f32_e32 v132, v221
	v_mul_f32_e32 v137, v219, v220
	v_add_f32_e32 v131, 1.0, v131
	v_rcp_f32_e32 v131, v131
	v_mul_f32_e32 v144, v134, v133
	v_add_u32_e32 v134, 0x80, v178
	v_mul_f32_e32 v141, v161, v132
	v_mul_f32_e32 v145, v130, v131
	v_cvt_pk_bf16_f32 v130, v177, v155
	v_cvt_pk_bf16_f32 v131, v200, v157
	v_cvt_pk_bf16_f32 v132, v152, v139
	v_cvt_pk_bf16_f32 v133, v135, v137
	v_mad_i64_i32 v[134:135], s[0:1], v134, s93, v[206:207]
	v_lshl_add_u64 v[200:201], v[134:135], 0, v[208:209]
	v_add_u32_e32 v134, 0x90, v178
	v_mad_i64_i32 v[134:135], s[0:1], v134, s93, v[206:207]
	v_lshl_add_u64 v[202:203], v[134:135], 0, v[208:209]
	v_add_u32_e32 v134, 0xa0, v178
	global_store_dwordx4 v[200:201], v[130:133], off nt
	v_mad_i64_i32 v[134:135], s[0:1], v134, s93, v[206:207]
	s_nop 0
	v_cvt_pk_bf16_f32 v130, v170, v154
	v_cvt_pk_bf16_f32 v131, v179, v159
	v_cvt_pk_bf16_f32 v132, v138, v143
	v_cvt_pk_bf16_f32 v133, v136, v141
	global_store_dwordx4 v[202:203], v[130:133], off nt
	v_mov_b32_e32 v170, v171
	v_mov_b32_e32 v177, v171
	v_cvt_pk_bf16_f32 v130, v150, v151
	v_cvt_pk_bf16_f32 v131, v204, v156
	v_lshl_add_u64 v[204:205], v[134:135], 0, v[208:209]
	v_add_u32_e32 v134, 0xb0, v178
	v_mad_i64_i32 v[134:135], s[0:1], v134, s93, v[206:207]
	v_cvt_pk_bf16_f32 v132, v153, v142
	v_cvt_pk_bf16_f32 v133, v140, v144
	v_lshl_add_u64 v[206:207], v[134:135], 0, v[208:209]
	global_store_dwordx4 v[204:205], v[130:133], off nt
	v_mov_b32_dpp v170, v114 row_ror:1 row_mask:0xf bank_mask:0xf
	v_mov_b32_dpp v177, v114 row_ror:15 row_mask:0xf bank_mask:0xf
	v_cvt_pk_bf16_f32 v130, v146, v147
	v_cvt_pk_bf16_f32 v131, v218, v158
	v_cvt_pk_bf16_f32 v132, v160, v148
	v_cvt_pk_bf16_f32 v133, v149, v145
	global_store_dwordx4 v[206:207], v[130:133], off nt
	global_load_dwordx4 v[146:149], v[182:183], off offset:512
	global_load_dwordx4 v[150:153], v[190:191], off offset:512
	global_load_dwordx4 v[158:161], v[188:189], off offset:512
	global_load_dwordx4 v[154:157], v[184:185], off offset:512
	global_load_dwordx4 v[138:141], v[182:183], off offset:528
	global_load_dwordx4 v[130:133], v[184:185], off offset:528
	global_load_dwordx4 v[142:145], v[188:189], off offset:528
	global_load_dwordx4 v[134:137], v[190:191], off offset:528
	v_mov_b32_e32 v188, v171
	v_cndmask_b32_e64 v182, v170, 0, s[14:15]
	v_mov_b32_e32 v184, v114
	v_mov_b32_dpp v188, v98 row_ror:15 row_mask:0xf bank_mask:0xf
	v_cndmask_b32_e64 v183, v177, v188, s[12:13]
	v_mov_b32_e32 v179, v171
	v_mov_b32_e32 v190, v171
	v_mov_b32_e32 v189, v171
	v_mov_b32_dpp v179, v98 row_ror:1 row_mask:0xf bank_mask:0xf
	v_mov_b32_dpp v190, v82 row_ror:15 row_mask:0xf bank_mask:0xf
	v_cndmask_b32_e64 v170, v179, v170, s[14:15]
	v_mov_b32_e32 v208, v171
	v_mov_b32_dpp v189, v82 row_ror:1 row_mask:0xf bank_mask:0xf
	v_cndmask_b32_e64 v179, v189, v179, s[14:15]
	v_mov_b32_dpp v208, v70 row_ror:15 row_mask:0xf bank_mask:0xf
	v_mov_b32_e32 v191, v171
	v_mov_b32_e32 v219, v171
	v_mov_b32_e32 v218, v171
	v_mov_b32_dpp v191, v70 row_ror:1 row_mask:0xf bank_mask:0xf
	v_mov_b32_dpp v219, v71 row_ror:15 row_mask:0xf bank_mask:0xf
	v_mov_b32_dpp v218, v71 row_ror:1 row_mask:0xf bank_mask:0xf
	v_mov_b32_dpp v223, v72 row_ror:15 row_mask:0xf bank_mask:0xf
	v_mov_b32_e32 v222, v171
	v_mov_b32_dpp v227, v73 row_ror:15 row_mask:0xf bank_mask:0xf
	v_mov_b32_e32 v226, v171
	v_mov_b32_dpp v222, v72 row_ror:1 row_mask:0xf bank_mask:0xf
	v_mov_b32_e32 v231, v171
	v_mov_b32_dpp v226, v73 row_ror:1 row_mask:0xf bank_mask:0xf
	v_mov_b32_e32 v230, v171
	v_mov_b32_dpp v231, v66 row_ror:15 row_mask:0xf bank_mask:0xf
	v_mov_b32_dpp v235, v67 row_ror:15 row_mask:0xf bank_mask:0xf
	v_mov_b32_dpp v230, v66 row_ror:1 row_mask:0xf bank_mask:0xf
	v_mov_b32_e32 v234, v171
	v_mov_b32_dpp v243, v69 row_ror:15 row_mask:0xf bank_mask:0xf
	v_mov_b32_dpp v242, v69 row_ror:1 row_mask:0xf bank_mask:0xf
	v_mov_b32_dpp v234, v67 row_ror:1 row_mask:0xf bank_mask:0xf
	s_mov_b64 s[0:1], 0
	s_waitcnt vmcnt(6)
; __device__ __forceinline__ float siluf(float x) { return x * __builtin_amdgcn_rcpf(1.f + __expf(-x)); }
; __device__ __forceinline__ float dpp_ror1(float v) { return __builtin_bit_cast(float, __builtin_amdgcn_update_dpp(0, __builtin_bit_cast(int, v), 0x121, 0xf, 0xf, false)); }
; __device__ __forceinline__ float dpp_ror15(float v) { return __builtin_bit_cast(float, __builtin_amdgcn_update_dpp(0, __builtin_bit_cast(int, v), 0x12F, 0xf, 0xf, false)); }
;     __device__ __forceinline__ void operator()(const f32x4 (&acc)[2][2][4][2], const pg8::Unit& u, int wr, int wc, int fr, int fq_in) const {
;     ...
;                     for (int ai = 0; ai < 2; ++ai) {
;                         f32x4 o[4][2];
; #pragma unroll
;                         for (int n = 0; n < 2; ++n)
; #pragma unroll
;                             for (int q = 0; q < 4; ++q) { float A[4], B[4];
; #pragma unroll
;                                 for (int m = 0; m < 4; ++m) { A[m] = dpp_ror1(acc[ai][bj][m][n][q]); B[m] = dpp_ror15(acc[ai][bj][m][n][q]); }
; #pragma unroll
;                                 for (int m = 0; m < 4; ++m) { const float pv = fr > 0 ? A[m] : (m > 0 ? A[m > 0 ? m - 1 : 0] : 0.f), nv = fr < 15 ? B[m] : (m < 3 ? B[m < 3 ? m + 1 : 3] : 0.f);
;                                     o[m][n][q] = siluf(bb[n][q] + w0[n][q] * pv + w1[n][q] * acc[ai][bj][m][n][q] + w2[n][q] * nv); } }
	v_fma_f32 v177, v146, v182, v150
	s_waitcnt vmcnt(5)
	v_mov_b32_e32 v185, v158
	s_waitcnt vmcnt(4)
	v_mov_b32_e32 v182, v154
	v_pk_mul_f32 v[182:183], v[184:185], v[182:183]
	v_mov_b32_e32 v184, v98
	v_add_f32_e32 v177, v182, v177
	v_add_f32_e32 v177, v177, v183
	v_mul_f32_e32 v182, 0xbfb8aa3b, v177
	v_exp_f32_e32 v209, v182
	v_cndmask_b32_e64 v183, v188, v190, s[12:13]
	v_mov_b32_e32 v182, v154
	v_fma_f32 v170, v146, v170, v150
	v_pk_mul_f32 v[182:183], v[184:185], v[182:183]
	v_mov_b32_e32 v184, v82
	v_add_f32_e32 v170, v182, v170
	v_add_f32_e32 v170, v170, v183
	v_mul_f32_e32 v182, 0xbfb8aa3b, v170
	v_exp_f32_e32 v182, v182
	v_add_f32_e32 v183, 1.0, v209
	v_rcp_f32_e32 v188, v183
	v_cndmask_b32_e64 v183, v190, v208, s[12:13]
	v_add_f32_e32 v209, 1.0, v182
	v_mov_b32_e32 v182, v154
	v_fma_f32 v179, v146, v179, v150
	v_pk_mul_f32 v[182:183], v[184:185], v[182:183]
	v_mov_b32_e32 v184, v158
	v_add_f32_e32 v179, v182, v179
	v_add_f32_e32 v190, v179, v183
	v_cndmask_b32_e64 v183, v191, v189, s[14:15]
	v_cndmask_b32_e64 v182, v208, 0, s[12:13]
	v_fma_f32 v189, v146, v183, v150
	v_mov_b32_e32 v185, v70
	v_mov_b32_e32 v183, v154
	v_pk_mul_f32 v[182:183], v[184:185], v[182:183]
	v_mul_f32_e32 v179, 0xbfb8aa3b, v190
	v_add_f32_e32 v183, v183, v189
	v_add_f32_e32 v183, v182, v183
	v_exp_f32_e32 v179, v179
	v_mul_f32_e32 v182, 0xbfb8aa3b, v183
	v_exp_f32_e32 v182, v182
	v_rcp_f32_e32 v184, v209
	v_add_f32_e32 v179, 1.0, v179
	v_rcp_f32_e32 v185, v179
	v_add_f32_e32 v179, 1.0, v182
	v_rcp_f32_e32 v189, v179
	v_mul_f32_e32 v179, v170, v184
	v_mov_b32_e32 v184, v171
	v_mov_b32_e32 v191, v171
	v_mul_f32_e32 v170, v183, v189
	v_mov_b32_e32 v183, v171
	v_mul_f32_e32 v182, v177, v188
	v_mov_b32_dpp v184, v115 row_ror:15 row_mask:0xf bank_mask:0xf
	v_mov_b32_dpp v183, v115 row_ror:1 row_mask:0xf bank_mask:0xf
	v_mov_b32_dpp v191, v99 row_ror:15 row_mask:0xf bank_mask:0xf
	v_cndmask_b32_e64 v188, v183, 0, s[14:15]
	v_mul_f32_e32 v177, v190, v185
	v_cndmask_b32_e64 v185, v184, v191, s[12:13]
	v_fma_f32 v220, v147, v188, v151
	v_mov_b32_e32 v188, v115
	v_mov_b32_e32 v189, v159
	v_mov_b32_e32 v184, v155
	v_pk_mul_f32 v[184:185], v[188:189], v[184:185]
	v_mov_b32_e32 v190, v171
	v_add_f32_e32 v184, v184, v220
	v_mov_b32_e32 v209, v171
	v_add_f32_e32 v220, v184, v185
	v_mov_b32_dpp v190, v99 row_ror:1 row_mask:0xf bank_mask:0xf
	v_mov_b32_dpp v209, v83 row_ror:15 row_mask:0xf bank_mask:0xf
	v_mul_f32_e32 v184, 0xbfb8aa3b, v220
	v_exp_f32_e32 v221, v184
	v_cndmask_b32_e64 v183, v190, v183, s[14:15]
	v_cndmask_b32_e64 v185, v191, v209, s[12:13]
	v_mov_b32_e32 v188, v99
	v_mov_b32_e32 v184, v155
	v_fma_f32 v183, v147, v183, v151
	v_pk_mul_f32 v[184:185], v[188:189], v[184:185]
	v_mov_b32_e32 v208, v171
	v_add_f32_e32 v183, v184, v183
	v_add_f32_e32 v183, v183, v185
	v_mul_f32_e32 v184, 0xbfb8aa3b, v183
	v_exp_f32_e32 v184, v184
	v_mov_b32_dpp v208, v83 row_ror:1 row_mask:0xf bank_mask:0xf
	v_add_f32_e32 v185, 1.0, v221
	v_rcp_f32_e32 v191, v185
	v_add_f32_e32 v221, 1.0, v184
	v_cndmask_b32_e64 v184, v208, v190, s[14:15]
	v_cndmask_b32_e64 v185, v209, v219, s[12:13]
	v_fma_f32 v190, v147, v184, v151
	v_mov_b32_e32 v188, v83
	v_mov_b32_e32 v184, v155
	v_pk_mul_f32 v[184:185], v[188:189], v[184:185]
	v_mov_b32_e32 v188, v159
	v_add_f32_e32 v184, v184, v190
	v_add_f32_e32 v190, v184, v185
	v_mul_f32_e32 v184, 0xbfb8aa3b, v190
	v_cndmask_b32_e64 v185, v218, v208, s[14:15]
	v_exp_f32_e32 v209, v184
	v_cndmask_b32_e64 v184, v219, 0, s[12:13]
	v_fma_f32 v208, v147, v185, v151
	v_mov_b32_e32 v189, v71
	v_mov_b32_e32 v185, v155
	v_pk_mul_f32 v[184:185], v[188:189], v[184:185]
	v_add_f32_e32 v188, 1.0, v209
	v_add_f32_e32 v185, v185, v208
	v_add_f32_e32 v189, v184, v185
	v_mul_f32_e32 v184, 0xbfb8aa3b, v189
	v_exp_f32_e32 v184, v184
	v_rcp_f32_e32 v185, v221
	v_rcp_f32_e32 v208, v188
	v_mov_b32_e32 v219, v171
	v_add_f32_e32 v184, 1.0, v184
	v_rcp_f32_e32 v209, v184
	v_mul_f32_e32 v185, v183, v185
	v_mul_f32_e32 v184, v190, v208
	v_mov_b32_e32 v190, v171
	v_mul_f32_e32 v183, v189, v209
	v_mov_b32_e32 v189, v171
	v_mov_b32_dpp v190, v116 row_ror:15 row_mask:0xf bank_mask:0xf
	v_mov_b32_dpp v219, v100 row_ror:15 row_mask:0xf bank_mask:0xf
	v_mov_b32_dpp v189, v116 row_ror:1 row_mask:0xf bank_mask:0xf
	v_cndmask_b32_e64 v208, v189, 0, s[14:15]
	v_mul_f32_e32 v188, v220, v191
	v_cndmask_b32_e64 v191, v190, v219, s[12:13]
	v_fma_f32 v224, v148, v208, v152
	v_mov_b32_e32 v208, v116
	v_mov_b32_e32 v209, v160
	v_mov_b32_e32 v190, v156
	v_pk_mul_f32 v[190:191], v[208:209], v[190:191]
	v_mov_b32_e32 v218, v171
	v_add_f32_e32 v190, v190, v224
	v_mov_b32_e32 v221, v171
	v_add_f32_e32 v224, v190, v191
	v_mov_b32_dpp v218, v100 row_ror:1 row_mask:0xf bank_mask:0xf
	v_mov_b32_dpp v221, v84 row_ror:15 row_mask:0xf bank_mask:0xf
	v_mul_f32_e32 v190, 0xbfb8aa3b, v224
	v_exp_f32_e32 v225, v190
	v_cndmask_b32_e64 v189, v218, v189, s[14:15]
	v_cndmask_b32_e64 v191, v219, v221, s[12:13]
	v_mov_b32_e32 v208, v100
	v_mov_b32_e32 v190, v156
	v_fma_f32 v189, v148, v189, v152
	v_pk_mul_f32 v[190:191], v[208:209], v[190:191]
	v_mov_b32_e32 v220, v171
	v_add_f32_e32 v189, v190, v189
	v_add_f32_e32 v189, v189, v191
	v_mul_f32_e32 v190, 0xbfb8aa3b, v189
	v_exp_f32_e32 v190, v190
	v_mov_b32_dpp v220, v84 row_ror:1 row_mask:0xf bank_mask:0xf
	v_add_f32_e32 v191, 1.0, v225
	v_rcp_f32_e32 v219, v191
	v_add_f32_e32 v225, 1.0, v190
	v_cndmask_b32_e64 v190, v220, v218, s[14:15]
	v_cndmask_b32_e64 v191, v221, v223, s[12:13]
	v_fma_f32 v218, v148, v190, v152
	v_mov_b32_e32 v208, v84
	v_mov_b32_e32 v190, v156
	v_pk_mul_f32 v[190:191], v[208:209], v[190:191]
	v_mov_b32_e32 v208, v160
	v_add_f32_e32 v190, v190, v218
; __device__ __forceinline__ float siluf(float x) { return x * __builtin_amdgcn_rcpf(1.f + __expf(-x)); }
; __device__ __forceinline__ float dpp_ror1(float v) { return __builtin_bit_cast(float, __builtin_amdgcn_update_dpp(0, __builtin_bit_cast(int, v), 0x121, 0xf, 0xf, false)); }
; __device__ __forceinline__ float dpp_ror15(float v) { return __builtin_bit_cast(float, __builtin_amdgcn_update_dpp(0, __builtin_bit_cast(int, v), 0x12F, 0xf, 0xf, false)); }
;     __device__ __forceinline__ void operator()(const f32x4 (&acc)[2][2][4][2], const pg8::Unit& u, int wr, int wc, int fr, int fq_in) const {
;     ...
;                     for (int n = 0; n < 2; ++n) { w0[n] = *(const f32x4*)(cw + col + 4 * n); w1[n] = *(const f32x4*)(cw + XBCW + col + 4 * n); w2[n] = *(const f32x4*)(cw + 2 * XBCW + col + 4 * n); bb[n] = *(const f32x4*)(cb + col + 4 * n); }
; #pragma unroll
;                     for (int ai = 0; ai < 2; ++ai) {
;                         f32x4 o[4][2];
; #pragma unroll
;                         for (int n = 0; n < 2; ++n)
; #pragma unroll
;                             for (int q = 0; q < 4; ++q) { float A[4], B[4];
; #pragma unroll
;                                 for (int m = 0; m < 4; ++m) { A[m] = dpp_ror1(acc[ai][bj][m][n][q]); B[m] = dpp_ror15(acc[ai][bj][m][n][q]); }
; #pragma unroll
;                                 for (int m = 0; m < 4; ++m) { const float pv = fr > 0 ? A[m] : (m > 0 ? A[m > 0 ? m - 1 : 0] : 0.f), nv = fr < 15 ? B[m] : (m < 3 ? B[m < 3 ? m + 1 : 3] : 0.f);
;                                     o[m][n][q] = siluf(bb[n][q] + w0[n][q] * pv + w1[n][q] * acc[ai][bj][m][n][q] + w2[n][q] * nv); } }
	v_add_f32_e32 v218, v190, v191
	v_mul_f32_e32 v190, 0xbfb8aa3b, v218
	v_cndmask_b32_e64 v191, v222, v220, s[14:15]
	v_exp_f32_e32 v221, v190
	v_cndmask_b32_e64 v190, v223, 0, s[12:13]
	v_fma_f32 v220, v148, v191, v152
	v_mov_b32_e32 v209, v72
	v_mov_b32_e32 v191, v156
	v_pk_mul_f32 v[190:191], v[208:209], v[190:191]
	v_rcp_f32_e32 v208, v225
	v_add_f32_e32 v191, v191, v220
	v_add_f32_e32 v190, v190, v191
	v_mul_f32_e32 v191, 0xbfb8aa3b, v190
	v_exp_f32_e32 v191, v191
	v_add_f32_e32 v209, 1.0, v221
	v_rcp_f32_e32 v209, v209
	v_mul_f32_e32 v220, v189, v208
	v_add_f32_e32 v191, 1.0, v191
	v_rcp_f32_e32 v191, v191
	v_mov_b32_e32 v189, v171
	v_mov_b32_e32 v223, v171
	v_mul_f32_e32 v218, v218, v209
	v_mul_f32_e32 v221, v190, v191
	v_mov_b32_dpp v189, v117 row_ror:1 row_mask:0xf bank_mask:0xf
	v_mov_b32_e32 v190, v171
	v_mov_b32_dpp v223, v101 row_ror:15 row_mask:0xf bank_mask:0xf
	v_cndmask_b32_e64 v208, v189, 0, s[14:15]
	v_mov_b32_dpp v190, v117 row_ror:15 row_mask:0xf bank_mask:0xf
	v_cndmask_b32_e64 v191, v190, v223, s[12:13]
	v_fma_f32 v228, v149, v208, v153
	v_mov_b32_e32 v208, v117
	v_mov_b32_e32 v209, v161
	v_mov_b32_e32 v190, v157
	v_pk_mul_f32 v[190:191], v[208:209], v[190:191]
	v_mov_b32_e32 v222, v171
	v_add_f32_e32 v190, v190, v228
	v_mov_b32_e32 v225, v171
	v_add_f32_e32 v228, v190, v191
	v_mov_b32_dpp v222, v101 row_ror:1 row_mask:0xf bank_mask:0xf
	v_mov_b32_dpp v225, v85 row_ror:15 row_mask:0xf bank_mask:0xf
	v_mul_f32_e32 v190, 0xbfb8aa3b, v228
	v_exp_f32_e32 v229, v190
	v_cndmask_b32_e64 v189, v222, v189, s[14:15]
	v_cndmask_b32_e64 v191, v223, v225, s[12:13]
	v_mov_b32_e32 v208, v101
	v_mov_b32_e32 v190, v157
	v_fma_f32 v189, v149, v189, v153
	v_pk_mul_f32 v[190:191], v[208:209], v[190:191]
	v_mul_f32_e32 v219, v224, v219
	v_add_f32_e32 v189, v190, v189
	v_add_f32_e32 v189, v189, v191
	v_mul_f32_e32 v190, 0xbfb8aa3b, v189
	v_exp_f32_e32 v190, v190
	v_mov_b32_e32 v224, v171
	v_add_f32_e32 v191, 1.0, v229
	v_rcp_f32_e32 v223, v191
	v_mov_b32_dpp v224, v85 row_ror:1 row_mask:0xf bank_mask:0xf
	v_add_f32_e32 v229, 1.0, v190
	v_cndmask_b32_e64 v190, v224, v222, s[14:15]
	v_cndmask_b32_e64 v191, v225, v227, s[12:13]
	v_fma_f32 v222, v149, v190, v153
	v_mov_b32_e32 v208, v85
	v_mov_b32_e32 v190, v157
	v_pk_mul_f32 v[190:191], v[208:209], v[190:191]
	v_mov_b32_e32 v208, v161
	v_add_f32_e32 v190, v190, v222
	v_add_f32_e32 v222, v190, v191
	v_mul_f32_e32 v190, 0xbfb8aa3b, v222
	v_cndmask_b32_e64 v191, v226, v224, s[14:15]
	v_exp_f32_e32 v225, v190
	v_cndmask_b32_e64 v190, v227, 0, s[12:13]
	v_fma_f32 v224, v149, v191, v153
	v_mov_b32_e32 v209, v73
	v_mov_b32_e32 v191, v157
	v_pk_mul_f32 v[190:191], v[208:209], v[190:191]
	v_rcp_f32_e32 v208, v229
	v_add_f32_e32 v191, v191, v224
	v_add_f32_e32 v190, v190, v191
	v_mul_f32_e32 v191, 0xbfb8aa3b, v190
	v_exp_f32_e32 v191, v191
	v_add_f32_e32 v209, 1.0, v225
	v_rcp_f32_e32 v209, v209
	v_mul_f32_e32 v224, v189, v208
	v_add_f32_e32 v191, 1.0, v191
	v_rcp_f32_e32 v191, v191
	v_mov_b32_e32 v189, v171
	v_mov_b32_e32 v227, v171
	v_mul_f32_e32 v222, v222, v209
	v_mul_f32_e32 v225, v190, v191
	v_mov_b32_dpp v189, v106 row_ror:1 row_mask:0xf bank_mask:0xf
	v_mov_b32_e32 v190, v171
	v_mov_b32_dpp v227, v90 row_ror:15 row_mask:0xf bank_mask:0xf
	v_cndmask_b32_e64 v208, v189, 0, s[14:15]
	v_mov_b32_dpp v190, v106 row_ror:15 row_mask:0xf bank_mask:0xf
	v_cndmask_b32_e64 v191, v190, v227, s[12:13]
	s_waitcnt vmcnt(0)
	v_fma_f32 v232, v138, v208, v134
	v_mov_b32_e32 v208, v106
	v_mov_b32_e32 v209, v142
	v_mov_b32_e32 v190, v130
	v_pk_mul_f32 v[190:191], v[208:209], v[190:191]
	v_mov_b32_e32 v226, v171
	v_add_f32_e32 v190, v190, v232
	v_mov_b32_e32 v229, v171
	v_add_f32_e32 v232, v190, v191
	v_mov_b32_dpp v226, v90 row_ror:1 row_mask:0xf bank_mask:0xf
	v_mov_b32_dpp v229, v74 row_ror:15 row_mask:0xf bank_mask:0xf
	v_mul_f32_e32 v190, 0xbfb8aa3b, v232
	v_exp_f32_e32 v233, v190
	v_cndmask_b32_e64 v189, v226, v189, s[14:15]
	v_cndmask_b32_e64 v191, v227, v229, s[12:13]
	v_mov_b32_e32 v208, v90
	v_mov_b32_e32 v190, v130
	v_fma_f32 v189, v138, v189, v134
	v_pk_mul_f32 v[190:191], v[208:209], v[190:191]
	v_mul_f32_e32 v223, v228, v223
	v_add_f32_e32 v189, v190, v189
	v_add_f32_e32 v189, v189, v191
	v_mul_f32_e32 v190, 0xbfb8aa3b, v189
	v_exp_f32_e32 v190, v190
	v_mov_b32_e32 v228, v171
	v_add_f32_e32 v191, 1.0, v233
	v_rcp_f32_e32 v227, v191
	v_mov_b32_dpp v228, v74 row_ror:1 row_mask:0xf bank_mask:0xf
	v_add_f32_e32 v233, 1.0, v190
	v_cndmask_b32_e64 v190, v228, v226, s[14:15]
	v_cndmask_b32_e64 v191, v229, v231, s[12:13]
	v_fma_f32 v226, v138, v190, v134
	v_mov_b32_e32 v208, v74
	v_mov_b32_e32 v190, v130
	v_pk_mul_f32 v[190:191], v[208:209], v[190:191]
	v_mov_b32_e32 v208, v142
	v_add_f32_e32 v190, v190, v226
	v_add_f32_e32 v226, v190, v191
	v_mul_f32_e32 v190, 0xbfb8aa3b, v226
	v_cndmask_b32_e64 v191, v230, v228, s[14:15]
	v_exp_f32_e32 v229, v190
	v_cndmask_b32_e64 v190, v231, 0, s[12:13]
	v_fma_f32 v228, v138, v191, v134
	v_mov_b32_e32 v209, v66
	v_mov_b32_e32 v191, v130
	v_pk_mul_f32 v[190:191], v[208:209], v[190:191]
	v_rcp_f32_e32 v208, v233
	v_add_f32_e32 v191, v191, v228
	v_add_f32_e32 v190, v190, v191
	v_mul_f32_e32 v191, 0xbfb8aa3b, v190
	v_exp_f32_e32 v191, v191
	v_add_f32_e32 v209, 1.0, v229
	v_rcp_f32_e32 v209, v209
	v_mul_f32_e32 v228, v189, v208
	v_add_f32_e32 v191, 1.0, v191
	v_rcp_f32_e32 v191, v191
	v_mov_b32_e32 v189, v171
	v_mov_b32_e32 v231, v171
	v_mul_f32_e32 v226, v226, v209
	v_mul_f32_e32 v229, v190, v191
	v_mov_b32_dpp v189, v107 row_ror:1 row_mask:0xf bank_mask:0xf
	v_mov_b32_e32 v190, v171
	v_mov_b32_dpp v231, v91 row_ror:15 row_mask:0xf bank_mask:0xf
	v_cndmask_b32_e64 v208, v189, 0, s[14:15]
; __device__ __forceinline__ float siluf(float x) { return x * __builtin_amdgcn_rcpf(1.f + __expf(-x)); }
; __device__ __forceinline__ float dpp_ror1(float v) { return __builtin_bit_cast(float, __builtin_amdgcn_update_dpp(0, __builtin_bit_cast(int, v), 0x121, 0xf, 0xf, false)); }
; __device__ __forceinline__ float dpp_ror15(float v) { return __builtin_bit_cast(float, __builtin_amdgcn_update_dpp(0, __builtin_bit_cast(int, v), 0x12F, 0xf, 0xf, false)); }
;     __device__ __forceinline__ void operator()(const f32x4 (&acc)[2][2][4][2], const pg8::Unit& u, int wr, int wc, int fr, int fq_in) const {
;     ...
;                     for (int n = 0; n < 2; ++n) { w0[n] = *(const f32x4*)(cw + col + 4 * n); w1[n] = *(const f32x4*)(cw + XBCW + col + 4 * n); w2[n] = *(const f32x4*)(cw + 2 * XBCW + col + 4 * n); bb[n] = *(const f32x4*)(cb + col + 4 * n); }
; #pragma unroll
;                     for (int ai = 0; ai < 2; ++ai) {
;                         f32x4 o[4][2];
; #pragma unroll
;                         for (int n = 0; n < 2; ++n)
; #pragma unroll
;                             for (int q = 0; q < 4; ++q) { float A[4], B[4];
; #pragma unroll
;                                 for (int m = 0; m < 4; ++m) { A[m] = dpp_ror1(acc[ai][bj][m][n][q]); B[m] = dpp_ror15(acc[ai][bj][m][n][q]); }
; #pragma unroll
;                                 for (int m = 0; m < 4; ++m) { const float pv = fr > 0 ? A[m] : (m > 0 ? A[m > 0 ? m - 1 : 0] : 0.f), nv = fr < 15 ? B[m] : (m < 3 ? B[m < 3 ? m + 1 : 3] : 0.f);
;                                     o[m][n][q] = siluf(bb[n][q] + w0[n][q] * pv + w1[n][q] * acc[ai][bj][m][n][q] + w2[n][q] * nv); } }
	v_mov_b32_dpp v190, v107 row_ror:15 row_mask:0xf bank_mask:0xf
	v_cndmask_b32_e64 v191, v190, v231, s[12:13]
	v_fma_f32 v236, v139, v208, v135
	v_mov_b32_e32 v208, v107
	v_mov_b32_e32 v209, v143
	v_mov_b32_e32 v190, v131
	v_pk_mul_f32 v[190:191], v[208:209], v[190:191]
	v_mov_b32_e32 v230, v171
	v_add_f32_e32 v190, v190, v236
	v_mov_b32_e32 v233, v171
	v_add_f32_e32 v236, v190, v191
	v_mov_b32_dpp v230, v91 row_ror:1 row_mask:0xf bank_mask:0xf
	v_mov_b32_dpp v233, v75 row_ror:15 row_mask:0xf bank_mask:0xf
	v_mul_f32_e32 v190, 0xbfb8aa3b, v236
	v_exp_f32_e32 v237, v190
	v_cndmask_b32_e64 v189, v230, v189, s[14:15]
	v_cndmask_b32_e64 v191, v231, v233, s[12:13]
	v_mov_b32_e32 v208, v91
	v_mov_b32_e32 v190, v131
	v_fma_f32 v189, v139, v189, v135
	v_pk_mul_f32 v[190:191], v[208:209], v[190:191]
	v_mul_f32_e32 v227, v232, v227
	v_add_f32_e32 v189, v190, v189
	v_add_f32_e32 v189, v189, v191
	v_mul_f32_e32 v190, 0xbfb8aa3b, v189
	v_exp_f32_e32 v190, v190
	v_mov_b32_e32 v232, v171
	v_add_f32_e32 v191, 1.0, v237
	v_rcp_f32_e32 v231, v191
	v_mov_b32_dpp v232, v75 row_ror:1 row_mask:0xf bank_mask:0xf
	v_add_f32_e32 v237, 1.0, v190
	v_cndmask_b32_e64 v190, v232, v230, s[14:15]
	v_cndmask_b32_e64 v191, v233, v235, s[12:13]
	v_fma_f32 v230, v139, v190, v135
	v_mov_b32_e32 v208, v75
	v_mov_b32_e32 v190, v131
	v_pk_mul_f32 v[190:191], v[208:209], v[190:191]
	v_mov_b32_e32 v208, v143
	v_add_f32_e32 v190, v190, v230
	v_add_f32_e32 v230, v190, v191
	v_mul_f32_e32 v190, 0xbfb8aa3b, v230
	v_cndmask_b32_e64 v191, v234, v232, s[14:15]
	v_exp_f32_e32 v233, v190
	v_cndmask_b32_e64 v190, v235, 0, s[12:13]
	v_fma_f32 v232, v139, v191, v135
	v_mov_b32_e32 v209, v67
	v_mov_b32_e32 v191, v131
	v_pk_mul_f32 v[190:191], v[208:209], v[190:191]
	v_rcp_f32_e32 v208, v237
	v_add_f32_e32 v191, v191, v232
	v_add_f32_e32 v190, v190, v191
	v_mul_f32_e32 v191, 0xbfb8aa3b, v190
	v_exp_f32_e32 v191, v191
	v_add_f32_e32 v209, 1.0, v233
	v_rcp_f32_e32 v209, v209
	v_mul_f32_e32 v232, v189, v208
	v_add_f32_e32 v191, 1.0, v191
	v_rcp_f32_e32 v191, v191
	v_mov_b32_e32 v189, v171
	v_mov_b32_e32 v235, v171
	v_mul_f32_e32 v230, v230, v209
	v_mul_f32_e32 v233, v190, v191
	v_mov_b32_dpp v189, v108 row_ror:1 row_mask:0xf bank_mask:0xf
	v_mov_b32_e32 v190, v171
	v_mov_b32_dpp v235, v92 row_ror:15 row_mask:0xf bank_mask:0xf
	v_cndmask_b32_e64 v208, v189, 0, s[14:15]
	v_mov_b32_dpp v190, v108 row_ror:15 row_mask:0xf bank_mask:0xf
	v_cndmask_b32_e64 v191, v190, v235, s[12:13]
	v_fma_f32 v240, v140, v208, v136
	v_mov_b32_e32 v208, v108
	v_mov_b32_e32 v209, v144
	v_mov_b32_e32 v190, v132
	v_pk_mul_f32 v[190:191], v[208:209], v[190:191]
	v_mov_b32_e32 v234, v171
	v_add_f32_e32 v190, v190, v240
	v_mov_b32_e32 v237, v171
	v_add_f32_e32 v240, v190, v191
	v_mov_b32_dpp v234, v92 row_ror:1 row_mask:0xf bank_mask:0xf
	v_mov_b32_dpp v237, v76 row_ror:15 row_mask:0xf bank_mask:0xf
	v_mul_f32_e32 v190, 0xbfb8aa3b, v240
	v_exp_f32_e32 v241, v190
	v_cndmask_b32_e64 v189, v234, v189, s[14:15]
	v_cndmask_b32_e64 v191, v235, v237, s[12:13]
	v_mov_b32_e32 v208, v92
	v_mov_b32_e32 v190, v132
	v_fma_f32 v189, v140, v189, v136
	v_pk_mul_f32 v[190:191], v[208:209], v[190:191]
	v_mul_f32_e32 v231, v236, v231
	v_add_f32_e32 v189, v190, v189
	v_add_f32_e32 v189, v189, v191
	v_mul_f32_e32 v190, 0xbfb8aa3b, v189
	v_exp_f32_e32 v190, v190
	v_mov_b32_e32 v236, v171
	v_add_f32_e32 v191, 1.0, v241
	v_rcp_f32_e32 v235, v191
	v_mov_b32_dpp v236, v76 row_ror:1 row_mask:0xf bank_mask:0xf
	v_add_f32_e32 v241, 1.0, v190
	v_cndmask_b32_e64 v190, v236, v234, s[14:15]
	v_cndmask_b32_e64 v191, v237, v239, s[12:13]
	v_fma_f32 v234, v140, v190, v136
	v_mov_b32_e32 v208, v76
	v_mov_b32_e32 v190, v132
	v_pk_mul_f32 v[190:191], v[208:209], v[190:191]
	v_mov_b32_e32 v208, v144
	v_add_f32_e32 v190, v190, v234
	v_add_f32_e32 v234, v190, v191
	v_mul_f32_e32 v190, 0xbfb8aa3b, v234
	v_cndmask_b32_e64 v191, v238, v236, s[14:15]
	v_exp_f32_e32 v237, v190
	v_cndmask_b32_e64 v190, v239, 0, s[12:13]
	v_fma_f32 v236, v140, v191, v136
	v_mov_b32_e32 v209, v68
	v_mov_b32_e32 v191, v132
	v_pk_mul_f32 v[190:191], v[208:209], v[190:191]
	v_rcp_f32_e32 v208, v241
	v_add_f32_e32 v191, v191, v236
	v_add_f32_e32 v190, v190, v191
	v_mul_f32_e32 v191, 0xbfb8aa3b, v190
	v_exp_f32_e32 v191, v191
	v_add_f32_e32 v209, 1.0, v237
	v_rcp_f32_e32 v209, v209
	v_mul_f32_e32 v236, v189, v208
	v_add_f32_e32 v191, 1.0, v191
	v_rcp_f32_e32 v191, v191
	v_mov_b32_e32 v189, v171
	v_mov_b32_e32 v239, v171
	v_mul_f32_e32 v234, v234, v209
	v_mul_f32_e32 v237, v190, v191
	v_mov_b32_dpp v189, v109 row_ror:1 row_mask:0xf bank_mask:0xf
	v_mov_b32_e32 v190, v171
	v_mov_b32_dpp v239, v93 row_ror:15 row_mask:0xf bank_mask:0xf
	v_cndmask_b32_e64 v208, v189, 0, s[14:15]
	v_mov_b32_dpp v190, v109 row_ror:15 row_mask:0xf bank_mask:0xf
	v_cndmask_b32_e64 v191, v190, v239, s[12:13]
	v_fma_f32 v244, v141, v208, v137
	v_mov_b32_e32 v208, v109
	v_mov_b32_e32 v209, v145
	v_mov_b32_e32 v190, v133
	v_pk_mul_f32 v[190:191], v[208:209], v[190:191]
	v_mov_b32_e32 v238, v171
	v_add_f32_e32 v190, v190, v244
	v_mov_b32_e32 v241, v171
	v_add_f32_e32 v244, v190, v191
	v_mov_b32_dpp v238, v93 row_ror:1 row_mask:0xf bank_mask:0xf
	v_mov_b32_dpp v241, v77 row_ror:15 row_mask:0xf bank_mask:0xf
	v_mul_f32_e32 v190, 0xbfb8aa3b, v244
	v_exp_f32_e32 v245, v190
	v_cndmask_b32_e64 v189, v238, v189, s[14:15]
	v_cndmask_b32_e64 v191, v239, v241, s[12:13]
	v_mov_b32_e32 v208, v93
	v_mov_b32_e32 v190, v133
	v_fma_f32 v189, v141, v189, v137
	v_pk_mul_f32 v[190:191], v[208:209], v[190:191]
	v_mul_f32_e32 v235, v240, v235
	v_add_f32_e32 v189, v190, v189
	v_add_f32_e32 v189, v189, v191
	v_mul_f32_e32 v190, 0xbfb8aa3b, v189
; __device__ __forceinline__ unsigned cvt_pk_bf16(float lo, float hi) { unsigned r; asm volatile("v_cvt_pk_bf16_f32 %0, %1, %2" : "=v"(r) : "v"(lo), "v"(hi)); return r; }
; __device__ __forceinline__ float siluf(float x) { return x * __builtin_amdgcn_rcpf(1.f + __expf(-x)); }
; __device__ __forceinline__ float dpp_ror1(float v) { return __builtin_bit_cast(float, __builtin_amdgcn_update_dpp(0, __builtin_bit_cast(int, v), 0x121, 0xf, 0xf, false)); }
; __device__ __forceinline__ float dpp_ror15(float v) { return __builtin_bit_cast(float, __builtin_amdgcn_update_dpp(0, __builtin_bit_cast(int, v), 0x12F, 0xf, 0xf, false)); }
;     __device__ __forceinline__ void operator()(const f32x4 (&acc)[2][2][4][2], const pg8::Unit& u, int wr, int wc, int fr, int fq_in) const {
;     ...
;                     for (int n = 0; n < 2; ++n) { w0[n] = *(const f32x4*)(cw + col + 4 * n); w1[n] = *(const f32x4*)(cw + XBCW + col + 4 * n); w2[n] = *(const f32x4*)(cw + 2 * XBCW + col + 4 * n); bb[n] = *(const f32x4*)(cb + col + 4 * n); }
; #pragma unroll
;                     for (int ai = 0; ai < 2; ++ai) {
;                         f32x4 o[4][2];
; #pragma unroll
;                         for (int n = 0; n < 2; ++n)
; #pragma unroll
;                             for (int q = 0; q < 4; ++q) { float A[4], B[4];
; #pragma unroll
;                                 for (int m = 0; m < 4; ++m) { A[m] = dpp_ror1(acc[ai][bj][m][n][q]); B[m] = dpp_ror15(acc[ai][bj][m][n][q]); }
; #pragma unroll
;                                 for (int m = 0; m < 4; ++m) { const float pv = fr > 0 ? A[m] : (m > 0 ? A[m > 0 ? m - 1 : 0] : 0.f), nv = fr < 15 ? B[m] : (m < 3 ? B[m < 3 ? m + 1 : 3] : 0.f);
;                                     o[m][n][q] = siluf(bb[n][q] + w0[n][q] * pv + w1[n][q] * acc[ai][bj][m][n][q] + w2[n][q] * nv); } }
; #pragma unroll
;                         for (int m = 0; m < 4; ++m) { u32x4 w; w.x = pg8::cvt_pk_bf16(o[m][0][0], o[m][0][1]); w.y = pg8::cvt_pk_bf16(o[m][0][2], o[m][0][3]); w.z = pg8::cvt_pk_bf16(o[m][1][0], o[m][1][1]); w.w = pg8::cvt_pk_bf16(o[m][1][2], o[m][1][3]);
;                             *(u32x4*)(XBC + (size_t)(row0 + ai * 128 + m * 16) * XBCW + col) = w; }
	v_exp_f32_e32 v190, v190
	v_mov_b32_e32 v240, v171
	v_add_f32_e32 v191, 1.0, v245
	v_rcp_f32_e32 v239, v191
	v_mov_b32_dpp v240, v77 row_ror:1 row_mask:0xf bank_mask:0xf
	v_add_f32_e32 v245, 1.0, v190
	v_cndmask_b32_e64 v190, v240, v238, s[14:15]
	v_cndmask_b32_e64 v191, v241, v243, s[12:13]
	v_fma_f32 v238, v141, v190, v137
	v_mov_b32_e32 v208, v77
	v_mov_b32_e32 v190, v133
	v_pk_mul_f32 v[190:191], v[208:209], v[190:191]
	v_mov_b32_e32 v208, v145
	v_add_f32_e32 v190, v190, v238
	v_add_f32_e32 v238, v190, v191
	v_mul_f32_e32 v190, 0xbfb8aa3b, v238
	v_cndmask_b32_e64 v191, v242, v240, s[14:15]
	v_exp_f32_e32 v241, v190
	v_cndmask_b32_e64 v190, v243, 0, s[12:13]
	v_fma_f32 v240, v141, v191, v137
	v_mov_b32_e32 v209, v69
	v_mov_b32_e32 v191, v133
	v_pk_mul_f32 v[190:191], v[208:209], v[190:191]
	v_add_f32_e32 v209, 1.0, v241
	v_add_f32_e32 v191, v191, v240
	v_add_f32_e32 v190, v190, v191
	v_mul_f32_e32 v191, 0xbfb8aa3b, v190
	v_exp_f32_e32 v191, v191
	v_rcp_f32_e32 v208, v245
	v_rcp_f32_e32 v209, v209
	v_mul_f32_e32 v239, v244, v239
	v_add_f32_e32 v191, 1.0, v191
	v_rcp_f32_e32 v191, v191
	v_mul_f32_e32 v208, v189, v208
	v_mul_f32_e32 v209, v238, v209
	v_cvt_pk_bf16_f32 v188, v182, v188
	v_mul_f32_e32 v238, v190, v191
	v_cvt_pk_bf16_f32 v189, v219, v223
	v_cvt_pk_bf16_f32 v190, v227, v231
	v_cvt_pk_bf16_f32 v191, v235, v239
	global_store_dwordx4 v[192:193], v[188:191], off offset:256 nt
	v_mov_b32_e32 v192, v171
	s_nop 0
	v_cvt_pk_bf16_f32 v188, v179, v185
	v_cvt_pk_bf16_f32 v189, v220, v224
	v_cvt_pk_bf16_f32 v190, v228, v232
	v_cvt_pk_bf16_f32 v191, v236, v208
	global_store_dwordx4 v[194:195], v[188:191], off offset:256 nt
	v_mov_b32_e32 v179, v171
	v_mov_b32_dpp v192, v6 row_ror:15 row_mask:0xf bank_mask:0xf
	v_cvt_pk_bf16_f32 v188, v177, v184
	v_cvt_pk_bf16_f32 v189, v218, v222
	v_cvt_pk_bf16_f32 v190, v226, v230
	v_cvt_pk_bf16_f32 v191, v234, v209
	global_store_dwordx4 v[196:197], v[188:191], off offset:256 nt
	v_cvt_pk_bf16_f32 v182, v170, v183
	v_mov_b32_e32 v170, v171
	v_mov_b32_e32 v177, v171
	v_mov_b32_e32 v188, v171
	v_mov_b32_dpp v170, v50 row_ror:1 row_mask:0xf bank_mask:0xf
	v_cvt_pk_bf16_f32 v183, v221, v225
	v_cvt_pk_bf16_f32 v184, v229, v233
	v_cvt_pk_bf16_f32 v185, v237, v238
	global_store_dwordx4 v[198:199], v[182:185], off offset:256 nt
	v_mov_b32_dpp v177, v50 row_ror:15 row_mask:0xf bank_mask:0xf
	v_mov_b32_dpp v188, v34 row_ror:15 row_mask:0xf bank_mask:0xf
	v_cndmask_b32_e64 v182, v170, 0, s[14:15]
	v_cndmask_b32_e64 v183, v177, v188, s[12:13]
	v_fma_f32 v177, v146, v182, v150
	v_mov_b32_e32 v184, v50
	v_mov_b32_e32 v185, v158
	v_mov_b32_e32 v182, v154
	v_pk_mul_f32 v[182:183], v[184:185], v[182:183]
	v_mov_b32_e32 v190, v171
	v_add_f32_e32 v177, v182, v177
	v_add_f32_e32 v177, v177, v183
	v_mov_b32_dpp v179, v34 row_ror:1 row_mask:0xf bank_mask:0xf
	v_mov_b32_dpp v190, v18 row_ror:15 row_mask:0xf bank_mask:0xf
	v_mul_f32_e32 v182, 0xbfb8aa3b, v177
	v_exp_f32_e32 v193, v182
	v_cndmask_b32_e64 v170, v179, v170, s[14:15]
	v_cndmask_b32_e64 v183, v188, v190, s[12:13]
	v_mov_b32_e32 v184, v34
	v_mov_b32_e32 v182, v154
	v_fma_f32 v170, v146, v170, v150
	v_pk_mul_f32 v[182:183], v[184:185], v[182:183]
	v_mov_b32_e32 v189, v171
	v_add_f32_e32 v170, v182, v170
	v_add_f32_e32 v170, v170, v183
	v_mul_f32_e32 v182, 0xbfb8aa3b, v170
	v_exp_f32_e32 v182, v182
	v_mov_b32_dpp v189, v18 row_ror:1 row_mask:0xf bank_mask:0xf
	v_add_f32_e32 v183, 1.0, v193
	v_rcp_f32_e32 v188, v183
	v_add_f32_e32 v193, 1.0, v182
	v_cndmask_b32_e64 v179, v189, v179, s[14:15]
	v_cndmask_b32_e64 v183, v190, v192, s[12:13]
	v_mov_b32_e32 v184, v18
	v_mov_b32_e32 v182, v154
	v_fma_f32 v179, v146, v179, v150
	v_pk_mul_f32 v[182:183], v[184:185], v[182:183]
	v_mov_b32_e32 v191, v171
	v_add_f32_e32 v179, v182, v179
	v_add_f32_e32 v179, v179, v183
	v_mov_b32_dpp v191, v6 row_ror:1 row_mask:0xf bank_mask:0xf
	v_mul_f32_e32 v182, 0xbfb8aa3b, v179
	v_cndmask_b32_e64 v183, v191, v189, s[14:15]
	v_exp_f32_e32 v190, v182
	v_cndmask_b32_e64 v182, v192, 0, s[12:13]
	v_fma_f32 v146, v146, v183, v150
	v_mov_b32_e32 v184, v158
	v_mov_b32_e32 v185, v6
	v_mov_b32_e32 v183, v154
	v_pk_mul_f32 v[182:183], v[184:185], v[182:183]
	v_rcp_f32_e32 v154, v193
	v_add_f32_e32 v146, v183, v146
	v_add_f32_e32 v146, v182, v146
	v_mul_f32_e32 v150, 0xbfb8aa3b, v146
	v_exp_f32_e32 v150, v150
	v_add_f32_e32 v158, 1.0, v190
	v_rcp_f32_e32 v158, v158
	v_mul_f32_e32 v170, v170, v154
	v_add_f32_e32 v150, 1.0, v150
	v_rcp_f32_e32 v182, v150
	v_mov_b32_e32 v154, v171
	v_mul_f32_e32 v150, v179, v158
	v_mov_b32_e32 v158, v171
	v_mov_b32_dpp v154, v51 row_ror:1 row_mask:0xf bank_mask:0xf
	v_mov_b32_e32 v184, v171
	v_mul_f32_e32 v146, v146, v182
	v_mov_b32_dpp v158, v51 row_ror:15 row_mask:0xf bank_mask:0xf
	v_mov_b32_dpp v184, v35 row_ror:15 row_mask:0xf bank_mask:0xf
	v_cndmask_b32_e64 v182, v154, 0, s[14:15]
	v_cndmask_b32_e64 v183, v158, v184, s[12:13]
	v_fma_f32 v191, v147, v182, v151
	v_mov_b32_e32 v158, v51
	v_mov_b32_e32 v182, v155
	v_pk_mul_f32 v[182:183], v[158:159], v[182:183]
	v_mul_f32_e32 v177, v177, v188
	v_add_f32_e32 v158, v182, v191
	v_mov_b32_e32 v179, v171
	v_mov_b32_e32 v188, v171
	v_add_f32_e32 v191, v158, v183
	v_mov_b32_dpp v179, v35 row_ror:1 row_mask:0xf bank_mask:0xf
	v_mov_b32_dpp v188, v19 row_ror:15 row_mask:0xf bank_mask:0xf
	v_mul_f32_e32 v158, 0xbfb8aa3b, v191
	v_exp_f32_e32 v192, v158
	v_cndmask_b32_e64 v154, v179, v154, s[14:15]
	v_cndmask_b32_e64 v183, v184, v188, s[12:13]
	v_mov_b32_e32 v158, v35
	v_mov_b32_e32 v182, v155
	v_fma_f32 v154, v147, v154, v151
	v_pk_mul_f32 v[182:183], v[158:159], v[182:183]
	v_mov_b32_e32 v185, v171
	v_add_f32_e32 v154, v182, v154
; __device__ __forceinline__ float siluf(float x) { return x * __builtin_amdgcn_rcpf(1.f + __expf(-x)); }
; __device__ __forceinline__ float dpp_ror1(float v) { return __builtin_bit_cast(float, __builtin_amdgcn_update_dpp(0, __builtin_bit_cast(int, v), 0x121, 0xf, 0xf, false)); }
; __device__ __forceinline__ float dpp_ror15(float v) { return __builtin_bit_cast(float, __builtin_amdgcn_update_dpp(0, __builtin_bit_cast(int, v), 0x12F, 0xf, 0xf, false)); }
;     __device__ __forceinline__ void operator()(const f32x4 (&acc)[2][2][4][2], const pg8::Unit& u, int wr, int wc, int fr, int fq_in) const {
;     ...
;                     for (int n = 0; n < 2; ++n) { w0[n] = *(const f32x4*)(cw + col + 4 * n); w1[n] = *(const f32x4*)(cw + XBCW + col + 4 * n); w2[n] = *(const f32x4*)(cw + 2 * XBCW + col + 4 * n); bb[n] = *(const f32x4*)(cb + col + 4 * n); }
; #pragma unroll
;                     for (int ai = 0; ai < 2; ++ai) {
;                         f32x4 o[4][2];
; #pragma unroll
;                         for (int n = 0; n < 2; ++n)
; #pragma unroll
;                             for (int q = 0; q < 4; ++q) { float A[4], B[4];
; #pragma unroll
;                                 for (int m = 0; m < 4; ++m) { A[m] = dpp_ror1(acc[ai][bj][m][n][q]); B[m] = dpp_ror15(acc[ai][bj][m][n][q]); }
; #pragma unroll
;                                 for (int m = 0; m < 4; ++m) { const float pv = fr > 0 ? A[m] : (m > 0 ? A[m > 0 ? m - 1 : 0] : 0.f), nv = fr < 15 ? B[m] : (m < 3 ? B[m < 3 ? m + 1 : 3] : 0.f);
;                                     o[m][n][q] = siluf(bb[n][q] + w0[n][q] * pv + w1[n][q] * acc[ai][bj][m][n][q] + w2[n][q] * nv); } }
	v_add_f32_e32 v184, v154, v183
	v_mul_f32_e32 v154, 0xbfb8aa3b, v184
	v_exp_f32_e32 v154, v154
	v_mov_b32_e32 v190, v171
	v_mov_b32_dpp v185, v19 row_ror:1 row_mask:0xf bank_mask:0xf
	v_add_f32_e32 v158, 1.0, v192
	v_mov_b32_dpp v190, v7 row_ror:15 row_mask:0xf bank_mask:0xf
	v_rcp_f32_e32 v192, v158
	v_add_f32_e32 v193, 1.0, v154
	v_cndmask_b32_e64 v154, v185, v179, s[14:15]
	v_cndmask_b32_e64 v183, v188, v190, s[12:13]
	v_mov_b32_e32 v158, v19
	v_mov_b32_e32 v182, v155
	v_fma_f32 v154, v147, v154, v151
	v_pk_mul_f32 v[182:183], v[158:159], v[182:183]
	v_mov_b32_e32 v189, v171
	v_add_f32_e32 v154, v182, v154
	v_add_f32_e32 v179, v154, v183
	v_mov_b32_dpp v189, v7 row_ror:1 row_mask:0xf bank_mask:0xf
	v_mul_f32_e32 v154, 0xbfb8aa3b, v179
	v_cndmask_b32_e64 v158, v189, v185, s[14:15]
	v_exp_f32_e32 v182, v154
	v_cndmask_b32_e64 v154, v190, 0, s[12:13]
	v_fma_f32 v147, v147, v158, v151
	v_mov_b32_e32 v158, v159
	v_mov_b32_e32 v159, v7
	v_pk_mul_f32 v[154:155], v[158:159], v[154:155]
	v_mov_b32_e32 v185, v171
	v_add_f32_e32 v147, v155, v147
	v_add_f32_e32 v147, v154, v147
	v_mul_f32_e32 v151, 0xbfb8aa3b, v147
	v_exp_f32_e32 v151, v151
	v_add_f32_e32 v155, 1.0, v182
	v_rcp_f32_e32 v158, v155
	v_rcp_f32_e32 v154, v193
	v_add_f32_e32 v151, 1.0, v151
	v_rcp_f32_e32 v159, v151
	v_mul_f32_e32 v151, v179, v158
	v_mov_b32_e32 v179, v171
	v_mov_b32_e32 v158, v171
	v_mov_b32_dpp v185, v36 row_ror:15 row_mask:0xf bank_mask:0xf
	v_mov_b32_dpp v179, v52 row_ror:1 row_mask:0xf bank_mask:0xf
	v_mov_b32_dpp v158, v52 row_ror:15 row_mask:0xf bank_mask:0xf
	v_cndmask_b32_e64 v182, v179, 0, s[14:15]
	v_mul_f32_e32 v155, v191, v192
	v_mul_f32_e32 v147, v147, v159
	v_cndmask_b32_e64 v159, v158, v185, s[12:13]
	v_fma_f32 v192, v148, v182, v152
	v_mov_b32_e32 v182, v52
	v_mov_b32_e32 v183, v160
	v_mov_b32_e32 v158, v156
	v_pk_mul_f32 v[158:159], v[182:183], v[158:159]
	v_mul_f32_e32 v154, v184, v154
	v_add_f32_e32 v158, v158, v192
	v_mov_b32_e32 v184, v171
	v_add_f32_e32 v192, v158, v159
	v_mov_b32_e32 v189, v171
	v_mov_b32_dpp v184, v36 row_ror:1 row_mask:0xf bank_mask:0xf
	v_mul_f32_e32 v158, 0xbfb8aa3b, v192
	v_mov_b32_dpp v189, v20 row_ror:15 row_mask:0xf bank_mask:0xf
	v_exp_f32_e32 v193, v158
	v_cndmask_b32_e64 v158, v184, v179, s[14:15]
	v_cndmask_b32_e64 v159, v185, v189, s[12:13]
	v_fma_f32 v179, v148, v158, v152
	v_mov_b32_e32 v182, v36
	v_mov_b32_e32 v158, v156
	v_pk_mul_f32 v[158:159], v[182:183], v[158:159]
	v_mov_b32_e32 v188, v171
	v_add_f32_e32 v158, v158, v179
	v_add_f32_e32 v179, v158, v159
	v_mul_f32_e32 v158, 0xbfb8aa3b, v179
	v_exp_f32_e32 v158, v158
	v_mov_b32_dpp v188, v20 row_ror:1 row_mask:0xf bank_mask:0xf
	v_mov_b32_e32 v191, v171
	v_add_f32_e32 v159, 1.0, v193
	v_add_f32_e32 v193, 1.0, v158
	v_mov_b32_dpp v191, v8 row_ror:15 row_mask:0xf bank_mask:0xf
	v_cndmask_b32_e64 v158, v188, v184, s[14:15]
	v_rcp_f32_e32 v185, v159
	v_cndmask_b32_e64 v159, v189, v191, s[12:13]
	v_fma_f32 v184, v148, v158, v152
	v_mov_b32_e32 v182, v20
	v_mov_b32_e32 v158, v156
	v_pk_mul_f32 v[158:159], v[182:183], v[158:159]
	v_mov_b32_e32 v190, v171
	v_add_f32_e32 v158, v158, v184
	v_add_f32_e32 v184, v158, v159
	v_mov_b32_dpp v190, v8 row_ror:1 row_mask:0xf bank_mask:0xf
	v_mul_f32_e32 v158, 0xbfb8aa3b, v184
	v_cndmask_b32_e64 v159, v190, v188, s[14:15]
	v_exp_f32_e32 v189, v158
	v_cndmask_b32_e64 v158, v191, 0, s[12:13]
	v_fma_f32 v148, v148, v159, v152
	v_mov_b32_e32 v182, v160
	v_mov_b32_e32 v183, v8
	v_mov_b32_e32 v159, v156
	v_pk_mul_f32 v[158:159], v[182:183], v[158:159]
	v_mul_f32_e32 v182, v192, v185
	v_add_f32_e32 v148, v159, v148
	v_add_f32_e32 v148, v158, v148
	v_mul_f32_e32 v152, 0xbfb8aa3b, v148
	v_exp_f32_e32 v152, v152
	v_add_f32_e32 v158, 1.0, v189
	v_rcp_f32_e32 v158, v158
	v_mov_b32_e32 v185, v171
	v_add_f32_e32 v152, 1.0, v152
	v_rcp_f32_e32 v152, v152
	v_mul_f32_e32 v183, v184, v158
	v_rcp_f32_e32 v156, v193
	v_mov_b32_dpp v185, v37 row_ror:15 row_mask:0xf bank_mask:0xf
	v_mul_f32_e32 v184, v148, v152
	v_mov_b32_e32 v148, v171
	v_mov_b32_e32 v152, v171
	v_mov_b32_e32 v160, v53
	v_mov_b32_dpp v148, v53 row_ror:1 row_mask:0xf bank_mask:0xf
	v_mov_b32_dpp v152, v53 row_ror:15 row_mask:0xf bank_mask:0xf
	v_cndmask_b32_e64 v158, v148, 0, s[14:15]
	v_cndmask_b32_e64 v159, v152, v185, s[12:13]
	v_fma_f32 v152, v149, v158, v153
	v_mov_b32_e32 v158, v157
	v_pk_mul_f32 v[158:159], v[160:161], v[158:159]
	v_mul_f32_e32 v179, v179, v156
	v_add_f32_e32 v152, v158, v152
	v_mov_b32_e32 v156, v171
	v_mov_b32_e32 v189, v171
	v_add_f32_e32 v152, v152, v159
	v_mov_b32_dpp v156, v37 row_ror:1 row_mask:0xf bank_mask:0xf
	v_mov_b32_dpp v189, v21 row_ror:15 row_mask:0xf bank_mask:0xf
	v_mul_f32_e32 v158, 0xbfb8aa3b, v152
	v_exp_f32_e32 v192, v158
	v_cndmask_b32_e64 v148, v156, v148, s[14:15]
	v_cndmask_b32_e64 v159, v185, v189, s[12:13]
	v_mov_b32_e32 v160, v37
	v_mov_b32_e32 v158, v157
	v_fma_f32 v148, v149, v148, v153
	v_pk_mul_f32 v[158:159], v[160:161], v[158:159]
	v_mov_b32_e32 v188, v171
	v_add_f32_e32 v148, v158, v148
	v_add_f32_e32 v185, v148, v159
	v_mul_f32_e32 v148, 0xbfb8aa3b, v185
	v_exp_f32_e32 v148, v148
	v_mov_b32_e32 v191, v171
	v_mov_b32_dpp v188, v21 row_ror:1 row_mask:0xf bank_mask:0xf
	v_add_f32_e32 v158, 1.0, v192
	v_mov_b32_dpp v191, v9 row_ror:15 row_mask:0xf bank_mask:0xf
	v_rcp_f32_e32 v192, v158
	v_add_f32_e32 v193, 1.0, v148
	v_cndmask_b32_e64 v148, v188, v156, s[14:15]
	v_cndmask_b32_e64 v159, v189, v191, s[12:13]
	v_mov_b32_e32 v160, v21
	v_mov_b32_e32 v158, v157
	v_fma_f32 v148, v149, v148, v153
	v_pk_mul_f32 v[158:159], v[160:161], v[158:159]
	v_mov_b32_e32 v190, v171
	v_add_f32_e32 v148, v158, v148
	v_add_f32_e32 v158, v148, v159
; __device__ __forceinline__ float siluf(float x) { return x * __builtin_amdgcn_rcpf(1.f + __expf(-x)); }
; __device__ __forceinline__ float dpp_ror1(float v) { return __builtin_bit_cast(float, __builtin_amdgcn_update_dpp(0, __builtin_bit_cast(int, v), 0x121, 0xf, 0xf, false)); }
; __device__ __forceinline__ float dpp_ror15(float v) { return __builtin_bit_cast(float, __builtin_amdgcn_update_dpp(0, __builtin_bit_cast(int, v), 0x12F, 0xf, 0xf, false)); }
;     __device__ __forceinline__ void operator()(const f32x4 (&acc)[2][2][4][2], const pg8::Unit& u, int wr, int wc, int fr, int fq_in) const {
;     ...
;                     for (int n = 0; n < 2; ++n) { w0[n] = *(const f32x4*)(cw + col + 4 * n); w1[n] = *(const f32x4*)(cw + XBCW + col + 4 * n); w2[n] = *(const f32x4*)(cw + 2 * XBCW + col + 4 * n); bb[n] = *(const f32x4*)(cb + col + 4 * n); }
; #pragma unroll
;                     for (int ai = 0; ai < 2; ++ai) {
;                         f32x4 o[4][2];
; #pragma unroll
;                         for (int n = 0; n < 2; ++n)
; #pragma unroll
;                             for (int q = 0; q < 4; ++q) { float A[4], B[4];
; #pragma unroll
;                                 for (int m = 0; m < 4; ++m) { A[m] = dpp_ror1(acc[ai][bj][m][n][q]); B[m] = dpp_ror15(acc[ai][bj][m][n][q]); }
; #pragma unroll
;                                 for (int m = 0; m < 4; ++m) { const float pv = fr > 0 ? A[m] : (m > 0 ? A[m > 0 ? m - 1 : 0] : 0.f), nv = fr < 15 ? B[m] : (m < 3 ? B[m < 3 ? m + 1 : 3] : 0.f);
;                                     o[m][n][q] = siluf(bb[n][q] + w0[n][q] * pv + w1[n][q] * acc[ai][bj][m][n][q] + w2[n][q] * nv); } }
	v_mov_b32_dpp v190, v9 row_ror:1 row_mask:0xf bank_mask:0xf
	v_mul_f32_e32 v148, 0xbfb8aa3b, v158
	v_exp_f32_e32 v159, v148
	v_cndmask_b32_e64 v148, v190, v188, s[14:15]
	v_cndmask_b32_e64 v156, v191, 0, s[12:13]
	v_fmac_f32_e32 v153, v149, v148
	v_mov_b32_e32 v148, v161
	v_mov_b32_e32 v149, v9
	v_pk_mul_f32 v[148:149], v[148:149], v[156:157]
	v_add_f32_e32 v156, 1.0, v159
	v_add_f32_e32 v149, v149, v153
	v_add_f32_e32 v148, v148, v149
	v_mul_f32_e32 v149, 0xbfb8aa3b, v148
	v_exp_f32_e32 v149, v149
	v_rcp_f32_e32 v153, v193
	v_rcp_f32_e32 v156, v156
	v_mov_b32_e32 v160, v171
	v_add_f32_e32 v149, 1.0, v149
	v_rcp_f32_e32 v149, v149
	v_mul_f32_e32 v159, v185, v153
	v_mul_f32_e32 v156, v158, v156
	v_mov_b32_dpp v160, v42 row_ror:1 row_mask:0xf bank_mask:0xf
	v_mul_f32_e32 v158, v148, v149
	v_mov_b32_e32 v148, v171
	v_mov_b32_e32 v185, v171
	v_mul_f32_e32 v157, v152, v192
	v_mov_b32_dpp v148, v42 row_ror:15 row_mask:0xf bank_mask:0xf
	v_mov_b32_dpp v185, v26 row_ror:15 row_mask:0xf bank_mask:0xf
	v_cndmask_b32_e64 v152, v160, 0, s[14:15]
	v_cndmask_b32_e64 v149, v148, v185, s[12:13]
	v_fma_f32 v192, v138, v152, v134
	v_mov_b32_e32 v152, v42
	v_mov_b32_e32 v153, v142
	v_mov_b32_e32 v148, v130
	v_pk_mul_f32 v[148:149], v[152:153], v[148:149]
	v_mov_b32_e32 v161, v171
	v_add_f32_e32 v148, v148, v192
	v_add_f32_e32 v192, v148, v149
	v_mov_b32_dpp v161, v26 row_ror:1 row_mask:0xf bank_mask:0xf
	v_mov_b32_e32 v189, v171
	v_mul_f32_e32 v148, 0xbfb8aa3b, v192
	v_exp_f32_e32 v193, v148
	v_mov_b32_dpp v189, v10 row_ror:15 row_mask:0xf bank_mask:0xf
	v_cndmask_b32_e64 v148, v161, v160, s[14:15]
	v_cndmask_b32_e64 v149, v185, v189, s[12:13]
	v_fma_f32 v160, v138, v148, v134
	v_mov_b32_e32 v152, v26
	v_mov_b32_e32 v148, v130
	v_pk_mul_f32 v[148:149], v[152:153], v[148:149]
	v_mov_b32_e32 v188, v171
	v_add_f32_e32 v148, v148, v160
	v_add_f32_e32 v160, v148, v149
	v_mul_f32_e32 v148, 0xbfb8aa3b, v160
	v_exp_f32_e32 v148, v148
	v_mov_b32_dpp v188, v10 row_ror:1 row_mask:0xf bank_mask:0xf
	v_mov_b32_e32 v191, v171
	v_add_f32_e32 v149, 1.0, v193
	v_add_f32_e32 v193, 1.0, v148
	v_mov_b32_dpp v191, v2 row_ror:15 row_mask:0xf bank_mask:0xf
	v_cndmask_b32_e64 v148, v188, v161, s[14:15]
	v_rcp_f32_e32 v185, v149
	v_cndmask_b32_e64 v149, v189, v191, s[12:13]
	v_fma_f32 v161, v138, v148, v134
	v_mov_b32_e32 v152, v10
	v_mov_b32_e32 v148, v130
	v_pk_mul_f32 v[148:149], v[152:153], v[148:149]
	v_mov_b32_e32 v190, v171
	v_add_f32_e32 v148, v148, v161
	v_add_f32_e32 v161, v148, v149
	v_mov_b32_dpp v190, v2 row_ror:1 row_mask:0xf bank_mask:0xf
	v_mul_f32_e32 v148, 0xbfb8aa3b, v161
	v_cndmask_b32_e64 v149, v190, v188, s[14:15]
	v_exp_f32_e32 v189, v148
	v_cndmask_b32_e64 v148, v191, 0, s[12:13]
	v_fma_f32 v134, v138, v149, v134
	v_mov_b32_e32 v152, v142
	v_mov_b32_e32 v153, v2
	v_mov_b32_e32 v149, v130
	v_pk_mul_f32 v[148:149], v[152:153], v[148:149]
	v_rcp_f32_e32 v138, v193
	v_add_f32_e32 v130, v149, v134
	v_add_f32_e32 v130, v148, v130
	v_mul_f32_e32 v134, 0xbfb8aa3b, v130
	v_exp_f32_e32 v134, v134
	v_add_f32_e32 v142, 1.0, v189
	v_rcp_f32_e32 v142, v142
	v_mul_f32_e32 v138, v160, v138
	v_add_f32_e32 v134, 1.0, v134
	v_rcp_f32_e32 v134, v134
	v_mul_f32_e32 v152, v192, v185
	v_mov_b32_e32 v185, v171
	v_mul_f32_e32 v153, v161, v142
	v_mul_f32_e32 v160, v130, v134
	v_mov_b32_e32 v130, v171
	v_mov_b32_e32 v134, v171
	v_mov_b32_dpp v185, v27 row_ror:15 row_mask:0xf bank_mask:0xf
	v_mov_b32_dpp v130, v43 row_ror:1 row_mask:0xf bank_mask:0xf
	v_mov_b32_dpp v134, v43 row_ror:15 row_mask:0xf bank_mask:0xf
	v_cndmask_b32_e64 v142, v130, 0, s[14:15]
	v_cndmask_b32_e64 v149, v134, v185, s[12:13]
	v_fma_f32 v134, v139, v142, v135
	v_mov_b32_e32 v142, v43
	v_mov_b32_e32 v148, v131
	v_mov_b32_e32 v161, v171
	v_mov_b32_e32 v189, v171
	v_pk_mul_f32 v[148:149], v[142:143], v[148:149]
	v_mov_b32_dpp v161, v27 row_ror:1 row_mask:0xf bank_mask:0xf
	v_mov_b32_dpp v189, v11 row_ror:15 row_mask:0xf bank_mask:0xf
	v_add_f32_e32 v134, v148, v134
	v_add_f32_e32 v192, v134, v149
	v_cndmask_b32_e64 v130, v161, v130, s[14:15]
	v_cndmask_b32_e64 v149, v185, v189, s[12:13]
	v_mov_b32_e32 v142, v27
	v_mov_b32_e32 v148, v131
	v_fma_f32 v130, v139, v130, v135
	v_pk_mul_f32 v[148:149], v[142:143], v[148:149]
	v_mov_b32_e32 v188, v171
	v_add_f32_e32 v130, v148, v130
	v_add_f32_e32 v185, v130, v149
	v_mul_f32_e32 v130, 0xbfb8aa3b, v185
	v_exp_f32_e32 v130, v130
	v_mov_b32_e32 v191, v171
	v_mul_f32_e32 v134, 0xbfb8aa3b, v192
	v_mov_b32_dpp v188, v11 row_ror:1 row_mask:0xf bank_mask:0xf
	v_exp_f32_e32 v134, v134
	v_mov_b32_dpp v191, v3 row_ror:15 row_mask:0xf bank_mask:0xf
	v_add_f32_e32 v194, 1.0, v130
	v_cndmask_b32_e64 v130, v188, v161, s[14:15]
	v_cndmask_b32_e64 v149, v189, v191, s[12:13]
	v_mov_b32_e32 v142, v11
	v_mov_b32_e32 v148, v131
	v_fma_f32 v130, v139, v130, v135
	v_pk_mul_f32 v[148:149], v[142:143], v[148:149]
	v_mov_b32_e32 v190, v171
	v_add_f32_e32 v130, v148, v130
	v_add_f32_e32 v134, 1.0, v134
	v_mov_b32_dpp v190, v3 row_ror:1 row_mask:0xf bank_mask:0xf
	v_add_f32_e32 v142, v130, v149
	v_rcp_f32_e32 v193, v134
	v_mul_f32_e32 v130, 0xbfb8aa3b, v142
	v_cndmask_b32_e64 v134, v190, v188, s[14:15]
	v_exp_f32_e32 v148, v130
	v_cndmask_b32_e64 v130, v191, 0, s[12:13]
	v_fma_f32 v139, v139, v134, v135
	v_mov_b32_e32 v134, v143
	v_mov_b32_e32 v135, v3
	v_pk_mul_f32 v[130:131], v[134:135], v[130:131]
	v_rcp_f32_e32 v134, v194
	v_add_f32_e32 v131, v131, v139
	v_add_f32_e32 v130, v130, v131
	v_mul_f32_e32 v131, 0xbfb8aa3b, v130
	v_exp_f32_e32 v131, v131
	v_add_f32_e32 v135, 1.0, v148
	v_rcp_f32_e32 v135, v135
	v_mov_b32_e32 v149, v171
	v_add_f32_e32 v131, 1.0, v131
	v_rcp_f32_e32 v131, v131
; __device__ __forceinline__ unsigned cvt_pk_bf16(float lo, float hi) { unsigned r; asm volatile("v_cvt_pk_bf16_f32 %0, %1, %2" : "=v"(r) : "v"(lo), "v"(hi)); return r; }
; __device__ __forceinline__ float siluf(float x) { return x * __builtin_amdgcn_rcpf(1.f + __expf(-x)); }
; __device__ __forceinline__ float dpp_ror1(float v) { return __builtin_bit_cast(float, __builtin_amdgcn_update_dpp(0, __builtin_bit_cast(int, v), 0x121, 0xf, 0xf, false)); }
; __device__ __forceinline__ float dpp_ror15(float v) { return __builtin_bit_cast(float, __builtin_amdgcn_update_dpp(0, __builtin_bit_cast(int, v), 0x12F, 0xf, 0xf, false)); }
;     __device__ __forceinline__ void operator()(const f32x4 (&acc)[2][2][4][2], const pg8::Unit& u, int wr, int wc, int fr, int fq_in) const {
;     ...
;                     for (int n = 0; n < 2; ++n) { w0[n] = *(const f32x4*)(cw + col + 4 * n); w1[n] = *(const f32x4*)(cw + XBCW + col + 4 * n); w2[n] = *(const f32x4*)(cw + 2 * XBCW + col + 4 * n); bb[n] = *(const f32x4*)(cb + col + 4 * n); }
; #pragma unroll
;                     for (int ai = 0; ai < 2; ++ai) {
;                         f32x4 o[4][2];
; #pragma unroll
;                         for (int n = 0; n < 2; ++n)
; #pragma unroll
;                             for (int q = 0; q < 4; ++q) { float A[4], B[4];
; #pragma unroll
;                                 for (int m = 0; m < 4; ++m) { A[m] = dpp_ror1(acc[ai][bj][m][n][q]); B[m] = dpp_ror15(acc[ai][bj][m][n][q]); }
; #pragma unroll
;                                 for (int m = 0; m < 4; ++m) { const float pv = fr > 0 ? A[m] : (m > 0 ? A[m > 0 ? m - 1 : 0] : 0.f), nv = fr < 15 ? B[m] : (m < 3 ? B[m < 3 ? m + 1 : 3] : 0.f);
;                                     o[m][n][q] = siluf(bb[n][q] + w0[n][q] * pv + w1[n][q] * acc[ai][bj][m][n][q] + w2[n][q] * nv); } }
; #pragma unroll
;                         for (int m = 0; m < 4; ++m) { u32x4 w; w.x = pg8::cvt_pk_bf16(o[m][0][0], o[m][0][1]); w.y = pg8::cvt_pk_bf16(o[m][0][2], o[m][0][3]); w.z = pg8::cvt_pk_bf16(o[m][1][0], o[m][1][1]); w.w = pg8::cvt_pk_bf16(o[m][1][2], o[m][1][3]);
;                             *(u32x4*)(XBC + (size_t)(row0 + ai * 128 + m * 16) * XBCW + col) = w; }
	v_mul_f32_e32 v143, v185, v134
	v_mov_b32_dpp v149, v44 row_ror:1 row_mask:0xf bank_mask:0xf
	v_mov_b32_e32 v185, v171
	v_mul_f32_e32 v148, v130, v131
	v_mov_b32_e32 v130, v171
	v_mov_b32_dpp v185, v28 row_ror:15 row_mask:0xf bank_mask:0xf
	v_cndmask_b32_e64 v134, v149, 0, s[14:15]
	v_mov_b32_dpp v130, v44 row_ror:15 row_mask:0xf bank_mask:0xf
	v_mul_f32_e32 v139, v192, v193
	v_mul_f32_e32 v142, v142, v135
	v_cndmask_b32_e64 v131, v130, v185, s[12:13]
	v_fma_f32 v192, v140, v134, v136
	v_mov_b32_e32 v134, v44
	v_mov_b32_e32 v135, v144
	v_mov_b32_e32 v130, v132
	v_pk_mul_f32 v[130:131], v[134:135], v[130:131]
	v_mov_b32_e32 v161, v171
	v_add_f32_e32 v130, v130, v192
	v_add_f32_e32 v192, v130, v131
	v_mov_b32_dpp v161, v28 row_ror:1 row_mask:0xf bank_mask:0xf
	v_mov_b32_e32 v189, v171
	v_mul_f32_e32 v130, 0xbfb8aa3b, v192
	v_exp_f32_e32 v193, v130
	v_mov_b32_dpp v189, v12 row_ror:15 row_mask:0xf bank_mask:0xf
	v_cndmask_b32_e64 v130, v161, v149, s[14:15]
	v_cndmask_b32_e64 v131, v185, v189, s[12:13]
	v_fma_f32 v149, v140, v130, v136
	v_mov_b32_e32 v134, v28
	v_mov_b32_e32 v130, v132
	v_pk_mul_f32 v[130:131], v[134:135], v[130:131]
	v_mov_b32_e32 v188, v171
	v_add_f32_e32 v130, v130, v149
	v_add_f32_e32 v149, v130, v131
	v_mul_f32_e32 v130, 0xbfb8aa3b, v149
	v_exp_f32_e32 v130, v130
	v_mov_b32_dpp v188, v12 row_ror:1 row_mask:0xf bank_mask:0xf
	v_mov_b32_e32 v191, v171
	v_add_f32_e32 v131, 1.0, v193
	v_add_f32_e32 v193, 1.0, v130
	v_mov_b32_dpp v191, v4 row_ror:15 row_mask:0xf bank_mask:0xf
	v_cndmask_b32_e64 v130, v188, v161, s[14:15]
	v_rcp_f32_e32 v185, v131
	v_cndmask_b32_e64 v131, v189, v191, s[12:13]
	v_fma_f32 v161, v140, v130, v136
	v_mov_b32_e32 v134, v12
	v_mov_b32_e32 v130, v132
	v_pk_mul_f32 v[130:131], v[134:135], v[130:131]
	v_mov_b32_e32 v190, v171
	v_add_f32_e32 v130, v130, v161
	v_add_f32_e32 v161, v130, v131
	v_mov_b32_dpp v190, v4 row_ror:1 row_mask:0xf bank_mask:0xf
	v_mul_f32_e32 v130, 0xbfb8aa3b, v161
	v_cndmask_b32_e64 v131, v190, v188, s[14:15]
	v_exp_f32_e32 v189, v130
	v_cndmask_b32_e64 v130, v191, 0, s[12:13]
	v_fma_f32 v136, v140, v131, v136
	v_mov_b32_e32 v134, v144
	v_mov_b32_e32 v135, v4
	v_mov_b32_e32 v131, v132
	v_pk_mul_f32 v[130:131], v[134:135], v[130:131]
	v_rcp_f32_e32 v132, v193
	v_add_f32_e32 v131, v131, v136
	v_add_f32_e32 v130, v130, v131
	v_mul_f32_e32 v131, 0xbfb8aa3b, v130
	v_exp_f32_e32 v131, v131
	v_add_f32_e32 v134, 1.0, v189
	v_rcp_f32_e32 v134, v134
	v_mul_f32_e32 v136, v149, v132
	v_add_f32_e32 v131, 1.0, v131
	v_rcp_f32_e32 v131, v131
	v_mov_b32_e32 v132, v171
	v_mul_f32_e32 v134, v161, v134
	v_mov_b32_e32 v161, v171
	v_mul_f32_e32 v140, v130, v131
	v_mov_b32_dpp v132, v45 row_ror:1 row_mask:0xf bank_mask:0xf
	v_mov_b32_e32 v130, v171
	v_mov_b32_dpp v161, v29 row_ror:15 row_mask:0xf bank_mask:0xf
	v_cndmask_b32_e64 v144, v132, 0, s[14:15]
	v_mov_b32_dpp v130, v45 row_ror:15 row_mask:0xf bank_mask:0xf
	v_cndmask_b32_e64 v131, v130, v161, s[12:13]
	v_fma_f32 v191, v141, v144, v137
	v_mov_b32_e32 v144, v45
	v_mov_b32_e32 v130, v133
	v_pk_mul_f32 v[130:131], v[144:145], v[130:131]
	v_mov_b32_e32 v149, v171
	v_add_f32_e32 v130, v130, v191
	v_add_f32_e32 v191, v130, v131
	v_mov_b32_dpp v149, v29 row_ror:1 row_mask:0xf bank_mask:0xf
	v_mov_b32_e32 v188, v171
	v_mul_f32_e32 v130, 0xbfb8aa3b, v191
	v_mul_f32_e32 v135, v192, v185
	v_mov_b32_dpp v188, v13 row_ror:15 row_mask:0xf bank_mask:0xf
	v_exp_f32_e32 v192, v130
	v_cndmask_b32_e64 v130, v149, v132, s[14:15]
	v_cndmask_b32_e64 v131, v161, v188, s[12:13]
	v_fma_f32 v132, v141, v130, v137
	v_mov_b32_e32 v144, v29
	v_mov_b32_e32 v130, v133
	v_pk_mul_f32 v[130:131], v[144:145], v[130:131]
	v_mov_b32_e32 v185, v171
	v_add_f32_e32 v130, v130, v132
	v_add_f32_e32 v161, v130, v131
	v_mul_f32_e32 v130, 0xbfb8aa3b, v161
	v_exp_f32_e32 v130, v130
	v_mov_b32_dpp v185, v13 row_ror:1 row_mask:0xf bank_mask:0xf
	v_mov_b32_e32 v190, v171
	v_add_f32_e32 v131, 1.0, v192
	v_add_f32_e32 v193, 1.0, v130
	v_mov_b32_dpp v190, v5 row_ror:15 row_mask:0xf bank_mask:0xf
	v_cndmask_b32_e64 v130, v185, v149, s[14:15]
	v_rcp_f32_e32 v192, v131
	v_cndmask_b32_e64 v131, v188, v190, s[12:13]
	v_fma_f32 v132, v141, v130, v137
	v_mov_b32_e32 v144, v13
	v_mov_b32_e32 v130, v133
	v_pk_mul_f32 v[130:131], v[144:145], v[130:131]
	v_mov_b32_e32 v189, v171
	v_add_f32_e32 v130, v130, v132
	v_add_f32_e32 v144, v130, v131
	v_mov_b32_dpp v189, v5 row_ror:1 row_mask:0xf bank_mask:0xf
	v_mul_f32_e32 v130, 0xbfb8aa3b, v144
	v_exp_f32_e32 v149, v130
	v_cndmask_b32_e64 v130, v189, v185, s[14:15]
	v_cndmask_b32_e64 v132, v190, 0, s[12:13]
	v_fmac_f32_e32 v137, v141, v130
	v_mov_b32_e32 v130, v145
	v_mov_b32_e32 v131, v5
	v_pk_mul_f32 v[130:131], v[130:131], v[132:133]
	v_add_f32_e32 v133, 1.0, v149
	v_add_f32_e32 v131, v131, v137
	v_add_f32_e32 v130, v130, v131
	v_mul_f32_e32 v131, 0xbfb8aa3b, v130
	v_exp_f32_e32 v131, v131
	v_rcp_f32_e32 v132, v193
	v_rcp_f32_e32 v133, v133
	v_mul_f32_e32 v137, v191, v192
	v_add_f32_e32 v131, 1.0, v131
	v_rcp_f32_e32 v131, v131
	v_mul_f32_e32 v141, v161, v132
	v_mul_f32_e32 v144, v144, v133
	v_mul_f32_e32 v145, v130, v131
	v_cvt_pk_bf16_f32 v130, v177, v155
	v_cvt_pk_bf16_f32 v131, v182, v157
	v_cvt_pk_bf16_f32 v132, v152, v139
	v_cvt_pk_bf16_f32 v133, v135, v137
	global_store_dwordx4 v[200:201], v[130:133], off offset:256 nt
	s_nop 1
	v_cvt_pk_bf16_f32 v130, v170, v154
	v_cvt_pk_bf16_f32 v131, v179, v159
	v_cvt_pk_bf16_f32 v132, v138, v143
	v_cvt_pk_bf16_f32 v133, v136, v141
	global_store_dwordx4 v[202:203], v[130:133], off offset:256 nt
	s_nop 1
	v_cvt_pk_bf16_f32 v130, v150, v151
	v_cvt_pk_bf16_f32 v131, v183, v156
	v_cvt_pk_bf16_f32 v132, v153, v142
	v_cvt_pk_bf16_f32 v133, v134, v144
	global_store_dwordx4 v[204:205], v[130:133], off offset:256 nt
	s_nop 1
	v_cvt_pk_bf16_f32 v130, v146, v147
	v_cvt_pk_bf16_f32 v131, v184, v158
	v_cvt_pk_bf16_f32 v132, v160, v148
	v_cvt_pk_bf16_f32 v133, v140, v145
	global_store_dwordx4 v[206:207], v[130:133], off offset:256 nt
; __device__ __forceinline__ unsigned cvt_pk_bf16(float lo, float hi) { unsigned r; asm volatile("v_cvt_pk_bf16_f32 %0, %1, %2" : "=v"(r) : "v"(lo), "v"(hi)); return r; }
;     __device__ __forceinline__ void operator()(const f32x4 (&acc)[2][2][4][2], const pg8::Unit& u, int wr, int wc, int fr, int fq_in) const {
;     ...
;             if (u.pm >= 64) {
; #pragma unroll
;                 for (int ai = 0; ai < 2; ++ai)
; #pragma unroll
;                     for (int m = 0; m < 4; ++m) { bf16* rowp = XBCR + (size_t)(row0 - M + ai * 128 + m * 16) * XBCW + col0;
; #pragma unroll
;                         for (int bj = 0; bj < 2; ++bj) { const f32x4 v0 = acc[ai][bj][m][0], v1 = acc[ai][bj][m][1];
;                             u32x4 w; w.x = pg8::cvt_pk_bf16(v0[0], v0[1]); w.y = pg8::cvt_pk_bf16(v0[2], v0[3]); w.z = pg8::cvt_pk_bf16(v1[0], v1[1]); w.w = pg8::cvt_pk_bf16(v1[2], v1[3]);
;                             *(u32x4*)(rowp + bj * 128) = w; } }
.LBB0_480:
	s_andn2_b64 vcc, exec, s[0:1]
	s_cbranch_vccnz .LBB0_482
	v_add_u32_e32 v132, 0xffffc000, v178
	v_mov_b64_e32 v[130:131], s[30:31]
	v_mad_i64_i32 v[134:135], s[0:1], v132, s93, v[130:131]
	v_lshlrev_b64 v[132:133], 1, v[180:181]
	v_lshl_add_u64 v[134:135], v[134:135], 0, v[132:133]
	v_cvt_pk_bf16_f32 v126, v126, v127
	v_cvt_pk_bf16_f32 v127, v128, v129
	v_cvt_pk_bf16_f32 v128, v122, v123
	v_cvt_pk_bf16_f32 v129, v124, v125
	global_store_dwordx4 v[134:135], v[126:129], off nt
	v_cvt_pk_bf16_f32 v114, v114, v115
	v_cvt_pk_bf16_f32 v115, v116, v117
	v_cvt_pk_bf16_f32 v116, v106, v107
	v_add_u32_e32 v106, 0xffffc010, v178
	v_mad_i64_i32 v[106:107], s[0:1], v106, s93, v[130:131]
	v_cvt_pk_bf16_f32 v117, v108, v109
	global_store_dwordx4 v[134:135], v[114:117], off offset:256 nt
	s_nop 1
	v_lshl_add_u64 v[114:115], v[106:107], 0, v[132:133]
	v_cvt_pk_bf16_f32 v106, v118, v119
	v_cvt_pk_bf16_f32 v107, v120, v121
	v_cvt_pk_bf16_f32 v108, v110, v111
	v_cvt_pk_bf16_f32 v109, v112, v113
	global_store_dwordx4 v[114:115], v[106:109], off nt
	v_cvt_pk_bf16_f32 v98, v98, v99
	v_cvt_pk_bf16_f32 v99, v100, v101
	v_cvt_pk_bf16_f32 v100, v90, v91
	v_add_u32_e32 v90, 0xffffc020, v178
	v_mad_i64_i32 v[90:91], s[0:1], v90, s93, v[130:131]
	v_cvt_pk_bf16_f32 v101, v92, v93
	global_store_dwordx4 v[114:115], v[98:101], off offset:256 nt
	s_nop 1
	v_lshl_add_u64 v[98:99], v[90:91], 0, v[132:133]
	v_cvt_pk_bf16_f32 v90, v102, v103
	v_cvt_pk_bf16_f32 v91, v104, v105
	v_cvt_pk_bf16_f32 v92, v94, v95
	v_cvt_pk_bf16_f32 v93, v96, v97
	global_store_dwordx4 v[98:99], v[90:93], off nt
	v_cvt_pk_bf16_f32 v82, v82, v83
	v_cvt_pk_bf16_f32 v83, v84, v85
	v_cvt_pk_bf16_f32 v84, v74, v75
	v_add_u32_e32 v74, 0xffffc030, v178
	v_mad_i64_i32 v[74:75], s[0:1], v74, s93, v[130:131]
	v_cvt_pk_bf16_f32 v85, v76, v77
	global_store_dwordx4 v[98:99], v[82:85], off offset:256 nt
	s_nop 1
	v_lshl_add_u64 v[82:83], v[74:75], 0, v[132:133]
	v_cvt_pk_bf16_f32 v74, v86, v87
	v_cvt_pk_bf16_f32 v75, v88, v89
	v_cvt_pk_bf16_f32 v76, v78, v79
	v_cvt_pk_bf16_f32 v77, v80, v81
	global_store_dwordx4 v[82:83], v[74:77], off nt
	v_cvt_pk_bf16_f32 v70, v70, v71
	v_cvt_pk_bf16_f32 v71, v72, v73
	v_cvt_pk_bf16_f32 v72, v66, v67
	v_add_u32_e32 v66, 0xffffc080, v178
	v_mad_i64_i32 v[66:67], s[0:1], v66, s93, v[130:131]
	v_lshl_add_u64 v[66:67], v[66:67], 0, v[132:133]
	v_cvt_pk_bf16_f32 v73, v68, v69
	global_store_dwordx4 v[82:83], v[70:73], off offset:256 nt
	v_cvt_pk_bf16_f32 v62, v62, v63
	v_cvt_pk_bf16_f32 v63, v64, v65
	v_cvt_pk_bf16_f32 v64, v58, v59
	v_cvt_pk_bf16_f32 v65, v60, v61
	global_store_dwordx4 v[66:67], v[62:65], off nt
	v_cvt_pk_bf16_f32 v50, v50, v51
	v_cvt_pk_bf16_f32 v51, v52, v53
	v_cvt_pk_bf16_f32 v52, v42, v43
	v_add_u32_e32 v42, 0xffffc090, v178
	v_mad_i64_i32 v[42:43], s[0:1], v42, s93, v[130:131]
	v_cvt_pk_bf16_f32 v53, v44, v45
	global_store_dwordx4 v[66:67], v[50:53], off offset:256 nt
	s_nop 1
	v_lshl_add_u64 v[50:51], v[42:43], 0, v[132:133]
	v_cvt_pk_bf16_f32 v42, v54, v55
	v_cvt_pk_bf16_f32 v43, v56, v57
	v_cvt_pk_bf16_f32 v44, v46, v47
	v_cvt_pk_bf16_f32 v45, v48, v49
	global_store_dwordx4 v[50:51], v[42:45], off nt
	v_cvt_pk_bf16_f32 v34, v34, v35
	v_cvt_pk_bf16_f32 v35, v36, v37
	v_cvt_pk_bf16_f32 v36, v26, v27
	v_add_u32_e32 v26, 0xffffc0a0, v178
	v_mad_i64_i32 v[26:27], s[0:1], v26, s93, v[130:131]
	v_cvt_pk_bf16_f32 v37, v28, v29
	global_store_dwordx4 v[50:51], v[34:37], off offset:256 nt
	s_nop 1
	v_lshl_add_u64 v[34:35], v[26:27], 0, v[132:133]
	v_cvt_pk_bf16_f32 v26, v38, v39
	v_cvt_pk_bf16_f32 v27, v40, v41
	v_cvt_pk_bf16_f32 v28, v30, v31
	v_cvt_pk_bf16_f32 v29, v32, v33
	global_store_dwordx4 v[34:35], v[26:29], off nt
	v_cvt_pk_bf16_f32 v18, v18, v19
	v_cvt_pk_bf16_f32 v19, v20, v21
	v_cvt_pk_bf16_f32 v20, v10, v11
	v_add_u32_e32 v10, 0xffffc0b0, v178
	v_mad_i64_i32 v[10:11], s[0:1], v10, s93, v[130:131]
	v_cvt_pk_bf16_f32 v21, v12, v13
	global_store_dwordx4 v[34:35], v[18:21], off offset:256 nt
	s_nop 1
	v_lshl_add_u64 v[18:19], v[10:11], 0, v[132:133]
	v_cvt_pk_bf16_f32 v10, v22, v23
	v_cvt_pk_bf16_f32 v11, v24, v25
	v_cvt_pk_bf16_f32 v12, v14, v15
	v_cvt_pk_bf16_f32 v13, v16, v17
	global_store_dwordx4 v[18:19], v[10:13], off nt
	v_cvt_pk_bf16_f32 v6, v6, v7
	v_cvt_pk_bf16_f32 v7, v8, v9
	v_cvt_pk_bf16_f32 v8, v2, v3
	v_cvt_pk_bf16_f32 v9, v4, v5
	global_store_dwordx4 v[18:19], v[6:9], off offset:256 nt
